# adds nt cache policy on read-once / write-once streams: x loads (P0), expert-weight f32 loads + fp8 stores (P5 conversion), H bf16 stores (P8), out stores (P12)
# speedup vs baseline: 1.0080x; 1.0080x over previous
; #define GAS __attribute__((address_space(1)))
; #define LAS __attribute__((address_space(3)))
; __device__ __forceinline__ unsigned pk2(float lo, float hi) { return cvt_pk_bf16_nat(lo, hi); }
; __global__ void __launch_bounds__(NTHR, 2) mk_fwd(Args args) {
;     ...
;     if (IN(0)) {
;         LAS float* scr = (LAS float*)(lds + wave * 16640);
;         for (size_t i = (size_t)gw * 64 + lane; i < (size_t)M * D / 8; i += (size_t)NGW * 64) {
;             const f32x4 a = *(const GAS f32x4*)(x + i * 8), b = *(const GAS f32x4*)(x + i * 8 + 4);
;             v4u o; o.x = pk2(a.x, a.y); o.y = pk2(a.z, a.w); o.z = pk2(b.x, b.y); o.w = pk2(b.z, b.w);
;             *(GAS v4u*)(XB + i * 8) = o;
;         }
.LBB0_9:
	s_or_b64 exec, exec, s[0:1]
	s_ashr_i32 s19, s18, 31
	s_lshr_b32 s0, s19, 29
	s_add_i32 s0, s18, s0
	s_ashr_i32 s1, s0, 3
	s_and_b32 s0, s0, -8
	s_ashr_i32 s74, s33, 31
	v_writelane_b32 v252, s0, 37
	s_sub_i32 s2, s18, s0
	s_lshr_b32 s0, s74, 29
	s_add_i32 s0, s33, s0
	s_ashr_i32 s0, s0, 3
	v_writelane_b32 v252, s2, 38
	s_mul_i32 s0, s0, s2
	v_writelane_b32 v252, s1, 39
	v_writelane_b32 v252, s0, 40
	s_add_i32 s0, s0, s1
	v_writelane_b32 v252, s0, 41
	s_lshl_b32 s0, s0, 3
	s_lshr_b32 s1, s12, 6
	s_add_i32 s30, s0, s1
	s_lshl_b32 s28, s33, 3
	v_writelane_b32 v252, s12, 42
	s_add_u32 s0, s26, 0x4348000
	v_writelane_b32 v252, s1, 43
	s_addc_u32 s1, s27, 0
	s_cmp_lt_i32 s88, 1
	s_cselect_b64 s[2:3], -1, 0
	s_cmp_gt_i32 s89, 0
	s_cselect_b64 s[4:5], -1, 0
	s_and_b64 s[4:5], s[2:3], s[4:5]
	s_andn2_b64 vcc, exec, s[4:5]
	v_and_b32_e32 v194, 63, v0
	s_cbranch_vccnz .LBB0_29
	s_ashr_i32 s31, s30, 31
	s_lshl_b64 s[6:7], s[30:31], 6
	v_mov_b64_e32 v[2:3], 0x3fffff
	v_cmp_gt_u64_e32 vcc, s[6:7], v[2:3]
	v_mov_b32_e32 v5, 0
	v_or_b32_e32 v6, s6, v194
	v_mov_b32_e32 v7, s7
	s_mov_b64 s[2:3], 0x3fffff
	s_cbranch_vccnz .LBB0_14
	v_readlane_b32 s36, v252, 0
	v_readlane_b32 s37, v252, 1
	s_lshl_b32 s8, s30, 11
	v_lshlrev_b32_e32 v2, 5, v194
	v_add_u32_e32 v2, s8, v2
	s_lshl_b32 s9, s30, 10
	v_lshlrev_b32_e32 v3, 4, v194
	v_add_u32_e32 v3, s9, v3
	s_add_u32 s12, s26, 0x348000
	s_addc_u32 s13, s27, 0
	s_nop 3
	s_mov_b32 s10, s36
	s_mov_b32 s11, s37
	global_load_dwordx4 v[10:13], v2, s[10:11] nt
	global_load_dwordx4 v[14:17], v2, s[10:11] offset:16 nt
	s_add_u32 s10, s10, 0x400000
	s_addc_u32 s11, s11, 0
	global_load_dwordx4 v[18:21], v2, s[10:11] nt
	global_load_dwordx4 v[22:25], v2, s[10:11] offset:16 nt
	s_add_u32 s10, s10, 0x400000
	s_addc_u32 s11, s11, 0
	global_load_dwordx4 v[26:29], v2, s[10:11] nt
	global_load_dwordx4 v[30:33], v2, s[10:11] offset:16 nt
	s_add_u32 s10, s10, 0x400000
	s_addc_u32 s11, s11, 0
	global_load_dwordx4 v[34:37], v2, s[10:11] nt
	global_load_dwordx4 v[38:41], v2, s[10:11] offset:16 nt
	s_add_u32 s10, s10, 0x400000
	s_addc_u32 s11, s11, 0
	global_load_dwordx4 v[42:45], v2, s[10:11] nt
	global_load_dwordx4 v[46:49], v2, s[10:11] offset:16 nt
	s_add_u32 s10, s10, 0x400000
	s_addc_u32 s11, s11, 0
	global_load_dwordx4 v[50:53], v2, s[10:11] nt
	global_load_dwordx4 v[54:57], v2, s[10:11] offset:16 nt
	s_add_u32 s10, s10, 0x400000
	s_addc_u32 s11, s11, 0
	global_load_dwordx4 v[58:61], v2, s[10:11] nt
	global_load_dwordx4 v[62:65], v2, s[10:11] offset:16 nt
	s_add_u32 s10, s10, 0x400000
	s_addc_u32 s11, s11, 0
	global_load_dwordx4 v[66:69], v2, s[10:11] nt
	global_load_dwordx4 v[70:73], v2, s[10:11] offset:16 nt
	s_add_u32 s10, s10, 0x400000
	s_addc_u32 s11, s11, 0
	s_waitcnt vmcnt(14)
	v_cvt_pk_bf16_f32 v10, v10, v11
	v_cvt_pk_bf16_f32 v11, v12, v13
	v_cvt_pk_bf16_f32 v12, v14, v15
	v_cvt_pk_bf16_f32 v13, v16, v17
	global_store_dwordx4 v3, v[10:13], s[12:13]
	s_add_u32 s12, s12, 0x200000
	s_addc_u32 s13, s13, 0
	global_load_dwordx4 v[14:17], v2, s[10:11] offset:16 nt
	global_load_dwordx4 v[10:13], v2, s[10:11] nt
	s_add_u32 s10, s10, 0x400000
	s_addc_u32 s11, s11, 0
	s_waitcnt vmcnt(15)
	v_cvt_pk_bf16_f32 v18, v18, v19
	v_cvt_pk_bf16_f32 v19, v20, v21
	v_cvt_pk_bf16_f32 v20, v22, v23
	v_cvt_pk_bf16_f32 v21, v24, v25
	global_store_dwordx4 v3, v[18:21], s[12:13]
	s_add_u32 s12, s12, 0x200000
	s_addc_u32 s13, s13, 0
	global_load_dwordx4 v[22:25], v2, s[10:11] offset:16 nt
	global_load_dwordx4 v[18:21], v2, s[10:11] nt
	s_add_u32 s10, s10, 0x400000
	s_addc_u32 s11, s11, 0
	s_waitcnt vmcnt(16)
	v_cvt_pk_bf16_f32 v26, v26, v27
	v_cvt_pk_bf16_f32 v27, v28, v29
	v_cvt_pk_bf16_f32 v28, v30, v31
	v_cvt_pk_bf16_f32 v29, v32, v33
	global_store_dwordx4 v3, v[26:29], s[12:13]
	s_add_u32 s12, s12, 0x200000
	s_addc_u32 s13, s13, 0
	global_load_dwordx4 v[30:33], v2, s[10:11] offset:16 nt
	global_load_dwordx4 v[26:29], v2, s[10:11] nt
	s_add_u32 s10, s10, 0x400000
	s_addc_u32 s11, s11, 0
	s_waitcnt vmcnt(17)
	v_cvt_pk_bf16_f32 v34, v34, v35
	v_cvt_pk_bf16_f32 v35, v36, v37
	v_cvt_pk_bf16_f32 v36, v38, v39
	v_cvt_pk_bf16_f32 v37, v40, v41
	global_store_dwordx4 v3, v[34:37], s[12:13]
	s_add_u32 s12, s12, 0x200000
	s_addc_u32 s13, s13, 0
	global_load_dwordx4 v[38:41], v2, s[10:11] offset:16 nt
	global_load_dwordx4 v[34:37], v2, s[10:11] nt
	s_add_u32 s10, s10, 0x400000
	s_addc_u32 s11, s11, 0
	s_waitcnt vmcnt(18)
	v_cvt_pk_bf16_f32 v42, v42, v43
	v_cvt_pk_bf16_f32 v43, v44, v45
	v_cvt_pk_bf16_f32 v44, v46, v47
	v_cvt_pk_bf16_f32 v45, v48, v49
	global_store_dwordx4 v3, v[42:45], s[12:13]
	s_add_u32 s12, s12, 0x200000
	s_addc_u32 s13, s13, 0
	global_load_dwordx4 v[46:49], v2, s[10:11] offset:16 nt
	global_load_dwordx4 v[42:45], v2, s[10:11] nt
	s_add_u32 s10, s10, 0x400000
	s_addc_u32 s11, s11, 0
	s_waitcnt vmcnt(19)
	v_cvt_pk_bf16_f32 v50, v50, v51
	v_cvt_pk_bf16_f32 v51, v52, v53
	v_cvt_pk_bf16_f32 v52, v54, v55
	v_cvt_pk_bf16_f32 v53, v56, v57
	global_store_dwordx4 v3, v[50:53], s[12:13]
	s_add_u32 s12, s12, 0x200000
	s_addc_u32 s13, s13, 0
	global_load_dwordx4 v[54:57], v2, s[10:11] offset:16 nt
	global_load_dwordx4 v[50:53], v2, s[10:11] nt
	s_add_u32 s10, s10, 0x400000
	s_addc_u32 s11, s11, 0
	s_waitcnt vmcnt(20)
	v_cvt_pk_bf16_f32 v58, v58, v59
	v_cvt_pk_bf16_f32 v59, v60, v61
	v_cvt_pk_bf16_f32 v60, v62, v63
	v_cvt_pk_bf16_f32 v61, v64, v65
	global_store_dwordx4 v3, v[58:61], s[12:13]
	s_add_u32 s12, s12, 0x200000
	s_addc_u32 s13, s13, 0
	global_load_dwordx4 v[62:65], v2, s[10:11] offset:16 nt
	global_load_dwordx4 v[58:61], v2, s[10:11] nt
	s_add_u32 s10, s10, 0x400000
	s_addc_u32 s11, s11, 0
	s_waitcnt vmcnt(21)
; #define GAS __attribute__((address_space(1)))
; __device__ __forceinline__ unsigned pk2(float lo, float hi) { return cvt_pk_bf16_nat(lo, hi); }
; __global__ void __launch_bounds__(NTHR, 2) mk_fwd(Args args) {
;     ...
;         for (size_t i = (size_t)gw * 64 + lane; i < (size_t)M * D / 8; i += (size_t)NGW * 64) {
;             const f32x4 a = *(const GAS f32x4*)(x + i * 8), b = *(const GAS f32x4*)(x + i * 8 + 4);
;             v4u o; o.x = pk2(a.x, a.y); o.y = pk2(a.z, a.w); o.z = pk2(b.x, b.y); o.w = pk2(b.z, b.w);
;             *(GAS v4u*)(XB + i * 8) = o;
;         }
	v_cvt_pk_bf16_f32 v66, v66, v67
	v_cvt_pk_bf16_f32 v67, v68, v69
	v_cvt_pk_bf16_f32 v68, v70, v71
	v_cvt_pk_bf16_f32 v69, v72, v73
	global_store_dwordx4 v3, v[66:69], s[12:13]
	s_add_u32 s12, s12, 0x200000
	s_addc_u32 s13, s13, 0
	global_load_dwordx4 v[70:73], v2, s[10:11] offset:16 nt
	global_load_dwordx4 v[66:69], v2, s[10:11] nt
	s_add_u32 s10, s10, 0x400000
	s_addc_u32 s11, s11, 0
	s_waitcnt vmcnt(21)
	v_cvt_pk_bf16_f32 v10, v10, v11
	v_cvt_pk_bf16_f32 v11, v12, v13
	v_cvt_pk_bf16_f32 v12, v14, v15
	v_cvt_pk_bf16_f32 v13, v16, v17
	global_store_dwordx4 v3, v[10:13], s[12:13]
	s_add_u32 s12, s12, 0x200000
	s_addc_u32 s13, s13, 0
	global_load_dwordx4 v[14:17], v2, s[10:11] offset:16 nt
	global_load_dwordx4 v[10:13], v2, s[10:11] nt
	s_add_u32 s10, s10, 0x400000
	s_addc_u32 s11, s11, 0
	s_waitcnt vmcnt(21)
	v_cvt_pk_bf16_f32 v18, v18, v19
	v_cvt_pk_bf16_f32 v19, v20, v21
	v_cvt_pk_bf16_f32 v20, v22, v23
	v_cvt_pk_bf16_f32 v21, v24, v25
	global_store_dwordx4 v3, v[18:21], s[12:13]
	s_add_u32 s12, s12, 0x200000
	s_addc_u32 s13, s13, 0
	global_load_dwordx4 v[22:25], v2, s[10:11] offset:16 nt
	global_load_dwordx4 v[18:21], v2, s[10:11] nt
	s_add_u32 s10, s10, 0x400000
	s_addc_u32 s11, s11, 0
	s_waitcnt vmcnt(21)
	v_cvt_pk_bf16_f32 v26, v26, v27
	v_cvt_pk_bf16_f32 v27, v28, v29
	v_cvt_pk_bf16_f32 v28, v30, v31
	v_cvt_pk_bf16_f32 v29, v32, v33
	global_store_dwordx4 v3, v[26:29], s[12:13]
	s_add_u32 s12, s12, 0x200000
	s_addc_u32 s13, s13, 0
	global_load_dwordx4 v[30:33], v2, s[10:11] offset:16 nt
	global_load_dwordx4 v[26:29], v2, s[10:11] nt
	s_add_u32 s10, s10, 0x400000
	s_addc_u32 s11, s11, 0
	s_waitcnt vmcnt(21)
	v_cvt_pk_bf16_f32 v34, v34, v35
	v_cvt_pk_bf16_f32 v35, v36, v37
	v_cvt_pk_bf16_f32 v36, v38, v39
	v_cvt_pk_bf16_f32 v37, v40, v41
	global_store_dwordx4 v3, v[34:37], s[12:13]
	s_add_u32 s12, s12, 0x200000
	s_addc_u32 s13, s13, 0
	global_load_dwordx4 v[38:41], v2, s[10:11] offset:16 nt
	global_load_dwordx4 v[34:37], v2, s[10:11] nt
	s_add_u32 s10, s10, 0x400000
	s_addc_u32 s11, s11, 0
	s_waitcnt vmcnt(21)
	v_cvt_pk_bf16_f32 v42, v42, v43
	v_cvt_pk_bf16_f32 v43, v44, v45
	v_cvt_pk_bf16_f32 v44, v46, v47
	v_cvt_pk_bf16_f32 v45, v48, v49
	global_store_dwordx4 v3, v[42:45], s[12:13]
	s_add_u32 s12, s12, 0x200000
	s_addc_u32 s13, s13, 0
	global_load_dwordx4 v[46:49], v2, s[10:11] offset:16 nt
	global_load_dwordx4 v[42:45], v2, s[10:11] nt
	s_add_u32 s10, s10, 0x400000
	s_addc_u32 s11, s11, 0
	s_waitcnt vmcnt(21)
	v_cvt_pk_bf16_f32 v50, v50, v51
	v_cvt_pk_bf16_f32 v51, v52, v53
	v_cvt_pk_bf16_f32 v52, v54, v55
	v_cvt_pk_bf16_f32 v53, v56, v57
	global_store_dwordx4 v3, v[50:53], s[12:13]
	s_add_u32 s12, s12, 0x200000
	s_addc_u32 s13, s13, 0
	global_load_dwordx4 v[54:57], v2, s[10:11] offset:16 nt
	global_load_dwordx4 v[50:53], v2, s[10:11] nt
	s_add_u32 s10, s10, 0x400000
	s_addc_u32 s11, s11, 0
	s_waitcnt vmcnt(21)
	v_cvt_pk_bf16_f32 v58, v58, v59
	v_cvt_pk_bf16_f32 v59, v60, v61
	v_cvt_pk_bf16_f32 v60, v62, v63
	v_cvt_pk_bf16_f32 v61, v64, v65
	global_store_dwordx4 v3, v[58:61], s[12:13]
	s_add_u32 s12, s12, 0x200000
	s_addc_u32 s13, s13, 0
	global_load_dwordx4 v[62:65], v2, s[10:11] offset:16 nt
	global_load_dwordx4 v[58:61], v2, s[10:11] nt
	s_add_u32 s10, s10, 0x400000
	s_addc_u32 s11, s11, 0
	s_waitcnt vmcnt(21)
	v_cvt_pk_bf16_f32 v66, v66, v67
	v_cvt_pk_bf16_f32 v67, v68, v69
	v_cvt_pk_bf16_f32 v68, v70, v71
	v_cvt_pk_bf16_f32 v69, v72, v73
	global_store_dwordx4 v3, v[66:69], s[12:13]
	s_add_u32 s12, s12, 0x200000
	s_addc_u32 s13, s13, 0
	global_load_dwordx4 v[70:73], v2, s[10:11] offset:16 nt
	global_load_dwordx4 v[66:69], v2, s[10:11] nt
	s_add_u32 s10, s10, 0x400000
	s_addc_u32 s11, s11, 0
	s_waitcnt vmcnt(21)
	v_cvt_pk_bf16_f32 v10, v10, v11
	v_cvt_pk_bf16_f32 v11, v12, v13
	v_cvt_pk_bf16_f32 v12, v14, v15
	v_cvt_pk_bf16_f32 v13, v16, v17
	global_store_dwordx4 v3, v[10:13], s[12:13]
	s_add_u32 s12, s12, 0x200000
	s_addc_u32 s13, s13, 0
	global_load_dwordx4 v[14:17], v2, s[10:11] offset:16 nt
	global_load_dwordx4 v[10:13], v2, s[10:11] nt
	s_add_u32 s10, s10, 0x400000
	s_addc_u32 s11, s11, 0
	s_waitcnt vmcnt(21)
	v_cvt_pk_bf16_f32 v18, v18, v19
	v_cvt_pk_bf16_f32 v19, v20, v21
	v_cvt_pk_bf16_f32 v20, v22, v23
	v_cvt_pk_bf16_f32 v21, v24, v25
	global_store_dwordx4 v3, v[18:21], s[12:13]
	s_add_u32 s12, s12, 0x200000
	s_addc_u32 s13, s13, 0
	global_load_dwordx4 v[22:25], v2, s[10:11] offset:16 nt
	global_load_dwordx4 v[18:21], v2, s[10:11] nt
	s_add_u32 s10, s10, 0x400000
	s_addc_u32 s11, s11, 0
	s_waitcnt vmcnt(21)
; #define GAS __attribute__((address_space(1)))
; __device__ __forceinline__ unsigned pk2(float lo, float hi) { return cvt_pk_bf16_nat(lo, hi); }
; __global__ void __launch_bounds__(NTHR, 2) mk_fwd(Args args) {
;     ...
;         for (size_t i = (size_t)gw * 64 + lane; i < (size_t)M * D / 8; i += (size_t)NGW * 64) {
;             const f32x4 a = *(const GAS f32x4*)(x + i * 8), b = *(const GAS f32x4*)(x + i * 8 + 4);
;             v4u o; o.x = pk2(a.x, a.y); o.y = pk2(a.z, a.w); o.z = pk2(b.x, b.y); o.w = pk2(b.z, b.w);
;             *(GAS v4u*)(XB + i * 8) = o;
;         }
	v_cvt_pk_bf16_f32 v26, v26, v27
	v_cvt_pk_bf16_f32 v27, v28, v29
	v_cvt_pk_bf16_f32 v28, v30, v31
	v_cvt_pk_bf16_f32 v29, v32, v33
	global_store_dwordx4 v3, v[26:29], s[12:13]
	s_add_u32 s12, s12, 0x200000
	s_addc_u32 s13, s13, 0
	global_load_dwordx4 v[30:33], v2, s[10:11] offset:16 nt
	global_load_dwordx4 v[26:29], v2, s[10:11] nt
	s_add_u32 s10, s10, 0x400000
	s_addc_u32 s11, s11, 0
	s_waitcnt vmcnt(21)
	v_cvt_pk_bf16_f32 v34, v34, v35
	v_cvt_pk_bf16_f32 v35, v36, v37
	v_cvt_pk_bf16_f32 v36, v38, v39
	v_cvt_pk_bf16_f32 v37, v40, v41
	global_store_dwordx4 v3, v[34:37], s[12:13]
	s_add_u32 s12, s12, 0x200000
	s_addc_u32 s13, s13, 0
	global_load_dwordx4 v[38:41], v2, s[10:11] offset:16 nt
	global_load_dwordx4 v[34:37], v2, s[10:11] nt
	s_add_u32 s10, s10, 0x400000
	s_addc_u32 s11, s11, 0
	s_waitcnt vmcnt(21)
	v_cvt_pk_bf16_f32 v42, v42, v43
	v_cvt_pk_bf16_f32 v43, v44, v45
	v_cvt_pk_bf16_f32 v44, v46, v47
	v_cvt_pk_bf16_f32 v45, v48, v49
	global_store_dwordx4 v3, v[42:45], s[12:13]
	s_add_u32 s12, s12, 0x200000
	s_addc_u32 s13, s13, 0
	global_load_dwordx4 v[46:49], v2, s[10:11] offset:16 nt
	global_load_dwordx4 v[42:45], v2, s[10:11] nt
	s_add_u32 s10, s10, 0x400000
	s_addc_u32 s11, s11, 0
	s_waitcnt vmcnt(21)
	v_cvt_pk_bf16_f32 v50, v50, v51
	v_cvt_pk_bf16_f32 v51, v52, v53
	v_cvt_pk_bf16_f32 v52, v54, v55
	v_cvt_pk_bf16_f32 v53, v56, v57
	global_store_dwordx4 v3, v[50:53], s[12:13]
	s_add_u32 s12, s12, 0x200000
	s_addc_u32 s13, s13, 0
	global_load_dwordx4 v[54:57], v2, s[10:11] offset:16 nt
	global_load_dwordx4 v[50:53], v2, s[10:11] nt
	s_add_u32 s10, s10, 0x400000
	s_addc_u32 s11, s11, 0
	s_waitcnt vmcnt(21)
	v_cvt_pk_bf16_f32 v58, v58, v59
	v_cvt_pk_bf16_f32 v59, v60, v61
	v_cvt_pk_bf16_f32 v60, v62, v63
	v_cvt_pk_bf16_f32 v61, v64, v65
	global_store_dwordx4 v3, v[58:61], s[12:13]
	s_add_u32 s12, s12, 0x200000
	s_addc_u32 s13, s13, 0
	global_load_dwordx4 v[62:65], v2, s[10:11] offset:16 nt
	global_load_dwordx4 v[58:61], v2, s[10:11] nt
	s_add_u32 s10, s10, 0x400000
	s_addc_u32 s11, s11, 0
	s_waitcnt vmcnt(21)
	v_cvt_pk_bf16_f32 v66, v66, v67
	v_cvt_pk_bf16_f32 v67, v68, v69
	v_cvt_pk_bf16_f32 v68, v70, v71
	v_cvt_pk_bf16_f32 v69, v72, v73
	global_store_dwordx4 v3, v[66:69], s[12:13]
	s_add_u32 s12, s12, 0x200000
	s_addc_u32 s13, s13, 0
	global_load_dwordx4 v[70:73], v2, s[10:11] offset:16 nt
	global_load_dwordx4 v[66:69], v2, s[10:11] nt
	s_add_u32 s10, s10, 0x400000
	s_addc_u32 s11, s11, 0
	s_waitcnt vmcnt(21)
	v_cvt_pk_bf16_f32 v10, v10, v11
	v_cvt_pk_bf16_f32 v11, v12, v13
	v_cvt_pk_bf16_f32 v12, v14, v15
	v_cvt_pk_bf16_f32 v13, v16, v17
	global_store_dwordx4 v3, v[10:13], s[12:13]
	s_add_u32 s12, s12, 0x200000
	s_addc_u32 s13, s13, 0
	s_waitcnt vmcnt(19)
	v_cvt_pk_bf16_f32 v18, v18, v19
	v_cvt_pk_bf16_f32 v19, v20, v21
	v_cvt_pk_bf16_f32 v20, v22, v23
	v_cvt_pk_bf16_f32 v21, v24, v25
	global_store_dwordx4 v3, v[18:21], s[12:13]
	s_add_u32 s12, s12, 0x200000
	s_addc_u32 s13, s13, 0
	s_waitcnt vmcnt(17)
	v_cvt_pk_bf16_f32 v26, v26, v27
	v_cvt_pk_bf16_f32 v27, v28, v29
	v_cvt_pk_bf16_f32 v28, v30, v31
	v_cvt_pk_bf16_f32 v29, v32, v33
	global_store_dwordx4 v3, v[26:29], s[12:13]
	s_add_u32 s12, s12, 0x200000
	s_addc_u32 s13, s13, 0
	s_waitcnt vmcnt(15)
	v_cvt_pk_bf16_f32 v34, v34, v35
	v_cvt_pk_bf16_f32 v35, v36, v37
	v_cvt_pk_bf16_f32 v36, v38, v39
	v_cvt_pk_bf16_f32 v37, v40, v41
	global_store_dwordx4 v3, v[34:37], s[12:13]
	s_add_u32 s12, s12, 0x200000
	s_addc_u32 s13, s13, 0
	s_waitcnt vmcnt(13)
	v_cvt_pk_bf16_f32 v42, v42, v43
	v_cvt_pk_bf16_f32 v43, v44, v45
	v_cvt_pk_bf16_f32 v44, v46, v47
	v_cvt_pk_bf16_f32 v45, v48, v49
	global_store_dwordx4 v3, v[42:45], s[12:13]
	s_add_u32 s12, s12, 0x200000
	s_addc_u32 s13, s13, 0
	s_waitcnt vmcnt(11)
	v_cvt_pk_bf16_f32 v50, v50, v51
	v_cvt_pk_bf16_f32 v51, v52, v53
	v_cvt_pk_bf16_f32 v52, v54, v55
	v_cvt_pk_bf16_f32 v53, v56, v57
	global_store_dwordx4 v3, v[50:53], s[12:13]
	s_add_u32 s12, s12, 0x200000
	s_addc_u32 s13, s13, 0
	s_waitcnt vmcnt(9)
	v_cvt_pk_bf16_f32 v58, v58, v59
	v_cvt_pk_bf16_f32 v59, v60, v61
	v_cvt_pk_bf16_f32 v60, v62, v63
	v_cvt_pk_bf16_f32 v61, v64, v65
	global_store_dwordx4 v3, v[58:61], s[12:13]
	s_add_u32 s12, s12, 0x200000
	s_addc_u32 s13, s13, 0
	s_waitcnt vmcnt(7)
	v_cvt_pk_bf16_f32 v66, v66, v67
	v_cvt_pk_bf16_f32 v67, v68, v69
	v_cvt_pk_bf16_f32 v68, v70, v71
	v_cvt_pk_bf16_f32 v69, v72, v73
	global_store_dwordx4 v3, v[66:69], s[12:13]
	s_add_u32 s12, s12, 0x200000
	s_addc_u32 s13, s13, 0

; #define GAS __attribute__((address_space(1)))
; #define LAS __attribute__((address_space(3)))
; #define LDS_WAIT() asm volatile("s_waitcnt lgkmcnt(0)" ::: "memory")
; __device__ __forceinline__ void tr_flush(LAS unsigned* img, int K, int N, unsigned char* WT, size_t row_off, int fl, int lane) {
;     const int nblk = N / 64, kb = fl / nblk, nb = fl % nblk, k0 = 64 * NHB * kb, n0 = 64 * nb;
;     LDS_WAIT(); asm volatile("" ::: "memory");
;     constexpr int CPR = 4 * NHB, RPP = 64 / CPR;
;     const int c = lane % CPR;
; #pragma unroll 4
;     for (int p = 0; p < CPR; ++p) { const int n = lane / CPR + RPP * p;
;         const v4u o = *(const LAS v4u*)(img + n * (16 * NHB) + 4 * (c ^ ((n >> 2) & 7)));
;         *(GAS v4u*)(WT + (row_off + n0 + n) * (size_t)K + k0 + 16 * c) = o; }
;     LDS_WAIT(); asm volatile("" ::: "memory");
; }
.LBB0_551:
	s_add_i32 s9, s8, -3
	s_add_i32 s11, s8, -2
	s_add_i32 s35, s8, -1
	v_bitop3_b32 v8, s9, v213, 4 bitop3:0x6c
	v_bitop3_b32 v9, s11, v213, 5 bitop3:0x6c
	v_bitop3_b32 v10, s35, v213, 6 bitop3:0x6c
	v_lshl_add_u64 v[26:27], v[2:3], 0, v[198:199]
	v_bitop3_b32 v7, s8, v213, 7 bitop3:0x6c
	v_lshl_add_u32 v8, v8, 4, v6
	v_lshl_add_u32 v12, v9, 4, v6
	v_lshl_add_u32 v16, v10, 4, v6
	v_add_co_u32_e32 v28, vcc, s14, v26
	v_lshl_add_u32 v7, v7, 4, v6
	ds_read_b128 v[8:11], v8
	ds_read_b128 v[12:15], v12 offset:1024
	ds_read_b128 v[16:19], v16 offset:2048
	ds_read_b128 v[20:23], v7 offset:3072
	v_addc_co_u32_e32 v29, vcc, 0, v27, vcc
	v_add_co_u32_e32 v30, vcc, s15, v26
	s_add_i32 s8, s8, 4
	s_nop 0
	v_addc_co_u32_e32 v31, vcc, 0, v27, vcc
	v_lshl_add_u64 v[24:25], v[4:5], 0, v[198:199]
	v_lshl_add_u64 v[2:3], v[2:3], 0, s[4:5]
	v_lshl_add_u64 v[4:5], v[4:5], 0, s[4:5]
	s_cmp_lg_u32 s8, 19
	v_add_u32_e32 v6, 0x1000, v6
	v_add_co_u32_e32 v26, vcc, 0x68c0e000, v26
	s_nop 1
	v_addc_co_u32_e32 v27, vcc, 0, v27, vcc
	s_waitcnt lgkmcnt(3)
	global_store_dwordx4 v[24:25], v[8:11], off nt
	s_waitcnt lgkmcnt(2)
	global_store_dwordx4 v[28:29], v[12:15], off nt
	s_waitcnt lgkmcnt(1)
	global_store_dwordx4 v[30:31], v[16:19], off nt
	s_waitcnt lgkmcnt(0)
	global_store_dwordx4 v[26:27], v[20:23], off nt
	s_cbranch_scc1 .LBB0_551
	s_waitcnt lgkmcnt(0)
	s_mov_b64 s[8:9], 0

; #define GAS __attribute__((address_space(1)))
; #define LAS __attribute__((address_space(3)))
; #define LDS_WAIT() asm volatile("s_waitcnt lgkmcnt(0)" ::: "memory")
; __device__ __forceinline__ void tr_flush(LAS unsigned* img, int K, int N, unsigned char* WT, size_t row_off, int fl, int lane) {
;     const int nblk = N / 64, kb = fl / nblk, nb = fl % nblk, k0 = 64 * NHB * kb, n0 = 64 * nb;
;     LDS_WAIT(); asm volatile("" ::: "memory");
;     constexpr int CPR = 4 * NHB, RPP = 64 / CPR;
;     const int c = lane % CPR;
; #pragma unroll 4
;     for (int p = 0; p < CPR; ++p) { const int n = lane / CPR + RPP * p;
;         const v4u o = *(const LAS v4u*)(img + n * (16 * NHB) + 4 * (c ^ ((n >> 2) & 7)));
;         *(GAS v4u*)(WT + (row_off + n0 + n) * (size_t)K + k0 + 16 * c) = o; }
;     LDS_WAIT(); asm volatile("" ::: "memory");
; }
.LBB0_555:
	s_add_i32 s7, s6, -3
	s_add_i32 s10, s6, -2
	s_add_i32 s11, s6, -1
	v_bitop3_b32 v8, s7, v213, 4 bitop3:0x6c
	v_bitop3_b32 v9, s10, v213, 5 bitop3:0x6c
	v_bitop3_b32 v10, s11, v213, 6 bitop3:0x6c
	v_lshl_add_u64 v[26:27], v[2:3], 0, s[8:9]
	v_bitop3_b32 v7, s6, v213, 7 bitop3:0x6c
	v_lshl_add_u32 v8, v8, 4, v6
	v_lshl_add_u32 v12, v9, 4, v6
	v_lshl_add_u32 v16, v10, 4, v6
	v_add_co_u32_e32 v28, vcc, s16, v26
	v_lshl_add_u32 v7, v7, 4, v6
	ds_read_b128 v[8:11], v8
	ds_read_b128 v[12:15], v12 offset:1024
	ds_read_b128 v[16:19], v16 offset:2048
	ds_read_b128 v[20:23], v7 offset:3072
	v_addc_co_u32_e32 v29, vcc, 0, v27, vcc
	v_add_co_u32_e32 v30, vcc, s17, v26
	s_add_i32 s6, s6, 4
	s_nop 0
	v_addc_co_u32_e32 v31, vcc, 0, v27, vcc
	v_lshl_add_u64 v[24:25], v[4:5], 0, s[8:9]
	v_lshl_add_u64 v[2:3], v[2:3], 0, s[4:5]
	v_lshl_add_u64 v[4:5], v[4:5], 0, s[4:5]
	s_cmp_lg_u32 s6, 19
	v_add_u32_e32 v6, 0x1000, v6
	v_add_co_u32_e32 v26, vcc, 0x58c0e000, v26
	s_nop 1
	v_addc_co_u32_e32 v27, vcc, 0, v27, vcc
	s_waitcnt lgkmcnt(3)
	global_store_dwordx4 v[24:25], v[8:11], off nt
	s_waitcnt lgkmcnt(2)
	global_store_dwordx4 v[28:29], v[12:15], off nt
	s_waitcnt lgkmcnt(1)
	global_store_dwordx4 v[30:31], v[16:19], off nt
	s_waitcnt lgkmcnt(0)
	global_store_dwordx4 v[26:27], v[20:23], off nt
	s_cbranch_scc1 .LBB0_555
	s_waitcnt lgkmcnt(0)

; #define GAS __attribute__((address_space(1)))
; #define LAS __attribute__((address_space(3)))
; #define LDS_WAIT() asm volatile("s_waitcnt lgkmcnt(0)" ::: "memory")
; __device__ __forceinline__ void tr_flush(LAS unsigned* img, int K, int N, unsigned char* WT, size_t row_off, int fl, int lane) {
;     const int nblk = N / 64, kb = fl / nblk, nb = fl % nblk, k0 = 64 * NHB * kb, n0 = 64 * nb;
;     LDS_WAIT(); asm volatile("" ::: "memory");
;     constexpr int CPR = 4 * NHB, RPP = 64 / CPR;
;     const int c = lane % CPR;
; #pragma unroll 4
;     for (int p = 0; p < CPR; ++p) { const int n = lane / CPR + RPP * p;
;         const v4u o = *(const LAS v4u*)(img + n * (16 * NHB) + 4 * (c ^ ((n >> 2) & 7)));
;         *(GAS v4u*)(WT + (row_off + n0 + n) * (size_t)K + k0 + 16 * c) = o; }
;     LDS_WAIT(); asm volatile("" ::: "memory");
; }
.LBB0_565:
	s_add_i32 s9, s8, -3
	s_add_i32 s11, s8, -2
	s_add_i32 s36, s8, -1
	v_bitop3_b32 v72, s9, v213, 4 bitop3:0x6c
	v_bitop3_b32 v73, s11, v213, 5 bitop3:0x6c
	v_bitop3_b32 v74, s36, v213, 6 bitop3:0x6c
	v_lshl_add_u64 v[90:91], v[66:67], 0, v[198:199]
	v_bitop3_b32 v71, s8, v213, 7 bitop3:0x6c
	v_lshl_add_u32 v72, v72, 4, v70
	v_lshl_add_u32 v76, v73, 4, v70
	v_lshl_add_u32 v80, v74, 4, v70
	v_add_co_u32_e32 v92, vcc, s14, v90
	v_lshl_add_u32 v71, v71, 4, v70
	ds_read_b128 v[72:75], v72
	ds_read_b128 v[76:79], v76 offset:1024
	ds_read_b128 v[80:83], v80 offset:2048
	ds_read_b128 v[84:87], v71 offset:3072
	v_addc_co_u32_e32 v93, vcc, 0, v91, vcc
	v_add_co_u32_e32 v94, vcc, s15, v90
	s_add_i32 s8, s8, 4
	s_nop 0
	v_addc_co_u32_e32 v95, vcc, 0, v91, vcc
	v_lshl_add_u64 v[88:89], v[68:69], 0, v[198:199]
	v_lshl_add_u64 v[66:67], v[66:67], 0, s[4:5]
	v_lshl_add_u64 v[68:69], v[68:69], 0, s[4:5]
	s_cmp_lg_u32 s8, 19
	v_add_u32_e32 v70, 0x1000, v70
	v_add_co_u32_e32 v90, vcc, 0x68c0e000, v90
	s_nop 1
	v_addc_co_u32_e32 v91, vcc, 0, v91, vcc
	s_waitcnt lgkmcnt(3)
	global_store_dwordx4 v[88:89], v[72:75], off nt
	s_waitcnt lgkmcnt(2)
	global_store_dwordx4 v[92:93], v[76:79], off nt
	s_waitcnt lgkmcnt(1)
	global_store_dwordx4 v[94:95], v[80:83], off nt
	s_waitcnt lgkmcnt(0)
	global_store_dwordx4 v[90:91], v[84:87], off nt
	s_cbranch_scc1 .LBB0_565
	s_waitcnt lgkmcnt(0)
	s_mov_b64 s[8:9], 0

; #define GAS __attribute__((address_space(1)))
; #define LAS __attribute__((address_space(3)))
; #define LDS_WAIT() asm volatile("s_waitcnt lgkmcnt(0)" ::: "memory")
; __device__ __forceinline__ void tr_flush(LAS unsigned* img, int K, int N, unsigned char* WT, size_t row_off, int fl, int lane) {
;     const int nblk = N / 64, kb = fl / nblk, nb = fl % nblk, k0 = 64 * NHB * kb, n0 = 64 * nb;
;     LDS_WAIT(); asm volatile("" ::: "memory");
;     constexpr int CPR = 4 * NHB, RPP = 64 / CPR;
;     const int c = lane % CPR;
; #pragma unroll 4
;     for (int p = 0; p < CPR; ++p) { const int n = lane / CPR + RPP * p;
;         const v4u o = *(const LAS v4u*)(img + n * (16 * NHB) + 4 * (c ^ ((n >> 2) & 7)));
;         *(GAS v4u*)(WT + (row_off + n0 + n) * (size_t)K + k0 + 16 * c) = o; }
;     LDS_WAIT(); asm volatile("" ::: "memory");
; }
.LBB0_569:
	s_add_i32 s7, s6, -3
	s_add_i32 s10, s6, -2
	s_add_i32 s11, s6, -1
	v_bitop3_b32 v72, s7, v213, 4 bitop3:0x6c
	v_bitop3_b32 v73, s10, v213, 5 bitop3:0x6c
	v_bitop3_b32 v74, s11, v213, 6 bitop3:0x6c
	v_lshl_add_u64 v[90:91], v[66:67], 0, s[8:9]
	v_bitop3_b32 v71, s6, v213, 7 bitop3:0x6c
	v_lshl_add_u32 v72, v72, 4, v70
	v_lshl_add_u32 v76, v73, 4, v70
	v_lshl_add_u32 v80, v74, 4, v70
	v_add_co_u32_e32 v92, vcc, s16, v90
	v_lshl_add_u32 v71, v71, 4, v70
	ds_read_b128 v[72:75], v72
	ds_read_b128 v[76:79], v76 offset:1024
	ds_read_b128 v[80:83], v80 offset:2048
	ds_read_b128 v[84:87], v71 offset:3072
	v_addc_co_u32_e32 v93, vcc, 0, v91, vcc
	v_add_co_u32_e32 v94, vcc, s17, v90
	s_add_i32 s6, s6, 4
	s_nop 0
	v_addc_co_u32_e32 v95, vcc, 0, v91, vcc
	v_lshl_add_u64 v[88:89], v[68:69], 0, s[8:9]
	v_lshl_add_u64 v[66:67], v[66:67], 0, s[4:5]
	v_lshl_add_u64 v[68:69], v[68:69], 0, s[4:5]
	s_cmp_lg_u32 s6, 19
	v_add_u32_e32 v70, 0x1000, v70
	v_add_co_u32_e32 v90, vcc, 0x58c0e000, v90
	s_nop 1
	v_addc_co_u32_e32 v91, vcc, 0, v91, vcc
	s_waitcnt lgkmcnt(3)
	global_store_dwordx4 v[88:89], v[72:75], off nt
	s_waitcnt lgkmcnt(2)
	global_store_dwordx4 v[92:93], v[76:79], off nt
	s_waitcnt lgkmcnt(1)
	global_store_dwordx4 v[94:95], v[80:83], off nt
	s_waitcnt lgkmcnt(0)
	global_store_dwordx4 v[90:91], v[84:87], off nt
	s_cbranch_scc1 .LBB0_569
	s_waitcnt lgkmcnt(0)

; #define GAS __attribute__((address_space(1)))
; #define LAS __attribute__((address_space(3)))
; #define LDS_WAIT() asm volatile("s_waitcnt lgkmcnt(0)" ::: "memory")
; __device__ __forceinline__ void tr_flush(LAS unsigned* img, int K, int N, unsigned char* WT, size_t row_off, int fl, int lane) {
;     const int nblk = N / 64, kb = fl / nblk, nb = fl % nblk, k0 = 64 * NHB * kb, n0 = 64 * nb;
;     LDS_WAIT(); asm volatile("" ::: "memory");
;     constexpr int CPR = 4 * NHB, RPP = 64 / CPR;
;     const int c = lane % CPR;
; #pragma unroll 4
;     for (int p = 0; p < CPR; ++p) { const int n = lane / CPR + RPP * p;
;         const v4u o = *(const LAS v4u*)(img + n * (16 * NHB) + 4 * (c ^ ((n >> 2) & 7)));
;         *(GAS v4u*)(WT + (row_off + n0 + n) * (size_t)K + k0 + 16 * c) = o; }
;     LDS_WAIT(); asm volatile("" ::: "memory");
; }
.LBB0_579:
	s_add_i32 s9, s8, -3
	s_add_i32 s11, s8, -2
	s_add_i32 s31, s8, -1
	v_bitop3_b32 v136, s9, v213, 4 bitop3:0x6c
	v_bitop3_b32 v137, s11, v213, 5 bitop3:0x6c
	v_bitop3_b32 v138, s31, v213, 6 bitop3:0x6c
	v_lshl_add_u64 v[154:155], v[130:131], 0, v[198:199]
	v_bitop3_b32 v135, s8, v213, 7 bitop3:0x6c
	v_lshl_add_u32 v136, v136, 4, v134
	v_lshl_add_u32 v140, v137, 4, v134
	v_lshl_add_u32 v144, v138, 4, v134
	v_add_co_u32_e32 v156, vcc, s14, v154
	v_lshl_add_u32 v135, v135, 4, v134
	ds_read_b128 v[136:139], v136
	ds_read_b128 v[140:143], v140 offset:1024
	ds_read_b128 v[144:147], v144 offset:2048
	ds_read_b128 v[148:151], v135 offset:3072
	v_addc_co_u32_e32 v157, vcc, 0, v155, vcc
	v_add_co_u32_e32 v158, vcc, s15, v154
	s_add_i32 s8, s8, 4
	s_nop 0
	v_addc_co_u32_e32 v159, vcc, 0, v155, vcc
	v_lshl_add_u64 v[152:153], v[132:133], 0, v[198:199]
	v_lshl_add_u64 v[130:131], v[130:131], 0, s[4:5]
	v_lshl_add_u64 v[132:133], v[132:133], 0, s[4:5]
	s_cmp_lg_u32 s8, 19
	v_add_u32_e32 v134, 0x1000, v134
	v_add_co_u32_e32 v154, vcc, 0x68c0e000, v154
	s_nop 1
	v_addc_co_u32_e32 v155, vcc, 0, v155, vcc
	s_waitcnt lgkmcnt(3)
	global_store_dwordx4 v[152:153], v[136:139], off nt
	s_waitcnt lgkmcnt(2)
	global_store_dwordx4 v[156:157], v[140:143], off nt
	s_waitcnt lgkmcnt(1)
	global_store_dwordx4 v[158:159], v[144:147], off nt
	s_waitcnt lgkmcnt(0)
	global_store_dwordx4 v[154:155], v[148:151], off nt
	s_cbranch_scc1 .LBB0_579
	s_waitcnt lgkmcnt(0)
	s_mov_b64 s[8:9], 0

; #define GAS __attribute__((address_space(1)))
; #define LAS __attribute__((address_space(3)))
; #define LDS_WAIT() asm volatile("s_waitcnt lgkmcnt(0)" ::: "memory")
; __device__ __forceinline__ void tr_flush(LAS unsigned* img, int K, int N, unsigned char* WT, size_t row_off, int fl, int lane) {
;     const int nblk = N / 64, kb = fl / nblk, nb = fl % nblk, k0 = 64 * NHB * kb, n0 = 64 * nb;
;     LDS_WAIT(); asm volatile("" ::: "memory");
;     constexpr int CPR = 4 * NHB, RPP = 64 / CPR;
;     const int c = lane % CPR;
; #pragma unroll 4
;     for (int p = 0; p < CPR; ++p) { const int n = lane / CPR + RPP * p;
;         const v4u o = *(const LAS v4u*)(img + n * (16 * NHB) + 4 * (c ^ ((n >> 2) & 7)));
;         *(GAS v4u*)(WT + (row_off + n0 + n) * (size_t)K + k0 + 16 * c) = o; }
;     LDS_WAIT(); asm volatile("" ::: "memory");
; }
.LBB0_583:
	s_add_i32 s7, s6, -3
	s_add_i32 s10, s6, -2
	s_add_i32 s11, s6, -1
	v_bitop3_b32 v136, s7, v213, 4 bitop3:0x6c
	v_bitop3_b32 v137, s10, v213, 5 bitop3:0x6c
	v_bitop3_b32 v138, s11, v213, 6 bitop3:0x6c
	v_lshl_add_u64 v[154:155], v[130:131], 0, s[8:9]
	v_bitop3_b32 v135, s6, v213, 7 bitop3:0x6c
	v_lshl_add_u32 v136, v136, 4, v134
	v_lshl_add_u32 v140, v137, 4, v134
	v_lshl_add_u32 v144, v138, 4, v134
	v_add_co_u32_e32 v156, vcc, s16, v154
	v_lshl_add_u32 v135, v135, 4, v134
	ds_read_b128 v[136:139], v136
	ds_read_b128 v[140:143], v140 offset:1024
	ds_read_b128 v[144:147], v144 offset:2048
	ds_read_b128 v[148:151], v135 offset:3072
	v_addc_co_u32_e32 v157, vcc, 0, v155, vcc
	v_add_co_u32_e32 v158, vcc, s17, v154
	s_add_i32 s6, s6, 4
	s_nop 0
	v_addc_co_u32_e32 v159, vcc, 0, v155, vcc
	v_lshl_add_u64 v[152:153], v[132:133], 0, s[8:9]
	v_lshl_add_u64 v[130:131], v[130:131], 0, s[4:5]
	v_lshl_add_u64 v[132:133], v[132:133], 0, s[4:5]
	s_cmp_lg_u32 s6, 19
	v_add_u32_e32 v134, 0x1000, v134
	v_add_co_u32_e32 v154, vcc, 0x58c0e000, v154
	s_nop 1
	v_addc_co_u32_e32 v155, vcc, 0, v155, vcc
	s_waitcnt lgkmcnt(3)
	global_store_dwordx4 v[152:153], v[136:139], off nt
	s_waitcnt lgkmcnt(2)
	global_store_dwordx4 v[156:157], v[140:143], off nt
	s_waitcnt lgkmcnt(1)
	global_store_dwordx4 v[158:159], v[144:147], off nt
	s_waitcnt lgkmcnt(0)
	global_store_dwordx4 v[154:155], v[148:151], off nt
	s_cbranch_scc1 .LBB0_583
	s_waitcnt lgkmcnt(0)
	s_branch .LBB0_542

; __global__ void __launch_bounds__(NTHR, 2) mk_fwd(Args args) {
;     ...
; #pragma unroll
;         for (int st = 0; st < 8; ++st)
; #pragma unroll
;             for (int hf = 0; hf < 2; ++hf) { float w8[8];
; #pragma unroll
;                 for (int j = 0; j < 8; ++j) w8[j] = router_w[(size_t)(256 * wave + 32 * st + 8 * rq + j) * 32 + re + 16 * hf];
.LBB0_803:
	s_cmp_lt_i32 s88, 9
	s_cselect_b64 s[4:5], -1, 0
	s_add_u32 s16, s26, 0x10000
	s_addc_u32 s17, s27, 0
	s_add_u32 s14, s26, 0x148000
	s_addc_u32 s15, s27, 0
	s_add_u32 s12, s26, 0x1c8000
	s_addc_u32 s13, s27, 0
	s_add_u32 s10, s26, 0x4dc08000
	s_addc_u32 s11, s27, 0
	s_add_u32 s66, s26, 0x188000
	s_addc_u32 s67, s27, 0
	s_and_b64 s[18:19], s[4:5], s[2:3]
	s_andn2_b64 vcc, exec, s[18:19]
	s_cbranch_vccnz .LBB0_903
	s_waitcnt vmcnt(0)
	v_lshrrev_b32_e32 v174, 4, v194
	v_readlane_b32 s2, v252, 43
	s_lshl_b32 s34, s2, 8
	v_lshlrev_b32_e32 v166, 3, v174
	v_and_b32_e32 v178, 15, v0
	v_or_b32_e32 v170, s34, v166
	v_mov_b32_e32 v171, 0
	v_readlane_b32 s36, v252, 16
	v_lshlrev_b32_e32 v172, 2, v178
	v_mov_b32_e32 v173, v171
	v_readlane_b32 s40, v252, 20
	v_readlane_b32 s41, v252, 21
	v_or_b32_e32 v6, 1, v170
	v_mov_b32_e32 v7, v171
	v_lshl_add_u64 v[2:3], s[40:41], 0, v[172:173]
	v_lshlrev_b64 v[6:7], 7, v[6:7]
	v_lshl_add_u64 v[10:11], v[2:3], 0, v[6:7]
	v_or_b32_e32 v6, 2, v170
	v_mov_b32_e32 v7, v171
	v_lshlrev_b64 v[6:7], 7, v[6:7]
	v_lshl_add_u64 v[12:13], v[2:3], 0, v[6:7]
	v_or_b32_e32 v6, 3, v170
	v_mov_b32_e32 v7, v171
	v_lshlrev_b64 v[6:7], 7, v[6:7]
	v_lshl_add_u64 v[14:15], v[2:3], 0, v[6:7]
	v_or_b32_e32 v6, 4, v170
	v_mov_b32_e32 v7, v171
	v_lshlrev_b64 v[6:7], 7, v[6:7]
	v_lshl_add_u64 v[22:23], v[2:3], 0, v[6:7]
	v_or_b32_e32 v6, 5, v170
	v_mov_b32_e32 v7, v171
	v_lshlrev_b64 v[6:7], 7, v[6:7]
	v_lshl_add_u64 v[20:21], v[2:3], 0, v[6:7]
	v_or_b32_e32 v6, 6, v170
	v_mov_b32_e32 v7, v171
	v_lshlrev_b64 v[6:7], 7, v[6:7]
	v_lshl_add_u64 v[24:25], v[2:3], 0, v[6:7]
	v_or_b32_e32 v6, 7, v170
	v_mov_b32_e32 v7, v171
	v_lshlrev_b64 v[4:5], 7, v[170:171]
	v_lshlrev_b64 v[6:7], 7, v[6:7]
	v_lshl_add_u64 v[4:5], v[2:3], 0, v[4:5]
	v_lshl_add_u64 v[18:19], v[2:3], 0, v[6:7]
	global_load_dword v6, v[4:5], off
	global_load_dword v7, v[10:11], off
	global_load_dword v8, v[12:13], off
	global_load_dword v9, v[14:15], off
	global_load_dword v17, v[14:15], off offset:64
	global_load_dword v16, v[12:13], off offset:64
	s_nop 0
	global_load_dword v15, v[10:11], off offset:64
	global_load_dword v14, v[4:5], off offset:64
	global_load_dword v12, v[22:23], off
	global_load_dword v13, v[20:21], off
	s_nop 0
	global_load_dword v10, v[24:25], off
	global_load_dword v11, v[18:19], off
	s_nop 0
	global_load_dword v19, v[18:19], off offset:64
	s_nop 0
	global_load_dword v18, v[24:25], off offset:64
	s_nop 0
	global_load_dword v21, v[20:21], off offset:64
	s_nop 0
	global_load_dword v20, v[22:23], off offset:64
	v_or_b32_e32 v22, 33, v170
	v_mov_b32_e32 v23, v171
	v_lshlrev_b64 v[22:23], 7, v[22:23]
	v_lshl_add_u64 v[26:27], v[2:3], 0, v[22:23]
	v_or_b32_e32 v22, 34, v170
	v_mov_b32_e32 v23, v171
	v_lshlrev_b64 v[22:23], 7, v[22:23]
	v_lshl_add_u64 v[28:29], v[2:3], 0, v[22:23]
	v_or_b32_e32 v22, 35, v170
	v_mov_b32_e32 v23, v171
	v_lshlrev_b64 v[22:23], 7, v[22:23]
	v_lshl_add_u64 v[30:31], v[2:3], 0, v[22:23]
	v_or_b32_e32 v22, 36, v170
	v_mov_b32_e32 v23, v171
	v_lshlrev_b64 v[22:23], 7, v[22:23]
	v_lshl_add_u64 v[38:39], v[2:3], 0, v[22:23]
	v_or_b32_e32 v22, 37, v170
	v_mov_b32_e32 v23, v171
	v_lshlrev_b64 v[22:23], 7, v[22:23]
	v_lshl_add_u64 v[36:37], v[2:3], 0, v[22:23]
	v_or_b32_e32 v22, 38, v170
	v_mov_b32_e32 v23, v171
	v_lshlrev_b64 v[22:23], 7, v[22:23]
	v_or_b32_e32 v4, 32, v170
	v_mov_b32_e32 v5, v171
	v_lshl_add_u64 v[40:41], v[2:3], 0, v[22:23]
	v_or_b32_e32 v22, 39, v170
	v_mov_b32_e32 v23, v171
	v_lshlrev_b64 v[4:5], 7, v[4:5]
	v_lshlrev_b64 v[22:23], 7, v[22:23]
	v_lshl_add_u64 v[4:5], v[2:3], 0, v[4:5]
	v_lshl_add_u64 v[34:35], v[2:3], 0, v[22:23]
	global_load_dword v22, v[4:5], off
	global_load_dword v23, v[26:27], off
	global_load_dword v24, v[28:29], off
	global_load_dword v25, v[30:31], off
	global_load_dword v33, v[30:31], off offset:64
	global_load_dword v32, v[28:29], off offset:64
	s_nop 0
	global_load_dword v31, v[26:27], off offset:64
	global_load_dword v30, v[4:5], off offset:64
	global_load_dword v28, v[38:39], off
	global_load_dword v29, v[36:37], off
	s_nop 0
	global_load_dword v26, v[40:41], off
	global_load_dword v27, v[34:35], off
	s_nop 0
	global_load_dword v35, v[34:35], off offset:64
	s_nop 0
	global_load_dword v34, v[40:41], off offset:64
	s_nop 0
	global_load_dword v37, v[36:37], off offset:64
	s_nop 0
	global_load_dword v36, v[38:39], off offset:64
	v_or_b32_e32 v38, 0x41, v170
	v_mov_b32_e32 v39, v171
	v_lshlrev_b64 v[38:39], 7, v[38:39]
	v_lshl_add_u64 v[42:43], v[2:3], 0, v[38:39]
	v_or_b32_e32 v38, 0x42, v170
	v_mov_b32_e32 v39, v171
	v_lshlrev_b64 v[38:39], 7, v[38:39]
	v_lshl_add_u64 v[44:45], v[2:3], 0, v[38:39]
	v_or_b32_e32 v38, 0x43, v170
	v_mov_b32_e32 v39, v171
	v_lshlrev_b64 v[38:39], 7, v[38:39]
	v_lshl_add_u64 v[46:47], v[2:3], 0, v[38:39]
	v_or_b32_e32 v38, 0x44, v170
	v_mov_b32_e32 v39, v171
	v_lshlrev_b64 v[38:39], 7, v[38:39]
	v_lshl_add_u64 v[54:55], v[2:3], 0, v[38:39]
	v_or_b32_e32 v38, 0x45, v170
	v_mov_b32_e32 v39, v171
	v_lshlrev_b64 v[38:39], 7, v[38:39]
	v_lshl_add_u64 v[52:53], v[2:3], 0, v[38:39]
	v_or_b32_e32 v38, 0x46, v170
	v_mov_b32_e32 v39, v171
	v_lshlrev_b64 v[38:39], 7, v[38:39]
	v_or_b32_e32 v4, 64, v170
	v_mov_b32_e32 v5, v171
	v_lshl_add_u64 v[56:57], v[2:3], 0, v[38:39]
	v_or_b32_e32 v38, 0x47, v170
	v_mov_b32_e32 v39, v171
	v_lshlrev_b64 v[4:5], 7, v[4:5]
	v_lshlrev_b64 v[38:39], 7, v[38:39]
	v_lshl_add_u64 v[4:5], v[2:3], 0, v[4:5]
	v_lshl_add_u64 v[50:51], v[2:3], 0, v[38:39]
	global_load_dword v38, v[4:5], off
	global_load_dword v39, v[42:43], off
	global_load_dword v40, v[44:45], off
	global_load_dword v41, v[46:47], off
	global_load_dword v49, v[46:47], off offset:64
; __global__ void __launch_bounds__(NTHR, 2) mk_fwd(Args args) {
;     ...
; #pragma unroll
;         for (int st = 0; st < 8; ++st)
; #pragma unroll
;             for (int hf = 0; hf < 2; ++hf) { float w8[8];
; #pragma unroll
;                 for (int j = 0; j < 8; ++j) w8[j] = router_w[(size_t)(256 * wave + 32 * st + 8 * rq + j) * 32 + re + 16 * hf];
	global_load_dword v48, v[44:45], off offset:64
	s_nop 0
	global_load_dword v47, v[42:43], off offset:64
	global_load_dword v46, v[4:5], off offset:64
	global_load_dword v44, v[54:55], off
	global_load_dword v45, v[52:53], off
	s_nop 0
	global_load_dword v42, v[56:57], off
	global_load_dword v43, v[50:51], off
	s_nop 0
	global_load_dword v51, v[50:51], off offset:64
	s_nop 0
	global_load_dword v50, v[56:57], off offset:64
	s_nop 0
	global_load_dword v53, v[52:53], off offset:64
	s_nop 0
	global_load_dword v52, v[54:55], off offset:64
	v_or_b32_e32 v54, 0x61, v170
	v_mov_b32_e32 v55, v171
	v_lshlrev_b64 v[54:55], 7, v[54:55]
	v_lshl_add_u64 v[58:59], v[2:3], 0, v[54:55]
	v_or_b32_e32 v54, 0x62, v170
	v_mov_b32_e32 v55, v171
	v_lshlrev_b64 v[54:55], 7, v[54:55]
	v_lshl_add_u64 v[60:61], v[2:3], 0, v[54:55]
	v_or_b32_e32 v54, 0x63, v170
	v_mov_b32_e32 v55, v171
	v_lshlrev_b64 v[54:55], 7, v[54:55]
	v_lshl_add_u64 v[62:63], v[2:3], 0, v[54:55]
	v_or_b32_e32 v54, 0x64, v170
	v_mov_b32_e32 v55, v171
	v_lshlrev_b64 v[54:55], 7, v[54:55]
	v_lshl_add_u64 v[70:71], v[2:3], 0, v[54:55]
	v_or_b32_e32 v54, 0x65, v170
	v_mov_b32_e32 v55, v171
	v_lshlrev_b64 v[54:55], 7, v[54:55]
	v_lshl_add_u64 v[68:69], v[2:3], 0, v[54:55]
	v_or_b32_e32 v54, 0x66, v170
	v_mov_b32_e32 v55, v171
	v_lshlrev_b64 v[54:55], 7, v[54:55]
	v_or_b32_e32 v4, 0x60, v170
	v_mov_b32_e32 v5, v171
	v_lshl_add_u64 v[72:73], v[2:3], 0, v[54:55]
	v_or_b32_e32 v54, 0x67, v170
	v_mov_b32_e32 v55, v171
	v_lshlrev_b64 v[4:5], 7, v[4:5]
	v_lshlrev_b64 v[54:55], 7, v[54:55]
	v_lshl_add_u64 v[4:5], v[2:3], 0, v[4:5]
	v_lshl_add_u64 v[66:67], v[2:3], 0, v[54:55]
	global_load_dword v54, v[4:5], off
	global_load_dword v55, v[58:59], off
	global_load_dword v56, v[60:61], off
	global_load_dword v57, v[62:63], off
	global_load_dword v65, v[62:63], off offset:64
	global_load_dword v64, v[60:61], off offset:64
	s_nop 0
	global_load_dword v63, v[58:59], off offset:64
	global_load_dword v62, v[4:5], off offset:64
	global_load_dword v60, v[70:71], off
	global_load_dword v61, v[68:69], off
	s_nop 0
	global_load_dword v58, v[72:73], off
	global_load_dword v59, v[66:67], off
	s_nop 0
	global_load_dword v67, v[66:67], off offset:64
	s_nop 0
	global_load_dword v66, v[72:73], off offset:64
	s_nop 0
	global_load_dword v69, v[68:69], off offset:64
	s_nop 0
	global_load_dword v68, v[70:71], off offset:64
	v_or_b32_e32 v70, 0x81, v170
	v_mov_b32_e32 v71, v171
	v_lshlrev_b64 v[70:71], 7, v[70:71]
	v_lshl_add_u64 v[74:75], v[2:3], 0, v[70:71]
	v_or_b32_e32 v70, 0x82, v170
	v_mov_b32_e32 v71, v171
	v_lshlrev_b64 v[70:71], 7, v[70:71]
	v_lshl_add_u64 v[76:77], v[2:3], 0, v[70:71]
	v_or_b32_e32 v70, 0x83, v170
	v_mov_b32_e32 v71, v171
	v_lshlrev_b64 v[70:71], 7, v[70:71]
	v_lshl_add_u64 v[78:79], v[2:3], 0, v[70:71]
	v_or_b32_e32 v70, 0x84, v170
	v_mov_b32_e32 v71, v171
	v_lshlrev_b64 v[70:71], 7, v[70:71]
	v_lshl_add_u64 v[86:87], v[2:3], 0, v[70:71]
	v_or_b32_e32 v70, 0x85, v170
	v_mov_b32_e32 v71, v171
	v_lshlrev_b64 v[70:71], 7, v[70:71]
	v_lshl_add_u64 v[80:81], v[2:3], 0, v[70:71]
	v_or_b32_e32 v70, 0x86, v170
	v_mov_b32_e32 v71, v171
	v_lshlrev_b64 v[70:71], 7, v[70:71]
	v_or_b32_e32 v4, 0x80, v170
	v_mov_b32_e32 v5, v171
	v_lshl_add_u64 v[88:89], v[2:3], 0, v[70:71]
	v_or_b32_e32 v70, 0x87, v170
	v_mov_b32_e32 v71, v171
	v_lshlrev_b64 v[4:5], 7, v[4:5]
	v_lshlrev_b64 v[70:71], 7, v[70:71]
	v_lshl_add_u64 v[4:5], v[2:3], 0, v[4:5]
	v_lshl_add_u64 v[82:83], v[2:3], 0, v[70:71]
	global_load_dword v70, v[4:5], off
	global_load_dword v71, v[74:75], off
	global_load_dword v72, v[76:77], off
	global_load_dword v73, v[78:79], off
	global_load_dword v85, v[78:79], off offset:64
	global_load_dword v84, v[76:77], off offset:64
	s_nop 0
	global_load_dword v79, v[74:75], off offset:64
	global_load_dword v78, v[4:5], off offset:64
	global_load_dword v76, v[86:87], off
	global_load_dword v77, v[80:81], off
	s_nop 0
	global_load_dword v74, v[88:89], off
	global_load_dword v75, v[82:83], off
	s_nop 0
	global_load_dword v83, v[82:83], off offset:64
	s_nop 0
	global_load_dword v82, v[88:89], off offset:64
	s_nop 0
	global_load_dword v81, v[80:81], off offset:64
	s_nop 0
	global_load_dword v80, v[86:87], off offset:64
	v_or_b32_e32 v86, 0xa1, v170
	v_mov_b32_e32 v87, v171
	v_lshlrev_b64 v[86:87], 7, v[86:87]
	v_lshl_add_u64 v[90:91], v[2:3], 0, v[86:87]
	v_or_b32_e32 v86, 0xa2, v170
	v_mov_b32_e32 v87, v171
	v_lshlrev_b64 v[86:87], 7, v[86:87]
	v_lshl_add_u64 v[92:93], v[2:3], 0, v[86:87]
	v_or_b32_e32 v86, 0xa3, v170
	v_mov_b32_e32 v87, v171
	v_lshlrev_b64 v[86:87], 7, v[86:87]
	v_lshl_add_u64 v[94:95], v[2:3], 0, v[86:87]
	v_or_b32_e32 v86, 0xa4, v170
	v_mov_b32_e32 v87, v171
	v_lshlrev_b64 v[86:87], 7, v[86:87]
	v_lshl_add_u64 v[102:103], v[2:3], 0, v[86:87]
	v_or_b32_e32 v86, 0xa5, v170
	v_mov_b32_e32 v87, v171
	v_lshlrev_b64 v[86:87], 7, v[86:87]
	v_lshl_add_u64 v[96:97], v[2:3], 0, v[86:87]
	v_or_b32_e32 v86, 0xa6, v170
	v_mov_b32_e32 v87, v171
	v_lshlrev_b64 v[86:87], 7, v[86:87]
	v_or_b32_e32 v4, 0xa0, v170
	v_mov_b32_e32 v5, v171
	v_lshl_add_u64 v[104:105], v[2:3], 0, v[86:87]
	v_or_b32_e32 v86, 0xa7, v170
	v_mov_b32_e32 v87, v171
	v_lshlrev_b64 v[4:5], 7, v[4:5]
	v_lshlrev_b64 v[86:87], 7, v[86:87]
	v_lshl_add_u64 v[4:5], v[2:3], 0, v[4:5]
	v_lshl_add_u64 v[98:99], v[2:3], 0, v[86:87]
	global_load_dword v86, v[4:5], off
	global_load_dword v87, v[90:91], off
	global_load_dword v88, v[92:93], off
	global_load_dword v89, v[94:95], off
	global_load_dword v101, v[94:95], off offset:64
	global_load_dword v100, v[92:93], off offset:64
	s_nop 0
	global_load_dword v95, v[90:91], off offset:64
	global_load_dword v94, v[4:5], off offset:64
; #define LAS __attribute__((address_space(3)))
; __device__ __forceinline__ unsigned pk2(float lo, float hi) { return cvt_pk_bf16_nat(lo, hi); }
; __global__ void __launch_bounds__(NTHR, 2) mk_fwd(Args args) {
;     ...
; #pragma unroll
;         for (int st = 0; st < 8; ++st)
; #pragma unroll
;             for (int hf = 0; hf < 2; ++hf) { float w8[8];
; #pragma unroll
;                 for (int j = 0; j < 8; ++j) w8[j] = router_w[(size_t)(256 * wave + 32 * st + 8 * rq + j) * 32 + re + 16 * hf];
;                 v4u hi, lo;
;                 hi.x = pk2(w8[0], w8[1]); hi.y = pk2(w8[2], w8[3]); hi.z = pk2(w8[4], w8[5]); hi.w = pk2(w8[6], w8[7]);
;                 lo.x = pk2(w8[0] - bflo(hi.x), w8[1] - bfhi(hi.x)); lo.y = pk2(w8[2] - bflo(hi.y), w8[3] - bfhi(hi.y)); lo.z = pk2(w8[4] - bflo(hi.z), w8[5] - bfhi(hi.z)); lo.w = pk2(w8[6] - bflo(hi.w), w8[7] - bfhi(hi.w));
;                 wh[st][hf] = __builtin_bit_cast(bf16x8, hi); wl[st][hf] = __builtin_bit_cast(bf16x8, lo); }
;         LAS int* lcnt = (LAS int*)(lds + LDSCTL_OFF + 512);
;         if (tid < NE) lcnt[tid] = 0;
	global_load_dword v92, v[102:103], off
	global_load_dword v93, v[96:97], off
	s_nop 0
	global_load_dword v90, v[104:105], off
	global_load_dword v91, v[98:99], off
	s_nop 0
	global_load_dword v99, v[98:99], off offset:64
	s_nop 0
	global_load_dword v98, v[104:105], off offset:64
	s_nop 0
	global_load_dword v97, v[96:97], off offset:64
	s_nop 0
	global_load_dword v96, v[102:103], off offset:64
	v_or_b32_e32 v102, 0xc1, v170
	v_mov_b32_e32 v103, v171
	v_lshlrev_b64 v[102:103], 7, v[102:103]
	v_lshl_add_u64 v[106:107], v[2:3], 0, v[102:103]
	v_or_b32_e32 v102, 0xc2, v170
	v_mov_b32_e32 v103, v171
	v_lshlrev_b64 v[102:103], 7, v[102:103]
	v_lshl_add_u64 v[108:109], v[2:3], 0, v[102:103]
	v_or_b32_e32 v102, 0xc3, v170
	v_mov_b32_e32 v103, v171
	v_lshlrev_b64 v[102:103], 7, v[102:103]
	v_lshl_add_u64 v[110:111], v[2:3], 0, v[102:103]
	v_or_b32_e32 v102, 0xc4, v170
	v_mov_b32_e32 v103, v171
	v_lshlrev_b64 v[102:103], 7, v[102:103]
	v_lshl_add_u64 v[118:119], v[2:3], 0, v[102:103]
	v_or_b32_e32 v102, 0xc5, v170
	v_mov_b32_e32 v103, v171
	v_lshlrev_b64 v[102:103], 7, v[102:103]
	v_lshl_add_u64 v[116:117], v[2:3], 0, v[102:103]
	v_or_b32_e32 v102, 0xc6, v170
	v_mov_b32_e32 v103, v171
	v_lshlrev_b64 v[102:103], 7, v[102:103]
	v_or_b32_e32 v4, 0xc0, v170
	v_mov_b32_e32 v5, v171
	v_lshl_add_u64 v[120:121], v[2:3], 0, v[102:103]
	v_or_b32_e32 v102, 0xc7, v170
	v_mov_b32_e32 v103, v171
	v_lshlrev_b64 v[4:5], 7, v[4:5]
	v_lshlrev_b64 v[102:103], 7, v[102:103]
	v_lshl_add_u64 v[4:5], v[2:3], 0, v[4:5]
	v_lshl_add_u64 v[114:115], v[2:3], 0, v[102:103]
	global_load_dword v102, v[4:5], off
	global_load_dword v103, v[106:107], off
	global_load_dword v104, v[108:109], off
	global_load_dword v105, v[110:111], off
	global_load_dword v113, v[110:111], off offset:64
	global_load_dword v112, v[108:109], off offset:64
	s_nop 0
	global_load_dword v111, v[106:107], off offset:64
	global_load_dword v110, v[4:5], off offset:64
	global_load_dword v108, v[118:119], off
	global_load_dword v109, v[116:117], off
	s_nop 0
	global_load_dword v106, v[120:121], off
	global_load_dword v107, v[114:115], off
	s_nop 0
	global_load_dword v115, v[114:115], off offset:64
	s_nop 0
	global_load_dword v114, v[120:121], off offset:64
	s_nop 0
	global_load_dword v117, v[116:117], off offset:64
	s_nop 0
	global_load_dword v116, v[118:119], off offset:64
	v_or_b32_e32 v118, 0xe1, v170
	v_mov_b32_e32 v119, v171
	v_lshlrev_b64 v[118:119], 7, v[118:119]
	v_lshl_add_u64 v[122:123], v[2:3], 0, v[118:119]
	v_or_b32_e32 v118, 0xe2, v170
	v_mov_b32_e32 v119, v171
	v_lshlrev_b64 v[118:119], 7, v[118:119]
	v_lshl_add_u64 v[124:125], v[2:3], 0, v[118:119]
	v_or_b32_e32 v118, 0xe3, v170
	v_mov_b32_e32 v119, v171
	v_lshlrev_b64 v[118:119], 7, v[118:119]
	v_lshl_add_u64 v[126:127], v[2:3], 0, v[118:119]
	v_or_b32_e32 v118, 0xe4, v170
	v_mov_b32_e32 v119, v171
	v_lshlrev_b64 v[118:119], 7, v[118:119]
	v_lshl_add_u64 v[130:131], v[2:3], 0, v[118:119]
	v_or_b32_e32 v118, 0xe5, v170
	v_mov_b32_e32 v119, v171
	v_lshlrev_b64 v[118:119], 7, v[118:119]
	v_or_b32_e32 v4, 0xe0, v170
	v_mov_b32_e32 v5, v171
	v_lshl_add_u64 v[132:133], v[2:3], 0, v[118:119]
	v_or_b32_e32 v118, 0xe6, v170
	v_mov_b32_e32 v119, v171
	v_lshlrev_b64 v[4:5], 7, v[4:5]
	v_lshlrev_b64 v[118:119], 7, v[118:119]
	v_or_b32_e32 v170, 0xe7, v170
	v_lshl_add_u64 v[4:5], v[2:3], 0, v[4:5]
	v_lshl_add_u64 v[134:135], v[2:3], 0, v[118:119]
	v_lshlrev_b64 v[118:119], 7, v[170:171]
	v_lshl_add_u64 v[2:3], v[2:3], 0, v[118:119]
	global_load_dword v118, v[4:5], off
	global_load_dword v119, v[122:123], off
	global_load_dword v120, v[124:125], off
	global_load_dword v121, v[126:127], off
	global_load_dword v129, v[126:127], off offset:64
	global_load_dword v128, v[124:125], off offset:64
	s_nop 0
	global_load_dword v127, v[122:123], off offset:64
	global_load_dword v126, v[4:5], off offset:64
	global_load_dword v124, v[130:131], off
	global_load_dword v125, v[132:133], off
	s_nop 0
	global_load_dword v122, v[134:135], off
	global_load_dword v123, v[2:3], off
	global_load_dword v163, v[2:3], off offset:64
	global_load_dword v162, v[134:135], off offset:64
	global_load_dword v165, v[132:133], off offset:64
	global_load_dword v164, v[130:131], off offset:64
	v_cmp_gt_u32_e64 s[2:3], 32, v0
	v_readlane_b32 s37, v252, 17
	v_readlane_b32 s38, v252, 18
	v_readlane_b32 s39, v252, 19
	v_readlane_b32 s42, v252, 22
	v_readlane_b32 s43, v252, 23
	v_readlane_b32 s44, v252, 24
	v_readlane_b32 s45, v252, 25
	v_readlane_b32 s46, v252, 26
	v_readlane_b32 s47, v252, 27
	v_readlane_b32 s48, v252, 28
	v_readlane_b32 s49, v252, 29
	v_readlane_b32 s50, v252, 30
	v_readlane_b32 s51, v252, 31
	s_and_saveexec_b64 s[4:5], s[2:3]
	v_lshl_add_u32 v1, v0, 2, 0
	v_add_u32_e32 v1, 0x27200, v1
	ds_write_b32 v1, v171
	s_or_b64 exec, exec, s[4:5]
	s_waitcnt vmcnt(0)
; #define GAS __attribute__((address_space(1)))
; #define LAS __attribute__((address_space(3)))
; __device__ __forceinline__ unsigned pk2(float lo, float hi) { return cvt_pk_bf16_nat(lo, hi); }
; __global__ void __launch_bounds__(NTHR, 2) mk_fwd(Args args) {
;     ...
;             for (int hf = 0; hf < 2; ++hf) { float w8[8];
; #pragma unroll
;                 for (int j = 0; j < 8; ++j) w8[j] = router_w[(size_t)(256 * wave + 32 * st + 8 * rq + j) * 32 + re + 16 * hf];
;                 v4u hi, lo;
;                 hi.x = pk2(w8[0], w8[1]); hi.y = pk2(w8[2], w8[3]); hi.z = pk2(w8[4], w8[5]); hi.w = pk2(w8[6], w8[7]);
;                 lo.x = pk2(w8[0] - bflo(hi.x), w8[1] - bfhi(hi.x)); lo.y = pk2(w8[2] - bflo(hi.y), w8[3] - bfhi(hi.y)); lo.z = pk2(w8[4] - bflo(hi.z), w8[5] - bfhi(hi.z)); lo.w = pk2(w8[6] - bflo(hi.w), w8[7] - bfhi(hi.w));
;                 wh[st][hf] = __builtin_bit_cast(bf16x8, hi); wl[st][hf] = __builtin_bit_cast(bf16x8, lo); }
;         LAS int* lcnt = (LAS int*)(lds + LDSCTL_OFF + 512);
;         if (tid < NE) lcnt[tid] = 0;
;         const float rb = router_b[lane & 31];
;         *(LAS f32x4*)(s_lnw + 4 * tid) = *(const GAS f32x4*)(ln1_w + 4 * tid); *(LAS f32x4*)(s_lnb + 4 * tid) = *(const GAS f32x4*)(ln1_b + 4 * tid);
;         __syncthreads();
	v_cvt_pk_bf16_f32 v2, v6, v7
	v_cvt_pk_bf16_f32 v3, v8, v9
	v_lshlrev_b32_e32 v130, 16, v2
	v_and_b32_e32 v131, 0xffff0000, v2
	v_pk_add_f32 v[6:7], v[6:7], v[130:131] neg_lo:[0,1] neg_hi:[0,1]
	v_lshlrev_b32_e32 v130, 16, v3
	v_and_b32_e32 v131, 0xffff0000, v3
	v_cvt_pk_bf16_f32 v4, v12, v13
	v_pk_add_f32 v[8:9], v[8:9], v[130:131] neg_lo:[0,1] neg_hi:[0,1]
	v_cvt_pk_bf16_f32 v5, v10, v11
	v_cvt_pk_bf16_f32 v6, v6, v7
	v_cvt_pk_bf16_f32 v7, v8, v9
	v_lshlrev_b32_e32 v8, 16, v4
	v_and_b32_e32 v9, 0xffff0000, v4
	v_pk_add_f32 v[8:9], v[12:13], v[8:9] neg_lo:[0,1] neg_hi:[0,1]
	v_lshlrev_b32_e32 v12, 16, v5
	v_and_b32_e32 v13, 0xffff0000, v5
	v_pk_add_f32 v[10:11], v[10:11], v[12:13] neg_lo:[0,1] neg_hi:[0,1]
	v_cvt_pk_bf16_f32 v8, v8, v9
	v_cvt_pk_bf16_f32 v9, v10, v11
	v_cvt_pk_bf16_f32 v10, v14, v15
	v_cvt_pk_bf16_f32 v11, v16, v17
	v_lshlrev_b32_e32 v130, 16, v10
	v_and_b32_e32 v131, 0xffff0000, v10
	v_readlane_b32 s36, v252, 16
	v_pk_add_f32 v[14:15], v[14:15], v[130:131] neg_lo:[0,1] neg_hi:[0,1]
	v_lshlrev_b32_e32 v130, 16, v11
	v_and_b32_e32 v131, 0xffff0000, v11
	v_lshlrev_b32_e32 v140, 2, v195
	v_readlane_b32 s37, v252, 17
	v_pk_add_f32 v[16:17], v[16:17], v[130:131] neg_lo:[0,1] neg_hi:[0,1]
	v_readlane_b32 s38, v252, 18
	v_readlane_b32 s39, v252, 19
	v_cvt_pk_bf16_f32 v12, v20, v21
	v_cvt_pk_bf16_f32 v13, v18, v19
	global_load_dwordx4 v[130:133], v140, s[36:37]
	v_cvt_pk_bf16_f32 v14, v14, v15
	v_cvt_pk_bf16_f32 v15, v16, v17
	global_load_dwordx4 v[134:137], v140, s[38:39]
	v_lshlrev_b32_e32 v16, 16, v12
	v_and_b32_e32 v17, 0xffff0000, v12
	v_pk_add_f32 v[16:17], v[20:21], v[16:17] neg_lo:[0,1] neg_hi:[0,1]
	v_lshlrev_b32_e32 v20, 16, v13
	v_and_b32_e32 v21, 0xffff0000, v13
	v_pk_add_f32 v[18:19], v[18:19], v[20:21] neg_lo:[0,1] neg_hi:[0,1]
	v_cvt_pk_bf16_f32 v16, v16, v17
	v_cvt_pk_bf16_f32 v17, v18, v19
	v_cvt_pk_bf16_f32 v18, v22, v23
	v_cvt_pk_bf16_f32 v19, v24, v25
	v_lshlrev_b32_e32 v138, 16, v18
	v_and_b32_e32 v139, 0xffff0000, v18
	v_pk_add_f32 v[22:23], v[22:23], v[138:139] neg_lo:[0,1] neg_hi:[0,1]
	v_lshlrev_b32_e32 v138, 16, v19
	v_and_b32_e32 v139, 0xffff0000, v19
	v_cvt_pk_bf16_f32 v20, v28, v29
	v_pk_add_f32 v[24:25], v[24:25], v[138:139] neg_lo:[0,1] neg_hi:[0,1]
	v_cvt_pk_bf16_f32 v21, v26, v27
	v_cvt_pk_bf16_f32 v22, v22, v23
	v_cvt_pk_bf16_f32 v23, v24, v25
	v_lshlrev_b32_e32 v24, 16, v20
	v_and_b32_e32 v25, 0xffff0000, v20
	v_pk_add_f32 v[24:25], v[28:29], v[24:25] neg_lo:[0,1] neg_hi:[0,1]
	v_lshlrev_b32_e32 v28, 16, v21
	v_and_b32_e32 v29, 0xffff0000, v21
	v_pk_add_f32 v[26:27], v[26:27], v[28:29] neg_lo:[0,1] neg_hi:[0,1]
	v_cvt_pk_bf16_f32 v24, v24, v25
	v_cvt_pk_bf16_f32 v25, v26, v27
	v_cvt_pk_bf16_f32 v26, v30, v31
	v_cvt_pk_bf16_f32 v27, v32, v33
	v_lshlrev_b32_e32 v138, 16, v26
	v_and_b32_e32 v139, 0xffff0000, v26
	v_pk_add_f32 v[30:31], v[30:31], v[138:139] neg_lo:[0,1] neg_hi:[0,1]
	v_lshlrev_b32_e32 v138, 16, v27
	v_and_b32_e32 v139, 0xffff0000, v27
	v_cvt_pk_bf16_f32 v28, v36, v37
	v_pk_add_f32 v[32:33], v[32:33], v[138:139] neg_lo:[0,1] neg_hi:[0,1]
	v_cvt_pk_bf16_f32 v29, v34, v35
	v_cvt_pk_bf16_f32 v30, v30, v31
	v_cvt_pk_bf16_f32 v31, v32, v33
	v_lshlrev_b32_e32 v32, 16, v28
	v_and_b32_e32 v33, 0xffff0000, v28
	v_pk_add_f32 v[32:33], v[36:37], v[32:33] neg_lo:[0,1] neg_hi:[0,1]
	v_lshlrev_b32_e32 v36, 16, v29
	v_and_b32_e32 v37, 0xffff0000, v29
	v_pk_add_f32 v[34:35], v[34:35], v[36:37] neg_lo:[0,1] neg_hi:[0,1]
	v_cvt_pk_bf16_f32 v32, v32, v33
	v_cvt_pk_bf16_f32 v33, v34, v35
	v_cvt_pk_bf16_f32 v34, v38, v39
	v_cvt_pk_bf16_f32 v35, v40, v41
	v_lshlrev_b32_e32 v138, 16, v34
	v_and_b32_e32 v139, 0xffff0000, v34
	v_pk_add_f32 v[38:39], v[38:39], v[138:139] neg_lo:[0,1] neg_hi:[0,1]
	v_lshlrev_b32_e32 v138, 16, v35
	v_and_b32_e32 v139, 0xffff0000, v35
	v_cvt_pk_bf16_f32 v36, v44, v45
	v_pk_add_f32 v[40:41], v[40:41], v[138:139] neg_lo:[0,1] neg_hi:[0,1]
	v_cvt_pk_bf16_f32 v37, v42, v43
	v_cvt_pk_bf16_f32 v38, v38, v39
	v_cvt_pk_bf16_f32 v39, v40, v41
	v_lshlrev_b32_e32 v40, 16, v36
	v_and_b32_e32 v41, 0xffff0000, v36
	v_pk_add_f32 v[40:41], v[44:45], v[40:41] neg_lo:[0,1] neg_hi:[0,1]
	v_lshlrev_b32_e32 v44, 16, v37
	v_and_b32_e32 v45, 0xffff0000, v37
	v_pk_add_f32 v[42:43], v[42:43], v[44:45] neg_lo:[0,1] neg_hi:[0,1]
	v_cvt_pk_bf16_f32 v40, v40, v41
	v_cvt_pk_bf16_f32 v41, v42, v43
	v_cvt_pk_bf16_f32 v42, v46, v47
	v_cvt_pk_bf16_f32 v43, v48, v49
	v_lshlrev_b32_e32 v138, 16, v42
	v_and_b32_e32 v139, 0xffff0000, v42
	v_pk_add_f32 v[46:47], v[46:47], v[138:139] neg_lo:[0,1] neg_hi:[0,1]
	v_lshlrev_b32_e32 v138, 16, v43
	v_and_b32_e32 v139, 0xffff0000, v43
	v_cvt_pk_bf16_f32 v44, v52, v53
	v_pk_add_f32 v[48:49], v[48:49], v[138:139] neg_lo:[0,1] neg_hi:[0,1]
	s_add_u32 s8, s26, 0x45c08000
	v_readlane_b32 s40, v252, 20
	v_cvt_pk_bf16_f32 v46, v46, v47
	v_cvt_pk_bf16_f32 v47, v48, v49
	v_lshlrev_b32_e32 v48, 16, v44
	v_and_b32_e32 v49, 0xffff0000, v44
	s_addc_u32 s9, s27, 0
	s_add_i32 s35, 0, 0x14000
	v_pk_add_f32 v[48:49], v[52:53], v[48:49] neg_lo:[0,1] neg_hi:[0,1]
	v_add_u32_e32 v52, s35, v140
	s_add_i32 s40, 0, 0x16000
	s_ashr_i32 s31, s30, 31
	v_cvt_pk_bf16_f32 v45, v50, v51
	s_waitcnt vmcnt(0)
	ds_write_b128 v52, v[130:133]
	v_add_u32_e32 v52, s40, v140
	s_lshl_b64 s[6:7], s[30:31], 11
	s_lshl_b64 s[38:39], s[30:31], 12
	v_readlane_b32 s44, v252, 24
	v_readlane_b32 s45, v252, 25
	ds_write_b128 v52, v[134:137]
	s_add_u32 s4, s0, s38
	v_lshlrev_b32_e32 v52, 16, v45
	v_and_b32_e32 v53, 0xffff0000, v45
	s_addc_u32 s5, s1, s39
	v_readlane_b32 s44, v252, 46
	v_pk_add_f32 v[50:51], v[50:51], v[52:53] neg_lo:[0,1] neg_hi:[0,1]
	v_and_b32_e32 v1, 31, v0
	v_readlane_b32 s45, v252, 47
	s_add_u32 s36, s44, s38
	v_cvt_pk_bf16_f32 v48, v48, v49
	v_cvt_pk_bf16_f32 v49, v50, v51
	v_cvt_pk_bf16_f32 v50, v54, v55
	v_readlane_b32 s42, v252, 22
	v_readlane_b32 s43, v252, 23
	v_lshlrev_b32_e32 v1, 2, v1
	s_addc_u32 s37, s45, s39
	v_lshlrev_b32_e32 v167, 4, v194
	v_cvt_pk_bf16_f32 v51, v56, v57
	v_lshlrev_b32_e32 v138, 16, v50
	v_and_b32_e32 v139, 0xffff0000, v50
	global_load_dword v1, v1, s[42:43]
	s_waitcnt lgkmcnt(0)
	s_barrier
; __device__ __forceinline__ unsigned pk2(float lo, float hi) { return cvt_pk_bf16_nat(lo, hi); }
; __global__ void __launch_bounds__(NTHR, 2) mk_fwd(Args args) {
;     ...
;                 v4u hi, lo;
;                 hi.x = pk2(w8[0], w8[1]); hi.y = pk2(w8[2], w8[3]); hi.z = pk2(w8[4], w8[5]); hi.w = pk2(w8[6], w8[7]);
;                 lo.x = pk2(w8[0] - bflo(hi.x), w8[1] - bfhi(hi.x)); lo.y = pk2(w8[2] - bflo(hi.y), w8[3] - bfhi(hi.y)); lo.z = pk2(w8[4] - bflo(hi.z), w8[5] - bfhi(hi.z)); lo.w = pk2(w8[6] - bflo(hi.w), w8[7] - bfhi(hi.w));
;                 wh[st][hf] = __builtin_bit_cast(bf16x8, hi); wl[st][hf] = __builtin_bit_cast(bf16x8, lo); }
	global_load_dwordx4 v[130:133], v167, s[36:37]
	global_load_dwordx4 v[184:187], v167, s[4:5] offset:2048
	global_load_dwordx4 v[134:137], v167, s[4:5]
	v_pk_add_f32 v[54:55], v[54:55], v[138:139] neg_lo:[0,1] neg_hi:[0,1]
	v_lshlrev_b32_e32 v138, 16, v51
	v_and_b32_e32 v139, 0xffff0000, v51
	v_cvt_pk_bf16_f32 v52, v60, v61
	v_pk_add_f32 v[56:57], v[56:57], v[138:139] neg_lo:[0,1] neg_hi:[0,1]
	v_cvt_pk_bf16_f32 v53, v58, v59
	v_cvt_pk_bf16_f32 v54, v54, v55
	v_cvt_pk_bf16_f32 v55, v56, v57
	v_lshlrev_b32_e32 v56, 16, v52
	v_and_b32_e32 v57, 0xffff0000, v52
	v_pk_add_f32 v[56:57], v[60:61], v[56:57] neg_lo:[0,1] neg_hi:[0,1]
	v_lshlrev_b32_e32 v60, 16, v53
	v_and_b32_e32 v61, 0xffff0000, v53
	v_pk_add_f32 v[58:59], v[58:59], v[60:61] neg_lo:[0,1] neg_hi:[0,1]
	v_cvt_pk_bf16_f32 v56, v56, v57
	v_cvt_pk_bf16_f32 v57, v58, v59
	v_cvt_pk_bf16_f32 v58, v62, v63
	v_lshlrev_b32_e32 v142, 16, v58
	v_and_b32_e32 v143, 0xffff0000, v58
	global_load_dwordx4 v[138:141], v167, s[36:37] offset:1024
	global_load_dwordx4 v[180:183], v167, s[36:37] offset:2048
	v_pk_add_f32 v[62:63], v[62:63], v[142:143] neg_lo:[0,1] neg_hi:[0,1]
	global_load_dwordx4 v[142:145], v167, s[4:5] offset:1024
	global_load_dwordx4 v[188:191], v167, s[4:5] offset:3072
	global_load_dwordx4 v[196:199], v167, s[36:37] offset:3072
	v_cvt_pk_bf16_f32 v59, v64, v65
	v_lshlrev_b32_e32 v146, 16, v59
	v_and_b32_e32 v147, 0xffff0000, v59
	v_cvt_pk_bf16_f32 v60, v68, v69
	v_pk_add_f32 v[64:65], v[64:65], v[146:147] neg_lo:[0,1] neg_hi:[0,1]
	v_cvt_pk_bf16_f32 v61, v66, v67
	v_cvt_pk_bf16_f32 v62, v62, v63
	v_cvt_pk_bf16_f32 v63, v64, v65
	v_lshlrev_b32_e32 v64, 16, v60
	v_and_b32_e32 v65, 0xffff0000, v60
	v_pk_add_f32 v[64:65], v[68:69], v[64:65] neg_lo:[0,1] neg_hi:[0,1]
	v_lshlrev_b32_e32 v68, 16, v61
	v_and_b32_e32 v69, 0xffff0000, v61
	v_pk_add_f32 v[66:67], v[66:67], v[68:69] neg_lo:[0,1] neg_hi:[0,1]
	v_cvt_pk_bf16_f32 v64, v64, v65
	v_cvt_pk_bf16_f32 v65, v66, v67
	v_cvt_pk_bf16_f32 v66, v70, v71
	v_cvt_pk_bf16_f32 v67, v72, v73
	v_lshlrev_b32_e32 v146, 16, v66
	v_and_b32_e32 v147, 0xffff0000, v66
	v_pk_add_f32 v[70:71], v[70:71], v[146:147] neg_lo:[0,1] neg_hi:[0,1]
	v_lshlrev_b32_e32 v146, 16, v67
	v_and_b32_e32 v147, 0xffff0000, v67
	v_cvt_pk_bf16_f32 v68, v76, v77
	v_pk_add_f32 v[72:73], v[72:73], v[146:147] neg_lo:[0,1] neg_hi:[0,1]
	v_cvt_pk_bf16_f32 v69, v74, v75
	v_cvt_pk_bf16_f32 v70, v70, v71
	v_cvt_pk_bf16_f32 v71, v72, v73
	v_lshlrev_b32_e32 v72, 16, v68
	v_and_b32_e32 v73, 0xffff0000, v68
	v_pk_add_f32 v[72:73], v[76:77], v[72:73] neg_lo:[0,1] neg_hi:[0,1]
	v_lshlrev_b32_e32 v76, 16, v69
	v_and_b32_e32 v77, 0xffff0000, v69
	v_pk_add_f32 v[74:75], v[74:75], v[76:77] neg_lo:[0,1] neg_hi:[0,1]
	v_cvt_pk_bf16_f32 v72, v72, v73
	v_cvt_pk_bf16_f32 v73, v74, v75
	v_cvt_pk_bf16_f32 v74, v78, v79
	v_lshlrev_b32_e32 v146, 16, v74
	v_and_b32_e32 v147, 0xffff0000, v74
	v_pk_add_f32 v[78:79], v[78:79], v[146:147] neg_lo:[0,1] neg_hi:[0,1]
	s_mov_b32 s36, 0x3f9837f0
	s_mov_b32 s31, 0xf800000
	v_cvt_pk_bf16_f32 v78, v78, v79
	v_cvt_pk_bf16_f32 v75, v84, v85
	v_readlane_b32 s42, v252, 43
	v_readlane_b32 s41, v252, 21
	s_add_u32 s38, s8, s38
	s_addc_u32 s39, s9, s39
	v_cvt_pk_bf16_f32 v76, v80, v81
	v_cvt_pk_bf16_f32 v77, v82, v83
	v_readlane_b32 s46, v252, 26
	v_readlane_b32 s47, v252, 27
	v_readlane_b32 s48, v252, 28
	s_waitcnt vmcnt(7)
	v_lshlrev_b32_e32 v146, 16, v130
	v_and_b32_e32 v147, 0xffff0000, v130
	v_lshlrev_b32_e32 v130, 16, v131
	v_and_b32_e32 v131, 0xffff0000, v131
	s_waitcnt vmcnt(5)
	v_lshlrev_b32_e32 v148, 16, v134
	v_and_b32_e32 v149, 0xffff0000, v134
	v_lshlrev_b32_e32 v134, 16, v135
	v_and_b32_e32 v135, 0xffff0000, v135
	v_pk_fma_f32 v[154:155], v[130:131], s[36:37], v[134:135] op_sel_hi:[1,0,1]
	v_lshlrev_b32_e32 v130, 16, v132
	v_and_b32_e32 v131, 0xffff0000, v132
	v_lshlrev_b32_e32 v134, 16, v136
	v_and_b32_e32 v135, 0xffff0000, v136
	v_pk_fma_f32 v[158:159], v[146:147], s[36:37], v[148:149] op_sel_hi:[1,0,1]
	v_lshlrev_b32_e32 v132, 16, v133
	v_and_b32_e32 v133, 0xffff0000, v133
	v_lshlrev_b32_e32 v136, 16, v137
	v_and_b32_e32 v137, 0xffff0000, v137
	v_pk_fma_f32 v[160:161], v[130:131], s[36:37], v[134:135] op_sel_hi:[1,0,1]
	v_pk_fma_f32 v[156:157], v[132:133], s[36:37], v[136:137] op_sel_hi:[1,0,1]
	v_mov_b32_e32 v130, v158
	v_mov_b32_e32 v131, v160
	v_mov_b32_e32 v132, v159
	v_mov_b32_e32 v133, v161
	v_pk_add_f32 v[130:131], v[130:131], v[132:133]
	v_mov_b32_e32 v132, v154
	v_mov_b32_e32 v133, v156
	v_mov_b32_e32 v134, v155
	v_mov_b32_e32 v135, v157
	v_pk_add_f32 v[132:133], v[132:133], v[134:135]
	s_waitcnt vmcnt(2)
	v_lshlrev_b32_e32 v134, 16, v142
	v_pk_add_f32 v[130:131], v[130:131], v[132:133]
	v_lshlrev_b32_e32 v132, 16, v139
	v_pk_add_f32 v[168:169], v[130:131], v[130:131] op_sel:[0,1] op_sel_hi:[1,0]
	v_lshlrev_b32_e32 v130, 16, v138
	v_and_b32_e32 v131, 0xffff0000, v138
	v_and_b32_e32 v133, 0xffff0000, v139
	v_and_b32_e32 v135, 0xffff0000, v142
	v_lshlrev_b32_e32 v136, 16, v143
	v_and_b32_e32 v137, 0xffff0000, v143
	v_pk_fma_f32 v[146:147], v[132:133], s[36:37], v[136:137] op_sel_hi:[1,0,1]
	v_pk_fma_f32 v[150:151], v[130:131], s[36:37], v[134:135] op_sel_hi:[1,0,1]
	v_lshlrev_b32_e32 v130, 16, v140
	v_and_b32_e32 v131, 0xffff0000, v140
	v_lshlrev_b32_e32 v132, 16, v141
	v_and_b32_e32 v133, 0xffff0000, v141
	v_lshlrev_b32_e32 v134, 16, v144
	v_and_b32_e32 v135, 0xffff0000, v144
	v_lshlrev_b32_e32 v136, 16, v145
	v_and_b32_e32 v137, 0xffff0000, v145
	v_pk_fma_f32 v[148:149], v[132:133], s[36:37], v[136:137] op_sel_hi:[1,0,1]
	v_pk_fma_f32 v[152:153], v[130:131], s[36:37], v[134:135] op_sel_hi:[1,0,1]
	v_pk_mov_b32 v[130:131], v[150:151], v[146:147] op_sel:[1,0]
	v_mov_b32_e32 v132, v150
	v_mov_b32_e32 v133, v147
	v_pk_add_f32 v[130:131], v[130:131], v[132:133]
	v_mov_b32_e32 v132, v152
	v_pk_add_f32 v[176:177], v[130:131], v[130:131] op_sel:[0,1] op_sel_hi:[1,0]
	v_pk_mov_b32 v[130:131], v[152:153], v[148:149] op_sel:[1,0]
	v_mov_b32_e32 v133, v149
	v_pk_add_f32 v[130:131], v[130:131], v[132:133]
	v_lshlrev_b32_e32 v132, 16, v181
	v_pk_add_f32 v[192:193], v[130:131], v[130:131] op_sel:[0,1] op_sel_hi:[1,0]
	v_lshlrev_b32_e32 v130, 16, v180
	v_and_b32_e32 v131, 0xffff0000, v180
	v_and_b32_e32 v133, 0xffff0000, v181
	v_lshlrev_b32_e32 v134, 16, v184
	v_and_b32_e32 v135, 0xffff0000, v184
	v_lshlrev_b32_e32 v136, 16, v185
	v_and_b32_e32 v137, 0xffff0000, v185
	v_pk_fma_f32 v[138:139], v[132:133], s[36:37], v[136:137] op_sel_hi:[1,0,1]
	v_pk_fma_f32 v[142:143], v[130:131], s[36:37], v[134:135] op_sel_hi:[1,0,1]
	v_lshlrev_b32_e32 v130, 16, v182
	v_and_b32_e32 v131, 0xffff0000, v182
	v_lshlrev_b32_e32 v132, 16, v183
	v_and_b32_e32 v133, 0xffff0000, v183
	v_lshlrev_b32_e32 v134, 16, v186
	v_and_b32_e32 v135, 0xffff0000, v186
	v_lshlrev_b32_e32 v136, 16, v187
	v_and_b32_e32 v137, 0xffff0000, v187
	v_pk_fma_f32 v[140:141], v[132:133], s[36:37], v[136:137] op_sel_hi:[1,0,1]
	v_pk_fma_f32 v[144:145], v[130:131], s[36:37], v[134:135] op_sel_hi:[1,0,1]
	s_waitcnt vmcnt(0)
	v_lshlrev_b32_e32 v132, 16, v196
	v_and_b32_e32 v133, 0xffff0000, v196
	v_lshlrev_b32_e32 v130, 16, v197
	v_and_b32_e32 v131, 0xffff0000, v197
	v_lshlrev_b32_e32 v134, 16, v188
	v_and_b32_e32 v135, 0xffff0000, v188
	v_lshlrev_b32_e32 v136, 16, v189
	v_and_b32_e32 v137, 0xffff0000, v189
	v_pk_fma_f32 v[130:131], v[130:131], s[36:37], v[136:137] op_sel_hi:[1,0,1]
	v_pk_fma_f32 v[134:135], v[132:133], s[36:37], v[134:135] op_sel_hi:[1,0,1]
	v_lshlrev_b32_e32 v136, 16, v198
	v_and_b32_e32 v137, 0xffff0000, v198
	v_lshlrev_b32_e32 v132, 16, v199
	v_and_b32_e32 v133, 0xffff0000, v199
	v_lshlrev_b32_e32 v188, 16, v190
	v_and_b32_e32 v189, 0xffff0000, v190
	v_lshlrev_b32_e32 v190, 16, v191
	v_and_b32_e32 v191, 0xffff0000, v191
	v_pk_fma_f32 v[132:133], v[132:133], s[36:37], v[190:191] op_sel_hi:[1,0,1]
	v_pk_fma_f32 v[136:137], v[136:137], s[36:37], v[188:189] op_sel_hi:[1,0,1]
	v_mov_b32_e32 v169, v134
	v_mov_b32_e32 v188, v171
	v_mov_b32_e32 v189, v135
	v_mov_b32_e32 v177, v130
	v_mov_b32_e32 v193, v131
	v_add_f32_e32 v180, v142, v143
	v_add_f32_e32 v182, v138, v139
	v_add_f32_e32 v184, v144, v145
	v_add_f32_e32 v186, v140, v141
	v_pk_add_f32 v[168:169], v[168:169], v[188:189]
	v_pk_add_f32 v[176:177], v[176:177], v[192:193]
	v_mov_b32_e32 v181, v136
	v_mov_b32_e32 v183, v137
	v_mov_b32_e32 v185, v132
	v_mov_b32_e32 v187, v133
	v_pk_add_f32 v[168:169], v[168:169], v[176:177]
	v_pk_add_f32 v[176:177], v[180:181], v[182:183]
	v_pk_add_f32 v[180:181], v[184:185], v[186:187]
	v_mov_b32_e32 v182, 0x3a000000
	v_pk_add_f32 v[176:177], v[176:177], v[180:181]
	v_mov_b32_e32 v180, 0xba000000
	v_pk_add_f32 v[168:169], v[168:169], v[176:177]
	v_mov_b32_e32 v181, 0x3727c5ac
	v_add_f32_e32 v168, v168, v169
	v_mov_b32_e32 v169, v171
	v_mov_b32_e32 v183, 0x260
	v_add_f32_dpp v168, v168, v168 quad_perm:[1,0,3,2] row_mask:0xf bank_mask:0xf bound_ctrl:1
	s_mov_b32 s37, 0xc3e00000
	v_readlane_b32 s49, v252, 29
	v_add_f32_dpp v168, v168, v168 quad_perm:[2,3,0,1] row_mask:0xf bank_mask:0xf bound_ctrl:1
	v_readlane_b32 s50, v252, 30
	v_readlane_b32 s51, v252, 31
	v_add_f32_dpp v168, v168, v168 row_half_mirror row_mask:0xf bank_mask:0xf bound_ctrl:1
	s_nop 1
	v_add_f32_dpp v168, v168, v168 row_mirror row_mask:0xf bank_mask:0xf bound_ctrl:1
	s_nop 1
	v_mov_b32_dpp v169, v168 row_bcast:15 row_mask:0xa bank_mask:0xf
	v_add_f32_e32 v168, v168, v169
	v_mov_b32_e32 v169, v171
	s_nop 1
	v_mov_b32_dpp v169, v168 row_bcast:31 row_mask:0xc bank_mask:0xf
	v_add_f32_e32 v168, v168, v169
	s_nop 0
	v_readlane_b32 s4, v168, 63
	s_nop 1
	v_fmac_f32_e32 v155, s4, v180
	v_fmac_f32_e32 v159, s4, v180
	v_fma_f32 v154, s4, v180, v154
	v_fma_f32 v158, s4, v180, v158
	v_mul_f32_e32 v168, v159, v159
	v_mul_f32_e32 v169, v155, v155
	v_fmac_f32_e32 v168, v158, v158
	v_fmac_f32_e32 v169, v154, v154
	v_fmac_f32_e32 v157, s4, v180
	v_fmac_f32_e32 v161, s4, v180
	v_add_f32_e32 v168, v168, v169
	v_fma_f32 v156, s4, v180, v156
	v_fma_f32 v160, s4, v180, v160
	v_mul_f32_e32 v169, v161, v161
	v_mul_f32_e32 v170, v157, v157
	v_fmac_f32_e32 v169, v160, v160
	v_fmac_f32_e32 v170, v156, v156
	v_add_f32_e32 v169, v169, v170
	v_fmac_f32_e32 v147, s4, v180
	v_fmac_f32_e32 v151, s4, v180
	v_add_f32_e32 v168, v168, v169
	v_fma_f32 v146, s4, v180, v146
	v_fma_f32 v150, s4, v180, v150
	v_mul_f32_e32 v169, v151, v151
	v_mul_f32_e32 v170, v147, v147
	v_fmac_f32_e32 v169, v150, v150
	v_fmac_f32_e32 v170, v146, v146
	v_add_f32_e32 v169, v169, v170
	v_fmac_f32_e32 v149, s4, v180
	v_fmac_f32_e32 v153, s4, v180
	v_add_f32_e32 v168, v168, v169
	v_fma_f32 v148, s4, v180, v148
	v_fma_f32 v152, s4, v180, v152
	v_mul_f32_e32 v169, v153, v153
	v_mul_f32_e32 v170, v149, v149
	v_fmac_f32_e32 v169, v152, v152
	v_fmac_f32_e32 v170, v148, v148
	v_add_f32_e32 v169, v169, v170
	v_fmac_f32_e32 v139, s4, v180
	v_fmac_f32_e32 v143, s4, v180
	v_add_f32_e32 v168, v168, v169
	v_fma_f32 v138, s4, v180, v138
	v_fma_f32 v142, s4, v180, v142
	v_mul_f32_e32 v169, v143, v143
	v_mul_f32_e32 v170, v139, v139
	v_fmac_f32_e32 v169, v142, v142
	v_fmac_f32_e32 v170, v138, v138
	v_add_f32_e32 v169, v169, v170
	v_fmac_f32_e32 v141, s4, v180
	v_fmac_f32_e32 v145, s4, v180
	v_add_f32_e32 v168, v168, v169
	v_fma_f32 v140, s4, v180, v140
	v_fma_f32 v144, s4, v180, v144
	v_mul_f32_e32 v169, v145, v145
	v_mul_f32_e32 v170, v141, v141
	v_fmac_f32_e32 v169, v144, v144
	v_fmac_f32_e32 v170, v140, v140
	v_add_f32_e32 v169, v169, v170
	v_fmac_f32_e32 v131, s4, v180
	v_fmac_f32_e32 v135, s4, v180
	v_add_f32_e32 v168, v168, v169
	v_fma_f32 v130, s4, v180, v130
	v_fma_f32 v134, s4, v180, v134
	v_mul_f32_e32 v169, v135, v135
	v_mul_f32_e32 v170, v131, v131
	v_fmac_f32_e32 v169, v134, v134
	v_fmac_f32_e32 v170, v130, v130
	v_add_f32_e32 v169, v169, v170
	v_fmac_f32_e32 v133, s4, v180
	v_fmac_f32_e32 v137, s4, v180
	v_add_f32_e32 v168, v168, v169
	v_fma_f32 v132, s4, v180, v132
	v_fma_f32 v136, s4, v180, v136
	v_mul_f32_e32 v169, v137, v137
	v_mul_f32_e32 v170, v133, v133
	v_fmac_f32_e32 v169, v136, v136
	v_fmac_f32_e32 v170, v132, v132
	v_add_f32_e32 v169, v169, v170
	v_add_f32_e32 v168, v168, v169
	v_mov_b32_e32 v169, v171
	s_nop 0
	v_add_f32_dpp v168, v168, v168 quad_perm:[1,0,3,2] row_mask:0xf bank_mask:0xf bound_ctrl:1
	s_nop 1
	v_add_f32_dpp v168, v168, v168 quad_perm:[2,3,0,1] row_mask:0xf bank_mask:0xf bound_ctrl:1
	s_nop 1
	v_add_f32_dpp v168, v168, v168 row_half_mirror row_mask:0xf bank_mask:0xf bound_ctrl:1
	s_nop 1
	v_add_f32_dpp v168, v168, v168 row_mirror row_mask:0xf bank_mask:0xf bound_ctrl:1
	s_nop 1
	v_mov_b32_dpp v169, v168 row_bcast:15 row_mask:0xa bank_mask:0xf
	v_add_f32_e32 v168, v168, v169
	v_mov_b32_e32 v169, v171
	s_nop 1
	v_mov_b32_dpp v169, v168 row_bcast:31 row_mask:0xc bank_mask:0xf
	v_add_f32_e32 v168, v168, v169
	s_nop 0
	v_readlane_b32 s4, v168, 63
	s_nop 1
	v_fma_f32 v168, s4, v182, v181
	v_mul_f32_e32 v169, 0x4f800000, v168
	v_cmp_gt_f32_e32 vcc, s31, v168
	s_nop 1
	v_cndmask_b32_e32 v170, v168, v169, vcc
	v_sqrt_f32_e32 v173, v170
	v_lshlrev_b32_e32 v168, 16, v75
	v_and_b32_e32 v169, 0xffff0000, v75
	v_pk_add_f32 v[84:85], v[84:85], v[168:169] neg_lo:[0,1] neg_hi:[0,1]
	v_add_u32_e32 v79, -1, v173
	v_fma_f32 v175, -v79, v173, v170
	v_cmp_ge_f32_e64 s[4:5], 0, v175
	v_add_u32_e32 v175, 1, v173
	s_nop 0
	v_cndmask_b32_e64 v79, v173, v79, s[4:5]
	v_fma_f32 v173, -v175, v173, v170
	v_cmp_lt_f32_e64 s[4:5], 0, v173
	s_nop 1
	v_cndmask_b32_e64 v79, v79, v175, s[4:5]
	v_mul_f32_e32 v173, 0x37800000, v79
	v_cndmask_b32_e32 v79, v79, v173, vcc
	v_cmp_class_f32_e32 vcc, v170, v183
	s_nop 1
	v_cndmask_b32_e32 v173, v79, v170, vcc
	v_div_scale_f32 v175, s[4:5], v173, v173, 1.0
	v_rcp_f32_e32 v176, v175
	v_cvt_pk_bf16_f32 v79, v84, v85
	s_mul_i32 s4, s42, 0x1040
	s_add_i32 s41, s4, 0
	v_fma_f32 v84, -v175, v176, 1.0
	v_fmac_f32_e32 v176, v84, v176
	v_div_scale_f32 v84, vcc, 1.0, v173, 1.0
	v_mul_f32_e32 v85, v84, v176
	v_fma_f32 v168, -v175, v85, v84
	v_fmac_f32_e32 v85, v168, v176
	v_fma_f32 v84, -v175, v85, v84
	v_div_fmas_f32 v84, v84, v176, v85
	v_lshlrev_b32_e32 v85, 5, v194
	v_add_u32_e32 v184, s35, v85
	v_add_u32_e32 v185, s40, v85
	ds_read_b128 v[186:189], v184
	ds_read_b128 v[190:193], v185
	ds_read_b128 v[196:199], v184 offset:16
	ds_read_b128 v[200:203], v185 offset:16
	v_div_fixup_f32 v84, v84, v173, 1.0
	v_pk_mul_f32 v[158:159], v[84:85], v[158:159] op_sel_hi:[0,1]
	v_pk_mul_f32 v[154:155], v[84:85], v[154:155] op_sel_hi:[0,1]
	s_waitcnt lgkmcnt(2)
	v_pk_fma_f32 v[168:169], v[154:155], v[188:189], v[192:193]
	v_pk_fma_f32 v[176:177], v[158:159], v[186:187], v[190:191]
	v_pk_mul_f32 v[154:155], v[84:85], v[160:161] op_sel_hi:[0,1]
	v_pk_mul_f32 v[156:157], v[84:85], v[156:157] op_sel_hi:[0,1]
	s_waitcnt lgkmcnt(0)
	v_pk_fma_f32 v[190:191], v[154:155], v[196:197], v[200:201]
	v_cvt_pk_bf16_f32 v154, v176, v177
	v_cvt_pk_bf16_f32 v155, v168, v169
	v_pk_fma_f32 v[188:189], v[156:157], v[198:199], v[202:203]
	v_lshlrev_b32_e32 v158, 16, v154
	v_and_b32_e32 v159, 0xffff0000, v154
	v_lshlrev_b32_e32 v160, 16, v155
	v_and_b32_e32 v161, 0xffff0000, v155
	v_cvt_pk_bf16_f32 v156, v190, v191
	v_cvt_pk_bf16_f32 v157, v188, v189
	v_pk_add_f32 v[158:159], v[176:177], v[158:159] neg_lo:[0,1] neg_hi:[0,1]
	v_pk_add_f32 v[160:161], v[168:169], v[160:161] neg_lo:[0,1] neg_hi:[0,1]
	v_cvt_pk_bf16_f32 v158, v158, v159
	v_cvt_pk_bf16_f32 v159, v160, v161
	v_lshlrev_b32_e32 v160, 16, v156
	v_and_b32_e32 v161, 0xffff0000, v156
	v_lshlrev_b32_e32 v186, 16, v157
	v_and_b32_e32 v187, 0xffff0000, v157
	v_pk_add_f32 v[160:161], v[190:191], v[160:161] neg_lo:[0,1] neg_hi:[0,1]
	v_pk_add_f32 v[186:187], v[188:189], v[186:187] neg_lo:[0,1] neg_hi:[0,1]
	v_cvt_pk_bf16_f32 v160, v160, v161
	v_cvt_pk_bf16_f32 v161, v186, v187
	v_mul_f32_e32 v173, 0x41000000, v176
	v_mul_f32_e32 v175, 0x41000000, v177
	v_mov_b32_e32 v186, 0x43e00000
	v_mul_f32_e32 v176, 0x41000000, v168
	v_med3_f32 v173, v173, s37, v186
	v_med3_f32 v175, v175, s37, v186
	v_mov_b32_e32 v168, v171
	v_cvt_pk_fp8_f32 v168, v173, v175
	v_mul_f32_e32 v169, 0x41000000, v169
	v_med3_f32 v173, v176, s37, v186
	v_med3_f32 v169, v169, s37, v186
	v_cvt_pk_fp8_f32 v168, v173, v169 op_sel:[0,0,1]
	v_mul_f32_e32 v169, 0x41000000, v190
	v_mul_f32_e32 v173, 0x41000000, v191
	v_med3_f32 v176, v169, s37, v186
	v_med3_f32 v173, v173, s37, v186
	v_mov_b32_e32 v169, v171
	v_cvt_pk_fp8_f32 v169, v176, v173
	v_mul_f32_e32 v175, 0x41000000, v188
	v_mul_f32_e32 v173, 0x41000000, v189
	v_med3_f32 v175, v175, s37, v186
	v_med3_f32 v173, v173, s37, v186
	v_cvt_pk_fp8_f32 v169, v175, v173 op_sel:[0,0,1]
	v_add_u32_e32 v187, s41, v167
	s_add_u32 s4, s10, s6
	global_store_dwordx4 v167, v[154:157], s[38:39] nt
	ds_write_b128 v187, v[154:157]
	ds_write_b128 v187, v[158:161] offset:33280
	v_or_b32_e32 v158, 0x800, v85
	v_lshlrev_b32_e32 v170, 3, v194
	s_addc_u32 s5, s11, s7
	v_add_u32_e32 v188, s35, v158
	v_add_u32_e32 v189, s40, v158
	global_store_dwordx2 v170, v[168:169], s[4:5]
	ds_read_b128 v[154:157], v188
	ds_read_b128 v[158:161], v189
	ds_read_b128 v[190:193], v188 offset:16
	ds_read_b128 v[196:199], v189 offset:16
	v_pk_mul_f32 v[150:151], v[84:85], v[150:151] op_sel_hi:[0,1]
	v_pk_mul_f32 v[146:147], v[84:85], v[146:147] op_sel_hi:[0,1]
	v_pk_mul_f32 v[148:149], v[84:85], v[148:149] op_sel_hi:[0,1]
	s_waitcnt lgkmcnt(2)
	v_pk_fma_f32 v[156:157], v[146:147], v[156:157], v[160:161]
	v_pk_fma_f32 v[154:155], v[150:151], v[154:155], v[158:159]
	v_pk_mul_f32 v[146:147], v[84:85], v[152:153] op_sel_hi:[0,1]
	s_waitcnt lgkmcnt(0)
	v_pk_fma_f32 v[160:161], v[146:147], v[190:191], v[196:197]
	v_cvt_pk_bf16_f32 v146, v154, v155
	v_cvt_pk_bf16_f32 v147, v156, v157
	v_lshlrev_b32_e32 v150, 16, v146
	v_and_b32_e32 v151, 0xffff0000, v146
	v_lshlrev_b32_e32 v152, 16, v147
	v_and_b32_e32 v153, 0xffff0000, v147
	v_pk_fma_f32 v[158:159], v[148:149], v[192:193], v[198:199]
	v_cvt_pk_bf16_f32 v148, v160, v161
	v_pk_add_f32 v[150:151], v[154:155], v[150:151] neg_lo:[0,1] neg_hi:[0,1]
	v_pk_add_f32 v[152:153], v[156:157], v[152:153] neg_lo:[0,1] neg_hi:[0,1]
	v_cvt_pk_bf16_f32 v150, v150, v151
	v_cvt_pk_bf16_f32 v151, v152, v153
	v_lshlrev_b32_e32 v152, 16, v148
	v_and_b32_e32 v153, 0xffff0000, v148
	v_pk_add_f32 v[152:153], v[160:161], v[152:153] neg_lo:[0,1] neg_hi:[0,1]
	v_cvt_pk_bf16_f32 v149, v158, v159
	v_cvt_pk_bf16_f32 v152, v152, v153
	v_mul_f32_e32 v153, 0x41000000, v154
	v_mul_f32_e32 v154, 0x41000000, v155
	v_mul_f32_e32 v155, 0x41000000, v156
	v_med3_f32 v153, v153, s37, v186
	v_med3_f32 v156, v154, s37, v186
	v_mov_b32_e32 v154, v171
	v_cvt_pk_fp8_f32 v154, v153, v156
	v_mul_f32_e32 v153, 0x41000000, v157
	v_med3_f32 v155, v155, s37, v186
	v_med3_f32 v153, v153, s37, v186
	v_cvt_pk_fp8_f32 v154, v155, v153 op_sel:[0,0,1]
	v_mul_f32_e32 v153, 0x41000000, v160
	v_mul_f32_e32 v155, 0x41000000, v161
	v_med3_f32 v153, v153, s37, v186
	v_med3_f32 v157, v155, s37, v186
	v_mov_b32_e32 v155, v171
	v_cvt_pk_fp8_f32 v155, v153, v157
	v_mul_f32_e32 v156, 0x41000000, v158
	v_mul_f32_e32 v153, 0x41000000, v159
	v_med3_f32 v156, v156, s37, v186
	v_med3_f32 v153, v153, s37, v186
	v_lshlrev_b32_e32 v168, 16, v149
	v_and_b32_e32 v169, 0xffff0000, v149
	v_cvt_pk_fp8_f32 v155, v156, v153 op_sel:[0,0,1]
	v_pk_add_f32 v[168:169], v[158:159], v[168:169] neg_lo:[0,1] neg_hi:[0,1]
	global_store_dwordx4 v167, v[146:149], s[38:39] offset:1024 nt
	v_cvt_pk_bf16_f32 v153, v168, v169
	ds_write_b128 v187, v[146:149] offset:1024
	ds_write_b128 v187, v[150:153] offset:34304
	v_or_b32_e32 v150, 0x1000, v85
	v_add_u32_e32 v190, s35, v150
	v_add_u32_e32 v191, s40, v150
	global_store_dwordx2 v170, v[154:155], s[4:5] offset:512
	ds_read_b128 v[146:149], v190
	ds_read_b128 v[150:153], v191
	ds_read_b128 v[154:157], v190 offset:16
	ds_read_b128 v[158:161], v191 offset:16
	v_pk_mul_f32 v[142:143], v[84:85], v[142:143] op_sel_hi:[0,1]
	v_pk_mul_f32 v[138:139], v[84:85], v[138:139] op_sel_hi:[0,1]
	v_pk_mul_f32 v[140:141], v[84:85], v[140:141] op_sel_hi:[0,1]
	s_waitcnt lgkmcnt(2)
	v_pk_fma_f32 v[148:149], v[138:139], v[148:149], v[152:153]
	v_pk_fma_f32 v[146:147], v[142:143], v[146:147], v[150:151]
	v_pk_mul_f32 v[138:139], v[84:85], v[144:145] op_sel_hi:[0,1]
	s_waitcnt lgkmcnt(0)
; #define P8_FETCH(m_) do { _Pragma("unroll") for (int q = 0; q < 4; ++q) { rm[q] = *(const GAS v4u*)(MIX + (size_t)(m_) * D + 8 * lane + 512 * q); rx[q] = *(const GAS v4u*)(XB + (size_t)(m_) * D + 8 * lane + 512 * q); } } while (0)
; #define P8_SYNC() do { asm volatile("s_waitcnt lgkmcnt(0)" ::: "memory"); __builtin_amdgcn_s_barrier(); asm volatile("" ::: "memory"); } while (0)
; __global__ void __launch_bounds__(NTHR, 2) mk_fwd(Args args) {
;     ...
;         const int mfirst = vcu * 8 + wave;
;         P8_FETCH(mfirst);
;         P8_LN(mfirst); P8_FETCH(mfirst + G * 8);
;         P8_SYNC();
	v_pk_fma_f32 v[152:153], v[138:139], v[154:155], v[158:159]
	v_cvt_pk_bf16_f32 v138, v146, v147
	v_cvt_pk_bf16_f32 v139, v148, v149
	v_lshlrev_b32_e32 v142, 16, v138
	v_and_b32_e32 v143, 0xffff0000, v138
	v_lshlrev_b32_e32 v144, 16, v139
	v_and_b32_e32 v145, 0xffff0000, v139
	v_pk_fma_f32 v[150:151], v[140:141], v[156:157], v[160:161]
	v_cvt_pk_bf16_f32 v140, v152, v153
	v_pk_add_f32 v[142:143], v[146:147], v[142:143] neg_lo:[0,1] neg_hi:[0,1]
	v_pk_add_f32 v[144:145], v[148:149], v[144:145] neg_lo:[0,1] neg_hi:[0,1]
	v_cvt_pk_bf16_f32 v142, v142, v143
	v_cvt_pk_bf16_f32 v143, v144, v145
	v_lshlrev_b32_e32 v144, 16, v140
	v_and_b32_e32 v145, 0xffff0000, v140
	v_pk_add_f32 v[144:145], v[152:153], v[144:145] neg_lo:[0,1] neg_hi:[0,1]
	v_cvt_pk_bf16_f32 v141, v150, v151
	v_cvt_pk_bf16_f32 v144, v144, v145
	v_mul_f32_e32 v145, 0x41000000, v146
	v_mul_f32_e32 v146, 0x41000000, v147
	v_mul_f32_e32 v147, 0x41000000, v148
	v_med3_f32 v145, v145, s37, v186
	v_med3_f32 v148, v146, s37, v186
	v_mov_b32_e32 v146, v171
	v_cvt_pk_fp8_f32 v146, v145, v148
	v_mul_f32_e32 v145, 0x41000000, v149
	v_med3_f32 v147, v147, s37, v186
	v_med3_f32 v145, v145, s37, v186
	v_cvt_pk_fp8_f32 v146, v147, v145 op_sel:[0,0,1]
	v_mul_f32_e32 v145, 0x41000000, v152
	v_mul_f32_e32 v147, 0x41000000, v153
	v_med3_f32 v145, v145, s37, v186
	v_med3_f32 v149, v147, s37, v186
	v_mov_b32_e32 v147, v171
	v_cvt_pk_fp8_f32 v147, v145, v149
	v_mul_f32_e32 v148, 0x41000000, v150
	v_mul_f32_e32 v145, 0x41000000, v151
	v_med3_f32 v148, v148, s37, v186
	v_med3_f32 v145, v145, s37, v186
	v_cvt_pk_fp8_f32 v147, v148, v145 op_sel:[0,0,1]
	v_lshlrev_b32_e32 v154, 16, v141
	v_and_b32_e32 v155, 0xffff0000, v141
	v_pk_add_f32 v[154:155], v[150:151], v[154:155] neg_lo:[0,1] neg_hi:[0,1]
	v_or_b32_e32 v85, 0x1800, v85
	global_store_dwordx4 v167, v[138:141], s[38:39] offset:2048 nt
	v_cvt_pk_bf16_f32 v145, v154, v155
	ds_write_b128 v187, v[138:141] offset:2048
	ds_write_b128 v187, v[142:145] offset:35328
	v_add_u32_e32 v193, s35, v85
	v_add_u32_e32 v196, s40, v85
	global_store_dwordx2 v170, v[146:147], s[4:5] offset:1024
	ds_read_b128 v[138:141], v193
	ds_read_b128 v[142:145], v196
	ds_read_b128 v[146:149], v193 offset:16
	ds_read_b128 v[150:153], v196 offset:16
	v_pk_mul_f32 v[134:135], v[84:85], v[134:135] op_sel_hi:[0,1]
	v_pk_mul_f32 v[130:131], v[84:85], v[130:131] op_sel_hi:[0,1]
	v_lshlrev_b32_e32 v173, 2, v174
	s_waitcnt lgkmcnt(2)
	v_pk_fma_f32 v[140:141], v[130:131], v[140:141], v[144:145]
	v_pk_fma_f32 v[138:139], v[134:135], v[138:139], v[142:143]
	v_pk_mul_f32 v[130:131], v[84:85], v[136:137] op_sel_hi:[0,1]
	s_waitcnt lgkmcnt(0)
	v_pk_fma_f32 v[142:143], v[130:131], v[146:147], v[150:151]
	v_cvt_pk_bf16_f32 v130, v138, v139
	v_cvt_pk_bf16_f32 v131, v140, v141
	v_lshlrev_b32_e32 v134, 16, v130
	v_and_b32_e32 v135, 0xffff0000, v130
	v_lshlrev_b32_e32 v136, 16, v131
	v_and_b32_e32 v137, 0xffff0000, v131
	v_pk_mul_f32 v[84:85], v[84:85], v[132:133] op_sel_hi:[0,1]
	v_cvt_pk_bf16_f32 v132, v142, v143
	v_pk_add_f32 v[134:135], v[138:139], v[134:135] neg_lo:[0,1] neg_hi:[0,1]
	v_pk_add_f32 v[136:137], v[140:141], v[136:137] neg_lo:[0,1] neg_hi:[0,1]
	v_cvt_pk_bf16_f32 v134, v134, v135
	v_cvt_pk_bf16_f32 v135, v136, v137
	v_lshlrev_b32_e32 v136, 16, v132
	v_and_b32_e32 v137, 0xffff0000, v132
	v_pk_add_f32 v[136:137], v[142:143], v[136:137] neg_lo:[0,1] neg_hi:[0,1]
	v_pk_fma_f32 v[84:85], v[84:85], v[148:149], v[152:153]
	v_cvt_pk_bf16_f32 v136, v136, v137
	v_mul_f32_e32 v137, 0x41000000, v138
	v_mul_f32_e32 v138, 0x41000000, v139
	v_mul_f32_e32 v139, 0x41000000, v140
	v_med3_f32 v137, v137, s37, v186
	v_med3_f32 v140, v138, s37, v186
	v_mov_b32_e32 v138, v171
	v_cvt_pk_fp8_f32 v138, v137, v140
	v_mul_f32_e32 v137, 0x41000000, v141
	v_med3_f32 v139, v139, s37, v186
	v_med3_f32 v137, v137, s37, v186
	v_cvt_pk_fp8_f32 v138, v139, v137 op_sel:[0,0,1]
	v_mul_f32_e32 v137, 0x41000000, v142
	v_mul_f32_e32 v139, 0x41000000, v143
	v_med3_f32 v137, v137, s37, v186
	v_med3_f32 v140, v139, s37, v186
	v_mov_b32_e32 v139, v171
	v_cvt_pk_bf16_f32 v133, v84, v85
	v_cvt_pk_fp8_f32 v139, v137, v140
	v_lshlrev_b32_e32 v144, 16, v133
	v_and_b32_e32 v145, 0xffff0000, v133
	v_pk_add_f32 v[144:145], v[84:85], v[144:145] neg_lo:[0,1] neg_hi:[0,1]
	v_mul_f32_e32 v84, 0x41000000, v84
	v_mul_f32_e32 v85, 0x41000000, v85
	v_med3_f32 v84, v84, s37, v186
	v_med3_f32 v85, v85, s37, v186
	v_cvt_pk_fp8_f32 v139, v84, v85 op_sel:[0,0,1]
	global_store_dwordx4 v167, v[130:133], s[38:39] offset:3072 nt
	v_cvt_pk_bf16_f32 v137, v144, v145
	ds_write_b128 v187, v[130:133] offset:3072
	ds_write_b128 v187, v[134:137] offset:36352
	global_store_dwordx2 v170, v[138:139], s[4:5] offset:1536
	s_add_i32 s4, s30, s28
	s_ashr_i32 s5, s4, 31
	s_lshl_b64 s[4:5], s[4:5], 12
	s_add_u32 s6, s0, s4
	s_addc_u32 s7, s1, s5
	s_add_u32 s4, s44, s4
	v_and_b32_e32 v84, 7, v0
	s_addc_u32 s5, s45, s5
	global_load_dwordx4 v[154:157], v167, s[6:7]
	global_load_dwordx4 v[146:149], v167, s[6:7] offset:1024
	global_load_dwordx4 v[158:161], v167, s[4:5]
	global_load_dwordx4 v[150:153], v167, s[4:5] offset:1024
	global_load_dwordx4 v[138:141], v167, s[6:7] offset:2048
	global_load_dwordx4 v[130:133], v167, s[6:7] offset:3072
	global_load_dwordx4 v[142:145], v167, s[4:5] offset:2048
	global_load_dwordx4 v[134:137], v167, s[4:5] offset:3072
	v_mul_u32_u24_e32 v84, 0x820, v84
	s_lshl_b32 s4, s34, 1
	v_lshlrev_b32_e32 v84, 1, v84
	s_add_i32 s4, s4, 0
	v_lshlrev_b32_e32 v85, 1, v166
	s_waitcnt lgkmcnt(0)
	s_barrier
; __device__ __forceinline__ unsigned pk2(float lo, float hi) { return cvt_pk_bf16_nat(lo, hi); }
; __global__ void __launch_bounds__(NTHR, 2) mk_fwd(Args args) {
;     ...
;                 v4u hi, lo;
;                 hi.x = pk2(w8[0], w8[1]); hi.y = pk2(w8[2], w8[3]); hi.z = pk2(w8[4], w8[5]); hi.w = pk2(w8[6], w8[7]);
;                 lo.x = pk2(w8[0] - bflo(hi.x), w8[1] - bfhi(hi.x)); lo.y = pk2(w8[2] - bflo(hi.y), w8[3] - bfhi(hi.y)); lo.z = pk2(w8[4] - bflo(hi.z), w8[5] - bfhi(hi.z)); lo.w = pk2(w8[6] - bflo(hi.w), w8[7] - bfhi(hi.w));
;                 wh[st][hf] = __builtin_bit_cast(bf16x8, hi); wl[st][hf] = __builtin_bit_cast(bf16x8, lo); }
	v_add3_u32 v197, s4, v84, v85
	ds_read_b128 v[166:169], v197
	ds_read_b128 v[198:201], v197 offset:64
	ds_read_b128 v[210:213], v197 offset:33280
	s_waitcnt lgkmcnt(2)
	v_mfma_f32_16x16x32_bf16 v[202:205], v[166:169], v[2:5], 0
	v_lshlrev_b32_e32 v84, 16, v76
	v_and_b32_e32 v85, 0xffff0000, v76
	v_pk_add_f32 v[80:81], v[80:81], v[84:85] neg_lo:[0,1] neg_hi:[0,1]
	v_mfma_f32_16x16x32_bf16 v[206:209], v[166:169], v[10:13], 0
	v_lshlrev_b32_e32 v84, 16, v77
	v_and_b32_e32 v85, 0xffff0000, v77
	v_pk_add_f32 v[82:83], v[82:83], v[84:85] neg_lo:[0,1] neg_hi:[0,1]
	v_mfma_f32_16x16x32_bf16 v[202:205], v[166:169], v[6:9], v[202:205]
	v_cvt_pk_bf16_f32 v80, v80, v81
	v_cvt_pk_bf16_f32 v81, v82, v83
	v_cvt_pk_bf16_f32 v82, v86, v87
	v_mfma_f32_16x16x32_bf16 v[166:169], v[166:169], v[14:17], v[206:209]
	v_cvt_pk_bf16_f32 v83, v88, v89
	v_lshlrev_b32_e32 v176, 16, v82
	v_and_b32_e32 v177, 0xffff0000, v82
	ds_read_b128 v[206:209], v197 offset:33344
	s_waitcnt lgkmcnt(1)
	v_mfma_f32_16x16x32_bf16 v[202:205], v[210:213], v[2:5], v[202:205]
	v_add_f32_e64 v86, v86, -v176
	v_add_f32_e64 v87, v87, -v177
	v_lshlrev_b32_e32 v176, 16, v83
	v_and_b32_e32 v177, 0xffff0000, v83
	v_mfma_f32_16x16x32_bf16 v[166:169], v[210:213], v[10:13], v[166:169]
	ds_read_b128 v[210:213], v197 offset:33408
	v_cvt_pk_bf16_f32 v84, v92, v93
	v_pk_add_f32 v[88:89], v[88:89], v[176:177] neg_lo:[0,1] neg_hi:[0,1]
	v_mfma_f32_16x16x32_bf16 v[202:205], v[198:201], v[18:21], v[202:205]
	v_cvt_pk_bf16_f32 v85, v90, v91
	v_cvt_pk_bf16_f32 v86, v86, v87
	v_cvt_pk_bf16_f32 v87, v88, v89
	v_mfma_f32_16x16x32_bf16 v[166:169], v[198:201], v[26:29], v[166:169]
	v_lshlrev_b32_e32 v88, 16, v84
	v_and_b32_e32 v89, 0xffff0000, v84
	v_pk_add_f32 v[88:89], v[92:93], v[88:89] neg_lo:[0,1] neg_hi:[0,1]
	v_mfma_f32_16x16x32_bf16 v[202:205], v[198:201], v[22:25], v[202:205]
	v_lshlrev_b32_e32 v92, 16, v85
	v_and_b32_e32 v93, 0xffff0000, v85
	v_pk_add_f32 v[90:91], v[90:91], v[92:93] neg_lo:[0,1] neg_hi:[0,1]
	v_mfma_f32_16x16x32_bf16 v[166:169], v[198:201], v[30:33], v[166:169]
	ds_read_b128 v[198:201], v197 offset:128
	v_cvt_pk_bf16_f32 v88, v88, v89
	v_cvt_pk_bf16_f32 v89, v90, v91
	s_waitcnt lgkmcnt(2)
	v_mfma_f32_16x16x32_bf16 v[202:205], v[206:209], v[18:21], v[202:205]
	v_cvt_pk_bf16_f32 v90, v94, v95
	v_cvt_pk_bf16_f32 v91, v100, v101
	v_lshlrev_b32_e32 v176, 16, v90
	v_mfma_f32_16x16x32_bf16 v[166:169], v[206:209], v[26:29], v[166:169]
	ds_read_b128 v[206:209], v197 offset:192
	v_and_b32_e32 v177, 0xffff0000, v90
	v_pk_add_f32 v[94:95], v[94:95], v[176:177] neg_lo:[0,1] neg_hi:[0,1]
	s_waitcnt lgkmcnt(1)
	v_mfma_f32_16x16x32_bf16 v[202:205], v[198:201], v[34:37], v[202:205]
	v_lshlrev_b32_e32 v176, 16, v91
	v_and_b32_e32 v177, 0xffff0000, v91
	v_cvt_pk_bf16_f32 v92, v96, v97
	v_mfma_f32_16x16x32_bf16 v[166:169], v[198:201], v[42:45], v[166:169]
	v_add_f32_e64 v100, v100, -v176
	v_add_f32_e64 v101, v101, -v177
	v_cvt_pk_bf16_f32 v93, v98, v99
	v_cvt_pk_bf16_f32 v94, v94, v95
	v_mfma_f32_16x16x32_bf16 v[202:205], v[198:201], v[38:41], v[202:205]
	v_cvt_pk_bf16_f32 v95, v100, v101
	v_lshlrev_b32_e32 v100, 16, v92
	v_and_b32_e32 v101, 0xffff0000, v92
	v_mfma_f32_16x16x32_bf16 v[166:169], v[198:201], v[46:49], v[166:169]
	ds_read_b128 v[198:201], v197 offset:33472
	v_pk_add_f32 v[96:97], v[96:97], v[100:101] neg_lo:[0,1] neg_hi:[0,1]
	v_lshlrev_b32_e32 v100, 16, v93
	v_mfma_f32_16x16x32_bf16 v[202:205], v[210:213], v[34:37], v[202:205]
	v_and_b32_e32 v101, 0xffff0000, v93
	v_pk_add_f32 v[98:99], v[98:99], v[100:101] neg_lo:[0,1] neg_hi:[0,1]
	v_cvt_pk_bf16_f32 v96, v96, v97
	v_mfma_f32_16x16x32_bf16 v[166:169], v[210:213], v[42:45], v[166:169]
	ds_read_b128 v[210:213], v197 offset:33536
	v_cvt_pk_bf16_f32 v97, v98, v99
	v_cvt_pk_bf16_f32 v98, v102, v103
	s_waitcnt lgkmcnt(2)
	v_mfma_f32_16x16x32_bf16 v[202:205], v[206:209], v[50:53], v[202:205]
	v_cvt_pk_bf16_f32 v99, v104, v105
	v_lshlrev_b32_e32 v176, 16, v98
	v_and_b32_e32 v177, 0xffff0000, v98
	v_mfma_f32_16x16x32_bf16 v[166:169], v[206:209], v[58:61], v[166:169]
	v_add_f32_e64 v102, v102, -v176
	v_add_f32_e64 v103, v103, -v177
	v_lshlrev_b32_e32 v176, 16, v99
	v_and_b32_e32 v177, 0xffff0000, v99
	v_mfma_f32_16x16x32_bf16 v[202:205], v[206:209], v[54:57], v[202:205]
	v_cvt_pk_bf16_f32 v100, v108, v109
	v_pk_add_f32 v[104:105], v[104:105], v[176:177] neg_lo:[0,1] neg_hi:[0,1]
	v_cvt_pk_bf16_f32 v101, v106, v107
	v_mfma_f32_16x16x32_bf16 v[166:169], v[206:209], v[62:65], v[166:169]
	ds_read_b128 v[206:209], v197 offset:256
	v_cvt_pk_bf16_f32 v102, v102, v103
	v_cvt_pk_bf16_f32 v103, v104, v105
	s_waitcnt lgkmcnt(2)
	v_mfma_f32_16x16x32_bf16 v[202:205], v[198:201], v[50:53], v[202:205]
	v_lshlrev_b32_e32 v104, 16, v100
	v_and_b32_e32 v105, 0xffff0000, v100
	v_pk_add_f32 v[104:105], v[108:109], v[104:105] neg_lo:[0,1] neg_hi:[0,1]
	v_mfma_f32_16x16x32_bf16 v[166:169], v[198:201], v[58:61], v[166:169]
	ds_read_b128 v[198:201], v197 offset:320
	v_lshlrev_b32_e32 v108, 16, v101
	v_and_b32_e32 v109, 0xffff0000, v101
	s_waitcnt lgkmcnt(1)
	v_mfma_f32_16x16x32_bf16 v[202:205], v[206:209], v[66:69], v[202:205]
	v_add_f32_e64 v106, v106, -v108
	v_add_f32_e64 v107, v107, -v109
	v_cvt_pk_bf16_f32 v104, v104, v105
	v_cvt_pk_bf16_f32 v105, v106, v107
	v_mfma_f32_16x16x32_bf16 v[166:169], v[206:209], v[74:77], v[166:169]
	v_cvt_pk_bf16_f32 v106, v110, v111
	v_cvt_pk_bf16_f32 v107, v112, v113
	v_lshlrev_b32_e32 v176, 16, v106
	v_mfma_f32_16x16x32_bf16 v[202:205], v[206:209], v[70:73], v[202:205]
	v_and_b32_e32 v177, 0xffff0000, v106
	v_pk_add_f32 v[110:111], v[110:111], v[176:177] neg_lo:[0,1] neg_hi:[0,1]
	v_lshlrev_b32_e32 v176, 16, v107
	v_mfma_f32_16x16x32_bf16 v[166:169], v[206:209], v[78:81], v[166:169]
	ds_read_b128 v[206:209], v197 offset:33600
	v_and_b32_e32 v177, 0xffff0000, v107
	v_cvt_pk_bf16_f32 v108, v116, v117
	v_mfma_f32_16x16x32_bf16 v[202:205], v[210:213], v[66:69], v[202:205]
	v_add_f32_e64 v112, v112, -v176
	v_add_f32_e64 v113, v113, -v177
	v_cvt_pk_bf16_f32 v109, v114, v115
	v_cvt_pk_bf16_f32 v110, v110, v111
	v_mfma_f32_16x16x32_bf16 v[166:169], v[210:213], v[74:77], v[166:169]
	v_cvt_pk_bf16_f32 v111, v112, v113
	v_lshlrev_b32_e32 v112, 16, v108
	v_and_b32_e32 v113, 0xffff0000, v108
	s_waitcnt lgkmcnt(1)
	v_mfma_f32_16x16x32_bf16 v[202:205], v[198:201], v[82:85], v[202:205]
	v_add_f32_e64 v112, v116, -v112
	v_add_f32_e64 v113, v117, -v113
	v_lshlrev_b32_e32 v116, 16, v109
	v_and_b32_e32 v117, 0xffff0000, v109
	v_mfma_f32_16x16x32_bf16 v[166:169], v[198:201], v[90:93], v[166:169]
	ds_read_b128 v[210:213], v197 offset:33664
	v_pk_add_f32 v[114:115], v[114:115], v[116:117] neg_lo:[0,1] neg_hi:[0,1]
	v_cvt_pk_bf16_f32 v112, v112, v113
	v_mfma_f32_16x16x32_bf16 v[202:205], v[198:201], v[86:89], v[202:205]
	v_cvt_pk_bf16_f32 v113, v114, v115
	v_cvt_pk_bf16_f32 v114, v118, v119
	v_cvt_pk_bf16_f32 v115, v120, v121
	v_mfma_f32_16x16x32_bf16 v[166:169], v[198:201], v[94:97], v[166:169]
	ds_read_b128 v[198:201], v197 offset:384
	v_lshlrev_b32_e32 v176, 16, v114
	v_and_b32_e32 v177, 0xffff0000, v114
	s_waitcnt lgkmcnt(2)
	v_mfma_f32_16x16x32_bf16 v[202:205], v[206:209], v[82:85], v[202:205]
	v_add_f32_e64 v118, v118, -v176
	v_add_f32_e64 v119, v119, -v177
	v_lshlrev_b32_e32 v176, 16, v115
	v_and_b32_e32 v177, 0xffff0000, v115
	v_mfma_f32_16x16x32_bf16 v[166:169], v[206:209], v[90:93], v[166:169]
	ds_read_b128 v[206:209], v197 offset:448
	v_cvt_pk_bf16_f32 v116, v124, v125
	v_pk_add_f32 v[120:121], v[120:121], v[176:177] neg_lo:[0,1] neg_hi:[0,1]
	s_waitcnt lgkmcnt(1)
	v_mfma_f32_16x16x32_bf16 v[202:205], v[198:201], v[98:101], v[202:205]
	v_cvt_pk_bf16_f32 v117, v122, v123
	v_cvt_pk_bf16_f32 v118, v118, v119
	v_cvt_pk_bf16_f32 v119, v120, v121
	v_mfma_f32_16x16x32_bf16 v[166:169], v[198:201], v[106:109], v[166:169]
	v_lshlrev_b32_e32 v120, 16, v116
	v_and_b32_e32 v121, 0xffff0000, v116
	v_pk_add_f32 v[120:121], v[124:125], v[120:121] neg_lo:[0,1] neg_hi:[0,1]
	v_mfma_f32_16x16x32_bf16 v[202:205], v[198:201], v[102:105], v[202:205]
	v_lshlrev_b32_e32 v124, 16, v117
	v_and_b32_e32 v125, 0xffff0000, v117
	v_pk_add_f32 v[122:123], v[122:123], v[124:125] neg_lo:[0,1] neg_hi:[0,1]
	v_mfma_f32_16x16x32_bf16 v[166:169], v[198:201], v[110:113], v[166:169]
	v_cvt_pk_bf16_f32 v120, v120, v121
	v_cvt_pk_bf16_f32 v121, v122, v123
	v_cvt_pk_bf16_f32 v122, v126, v127
	ds_read_b128 v[198:201], v197 offset:33728
	v_mfma_f32_16x16x32_bf16 v[202:205], v[210:213], v[98:101], v[202:205]
	v_cvt_pk_bf16_f32 v123, v128, v129
	v_lshlrev_b32_e32 v176, 16, v122
	v_and_b32_e32 v177, 0xffff0000, v122
	v_mfma_f32_16x16x32_bf16 v[166:169], v[210:213], v[106:109], v[166:169]
	v_add_f32_e64 v126, v126, -v176
	v_add_f32_e64 v127, v127, -v177
	v_lshlrev_b32_e32 v176, 16, v123
	v_and_b32_e32 v177, 0xffff0000, v123
	v_cvt_pk_bf16_f32 v124, v164, v165
	v_cvt_pk_bf16_f32 v125, v162, v163
	v_pk_add_f32 v[128:129], v[128:129], v[176:177] neg_lo:[0,1] neg_hi:[0,1]
	v_cvt_pk_bf16_f32 v126, v126, v127
	s_waitcnt lgkmcnt(1)
	v_mfma_f32_16x16x32_bf16 v[202:205], v[206:209], v[114:117], v[202:205]
	v_cvt_pk_bf16_f32 v127, v128, v129
	v_lshlrev_b32_e32 v128, 16, v124
	v_and_b32_e32 v129, 0xffff0000, v124
	v_mfma_f32_16x16x32_bf16 v[166:169], v[206:209], v[122:125], v[166:169]
	v_add_f32_e64 v128, v164, -v128
	v_add_f32_e64 v129, v165, -v129
	v_lshlrev_b32_e32 v164, 16, v125
	v_and_b32_e32 v165, 0xffff0000, v125
	v_pk_add_f32 v[162:163], v[162:163], v[164:165] neg_lo:[0,1] neg_hi:[0,1]
	v_cvt_pk_bf16_f32 v128, v128, v129
	v_cvt_pk_bf16_f32 v129, v162, v163
	v_mfma_f32_16x16x32_bf16 v[202:205], v[206:209], v[118:121], v[202:205]
	v_cmp_gt_u32_e64 s[6:7], 32, v194
	s_lshl_b32 s34, s42, 3
	v_mfma_f32_16x16x32_bf16 v[166:169], v[206:209], v[126:129], v[166:169]
	s_waitcnt lgkmcnt(0)
	v_mfma_f32_16x16x32_bf16 v[162:165], v[198:201], v[114:117], v[202:205]
	v_mfma_f32_16x16x32_bf16 v[166:169], v[198:201], v[122:125], v[166:169]
	s_and_saveexec_b64 s[4:5], s[6:7]
	s_cbranch_execz .LBB0_808
	v_or_b32_e32 v174, s34, v173
	s_add_i32 s35, 0, 0x11000
	v_lshlrev_b32_e32 v174, 7, v174
	v_add3_u32 v172, s35, v172, v174
	s_nop 1
	ds_write2_b32 v172, v162, v166 offset1:16
	ds_write2_b32 v172, v163, v167 offset0:32 offset1:48
	ds_write2_b32 v172, v164, v168 offset0:64 offset1:80
	ds_write2_b32 v172, v165, v169 offset0:96 offset1:112

; #define P8_FETCH(m_) do { _Pragma("unroll") for (int q = 0; q < 4; ++q) { rm[q] = *(const GAS v4u*)(MIX + (size_t)(m_) * D + 8 * lane + 512 * q); rx[q] = *(const GAS v4u*)(XB + (size_t)(m_) * D + 8 * lane + 512 * q); } } while (0)
; __global__ void __launch_bounds__(NTHR, 2) mk_fwd(Args args) {
;     ...
;         for (int it = 1; it < NIT; ++it) {
;             const int m = mfirst + it * G * 8;
;             P8_LN(m); P8_FETCH(it + 1 < NIT ? m + G * 8 : m);
.LBB0_810:
	s_waitcnt vmcnt(5)
	v_lshlrev_b32_e32 v162, 16, v158
	v_and_b32_e32 v163, 0xffff0000, v158
	v_lshlrev_b32_e32 v158, 16, v159
	v_and_b32_e32 v159, 0xffff0000, v159
	v_lshlrev_b32_e32 v164, 16, v154
	v_and_b32_e32 v165, 0xffff0000, v154
	v_lshlrev_b32_e32 v154, 16, v155
	v_and_b32_e32 v155, 0xffff0000, v155
	v_pk_fma_f32 v[154:155], v[158:159], s[36:37], v[154:155] op_sel_hi:[1,0,1]
	v_pk_fma_f32 v[158:159], v[162:163], s[36:37], v[164:165] op_sel_hi:[1,0,1]
	v_lshlrev_b32_e32 v162, 16, v160
	v_and_b32_e32 v163, 0xffff0000, v160
	v_lshlrev_b32_e32 v160, 16, v161
	v_and_b32_e32 v161, 0xffff0000, v161
	v_lshlrev_b32_e32 v164, 16, v156
	v_and_b32_e32 v165, 0xffff0000, v156
	v_lshlrev_b32_e32 v156, 16, v157
	v_and_b32_e32 v157, 0xffff0000, v157
	v_pk_fma_f32 v[156:157], v[160:161], s[36:37], v[156:157] op_sel_hi:[1,0,1]
	v_pk_fma_f32 v[160:161], v[162:163], s[36:37], v[164:165] op_sel_hi:[1,0,1]
	v_mov_b32_e32 v162, v158
	v_mov_b32_e32 v163, v160
	v_mov_b32_e32 v164, v159
	v_mov_b32_e32 v165, v161
	v_pk_add_f32 v[162:163], v[162:163], v[164:165]
	v_mov_b32_e32 v164, v154
	v_mov_b32_e32 v165, v156
	v_mov_b32_e32 v166, v155
	v_mov_b32_e32 v167, v157
	v_pk_add_f32 v[164:165], v[164:165], v[166:167]
	v_lshlrev_b32_e32 v166, 16, v146
	v_pk_add_f32 v[162:163], v[162:163], v[164:165]
	s_waitcnt vmcnt(4)
	v_lshlrev_b32_e32 v164, 16, v150
	v_and_b32_e32 v165, 0xffff0000, v150
	v_lshlrev_b32_e32 v150, 16, v151
	v_and_b32_e32 v151, 0xffff0000, v151
	v_and_b32_e32 v167, 0xffff0000, v146
	v_lshlrev_b32_e32 v146, 16, v147
	v_and_b32_e32 v147, 0xffff0000, v147
	v_pk_fma_f32 v[146:147], v[150:151], s[36:37], v[146:147] op_sel_hi:[1,0,1]
	v_pk_fma_f32 v[150:151], v[164:165], s[36:37], v[166:167] op_sel_hi:[1,0,1]
	v_lshlrev_b32_e32 v164, 16, v152
	v_and_b32_e32 v165, 0xffff0000, v152
	v_lshlrev_b32_e32 v152, 16, v153
	v_and_b32_e32 v153, 0xffff0000, v153
	v_lshlrev_b32_e32 v166, 16, v148
	v_and_b32_e32 v167, 0xffff0000, v148
	v_lshlrev_b32_e32 v148, 16, v149
	v_and_b32_e32 v149, 0xffff0000, v149
	v_pk_fma_f32 v[148:149], v[152:153], s[36:37], v[148:149] op_sel_hi:[1,0,1]
	v_pk_fma_f32 v[152:153], v[164:165], s[36:37], v[166:167] op_sel_hi:[1,0,1]
	v_pk_mov_b32 v[164:165], v[150:151], v[146:147] op_sel:[1,0]
	v_mov_b32_e32 v166, v150
	v_mov_b32_e32 v167, v147
	v_pk_add_f32 v[164:165], v[164:165], v[166:167]
	v_pk_mov_b32 v[166:167], v[152:153], v[148:149] op_sel:[1,0]
	v_mov_b32_e32 v168, v152
	v_mov_b32_e32 v169, v149
	v_pk_add_f32 v[166:167], v[166:167], v[168:169]
	s_waitcnt vmcnt(1)
	v_lshlrev_b32_e32 v168, 16, v142
	v_and_b32_e32 v169, 0xffff0000, v142
	v_lshlrev_b32_e32 v142, 16, v143
	v_and_b32_e32 v143, 0xffff0000, v143
	v_lshlrev_b32_e32 v204, 16, v138
	v_and_b32_e32 v205, 0xffff0000, v138
	v_lshlrev_b32_e32 v138, 16, v139
	v_and_b32_e32 v139, 0xffff0000, v139
	s_waitcnt vmcnt(0)
	v_lshlrev_b32_e32 v210, 16, v134
	v_and_b32_e32 v211, 0xffff0000, v134
	v_lshlrev_b32_e32 v134, 16, v135
	v_and_b32_e32 v135, 0xffff0000, v135
	v_lshlrev_b32_e32 v212, 16, v130
	v_and_b32_e32 v213, 0xffff0000, v130
	v_lshlrev_b32_e32 v130, 16, v131
	v_and_b32_e32 v131, 0xffff0000, v131
	v_pk_add_f32 v[162:163], v[162:163], v[162:163] op_sel:[0,1] op_sel_hi:[1,0]
	v_pk_add_f32 v[164:165], v[164:165], v[164:165] op_sel:[0,1] op_sel_hi:[1,0]
	v_pk_add_f32 v[166:167], v[166:167], v[166:167] op_sel:[0,1] op_sel_hi:[1,0]
	v_pk_fma_f32 v[138:139], v[142:143], s[36:37], v[138:139] op_sel_hi:[1,0,1]
	v_pk_fma_f32 v[142:143], v[168:169], s[36:37], v[204:205] op_sel_hi:[1,0,1]
	v_lshlrev_b32_e32 v168, 16, v144
	v_and_b32_e32 v169, 0xffff0000, v144
	v_lshlrev_b32_e32 v144, 16, v145
	v_and_b32_e32 v145, 0xffff0000, v145
	v_lshlrev_b32_e32 v204, 16, v140
	v_and_b32_e32 v205, 0xffff0000, v140
	v_lshlrev_b32_e32 v140, 16, v141
	v_and_b32_e32 v141, 0xffff0000, v141
	v_pk_fma_f32 v[130:131], v[134:135], s[36:37], v[130:131] op_sel_hi:[1,0,1]
	v_pk_fma_f32 v[134:135], v[210:211], s[36:37], v[212:213] op_sel_hi:[1,0,1]
	v_lshlrev_b32_e32 v210, 16, v136
	v_and_b32_e32 v211, 0xffff0000, v136
	v_lshlrev_b32_e32 v136, 16, v137
	v_and_b32_e32 v137, 0xffff0000, v137
	v_lshlrev_b32_e32 v212, 16, v132
	v_and_b32_e32 v213, 0xffff0000, v132
	v_lshlrev_b32_e32 v132, 16, v133
	v_and_b32_e32 v133, 0xffff0000, v133
	v_pk_fma_f32 v[140:141], v[144:145], s[36:37], v[140:141] op_sel_hi:[1,0,1]
	v_pk_fma_f32 v[144:145], v[168:169], s[36:37], v[204:205] op_sel_hi:[1,0,1]
	v_pk_fma_f32 v[132:133], v[136:137], s[36:37], v[132:133] op_sel_hi:[1,0,1]
	v_pk_fma_f32 v[136:137], v[210:211], s[36:37], v[212:213] op_sel_hi:[1,0,1]
	v_mov_b32_e32 v163, v134
	v_mov_b32_e32 v173, v135
	v_mov_b32_e32 v165, v130
	v_mov_b32_e32 v167, v131
	v_add_f32_e32 v168, v142, v143
	v_add_f32_e32 v204, v138, v139
	v_add_f32_e32 v206, v144, v145
	v_add_f32_e32 v208, v140, v141
	v_pk_add_f32 v[162:163], v[162:163], v[172:173]
	v_pk_add_f32 v[164:165], v[164:165], v[166:167]
	v_mov_b32_e32 v169, v136
	v_mov_b32_e32 v205, v137
	v_mov_b32_e32 v207, v132
	v_mov_b32_e32 v209, v133
	v_pk_add_f32 v[162:163], v[162:163], v[164:165]
	v_pk_add_f32 v[164:165], v[168:169], v[204:205]
	v_pk_add_f32 v[166:167], v[206:207], v[208:209]
	s_nop 0
	v_pk_add_f32 v[164:165], v[164:165], v[166:167]
	s_nop 0
	v_pk_add_f32 v[162:163], v[162:163], v[164:165]
	s_nop 0
	v_add_f32_e32 v162, v162, v163
	v_mov_b32_e32 v163, v172
	s_nop 0
	v_add_f32_dpp v162, v162, v162 quad_perm:[1,0,3,2] row_mask:0xf bank_mask:0xf bound_ctrl:1
	s_nop 1
	v_add_f32_dpp v162, v162, v162 quad_perm:[2,3,0,1] row_mask:0xf bank_mask:0xf bound_ctrl:1
	s_nop 1
	v_add_f32_dpp v162, v162, v162 row_half_mirror row_mask:0xf bank_mask:0xf bound_ctrl:1
	s_nop 1
	v_add_f32_dpp v162, v162, v162 row_mirror row_mask:0xf bank_mask:0xf bound_ctrl:1
	s_nop 1
	v_mov_b32_dpp v163, v162 row_bcast:15 row_mask:0xa bank_mask:0xf
	v_add_f32_e32 v162, v162, v163
	v_mov_b32_e32 v163, v172
	s_nop 1
	v_mov_b32_dpp v163, v162 row_bcast:31 row_mask:0xc bank_mask:0xf
	v_add_f32_e32 v162, v162, v163
	s_nop 0
	v_readlane_b32 s1, v162, 63
	s_nop 1
	v_fmac_f32_e32 v155, s1, v180
	v_fmac_f32_e32 v159, s1, v180
	v_fma_f32 v154, s1, v180, v154
	v_fma_f32 v158, s1, v180, v158
	v_mul_f32_e32 v162, v159, v159
	v_mul_f32_e32 v163, v155, v155
	v_fmac_f32_e32 v162, v158, v158
	v_fmac_f32_e32 v163, v154, v154
	v_fmac_f32_e32 v157, s1, v180
	v_fmac_f32_e32 v161, s1, v180
	v_add_f32_e32 v162, v162, v163
	v_fma_f32 v156, s1, v180, v156
	v_fma_f32 v160, s1, v180, v160
	v_mul_f32_e32 v163, v161, v161
	v_mul_f32_e32 v164, v157, v157
	v_fmac_f32_e32 v163, v160, v160
	v_fmac_f32_e32 v164, v156, v156
	v_add_f32_e32 v163, v163, v164
	v_fmac_f32_e32 v147, s1, v180
	v_fmac_f32_e32 v151, s1, v180
	v_add_f32_e32 v162, v162, v163
	v_fma_f32 v146, s1, v180, v146
	v_fma_f32 v150, s1, v180, v150
	v_mul_f32_e32 v163, v151, v151
	v_mul_f32_e32 v164, v147, v147
	v_fmac_f32_e32 v163, v150, v150
	v_fmac_f32_e32 v164, v146, v146
	v_add_f32_e32 v163, v163, v164
	v_fmac_f32_e32 v149, s1, v180
	v_fmac_f32_e32 v153, s1, v180
	v_add_f32_e32 v162, v162, v163
	v_fma_f32 v148, s1, v180, v148
	v_fma_f32 v152, s1, v180, v152
	v_mul_f32_e32 v163, v153, v153
	v_mul_f32_e32 v164, v149, v149
	v_fmac_f32_e32 v163, v152, v152
	v_fmac_f32_e32 v164, v148, v148
	v_add_f32_e32 v163, v163, v164
	v_fmac_f32_e32 v139, s1, v180
	v_fmac_f32_e32 v143, s1, v180
	v_add_f32_e32 v162, v162, v163
	v_fma_f32 v138, s1, v180, v138
	v_fma_f32 v142, s1, v180, v142
	v_mul_f32_e32 v163, v143, v143
	v_mul_f32_e32 v164, v139, v139
	v_fmac_f32_e32 v163, v142, v142
	v_fmac_f32_e32 v164, v138, v138
	v_add_f32_e32 v163, v163, v164
	v_fmac_f32_e32 v141, s1, v180
	v_fmac_f32_e32 v145, s1, v180
	v_add_f32_e32 v162, v162, v163
	v_fma_f32 v140, s1, v180, v140
	v_fma_f32 v144, s1, v180, v144
	v_mul_f32_e32 v163, v145, v145
	v_mul_f32_e32 v164, v141, v141
	v_fmac_f32_e32 v163, v144, v144
	v_fmac_f32_e32 v164, v140, v140
	v_add_f32_e32 v163, v163, v164
	v_fmac_f32_e32 v131, s1, v180
	v_fmac_f32_e32 v135, s1, v180
	v_add_f32_e32 v162, v162, v163
	v_fma_f32 v130, s1, v180, v130
	v_fma_f32 v134, s1, v180, v134
	v_mul_f32_e32 v163, v135, v135
	v_mul_f32_e32 v164, v131, v131
	v_fmac_f32_e32 v163, v134, v134
	v_fmac_f32_e32 v164, v130, v130
	v_add_f32_e32 v163, v163, v164
	v_fmac_f32_e32 v133, s1, v180
	v_fmac_f32_e32 v137, s1, v180
	v_add_f32_e32 v162, v162, v163
	v_fma_f32 v132, s1, v180, v132
	v_fma_f32 v136, s1, v180, v136
	v_mul_f32_e32 v163, v137, v137
	v_mul_f32_e32 v164, v133, v133
	v_fmac_f32_e32 v163, v136, v136
	v_fmac_f32_e32 v164, v132, v132
	v_add_f32_e32 v163, v163, v164
	v_add_f32_e32 v162, v162, v163
	v_mov_b32_e32 v163, v172
	s_nop 0
	v_add_f32_dpp v162, v162, v162 quad_perm:[1,0,3,2] row_mask:0xf bank_mask:0xf bound_ctrl:1
	s_nop 1
	v_add_f32_dpp v162, v162, v162 quad_perm:[2,3,0,1] row_mask:0xf bank_mask:0xf bound_ctrl:1
	s_nop 1
	v_add_f32_dpp v162, v162, v162 row_half_mirror row_mask:0xf bank_mask:0xf bound_ctrl:1
	s_nop 1
	v_add_f32_dpp v162, v162, v162 row_mirror row_mask:0xf bank_mask:0xf bound_ctrl:1
	s_nop 1
	v_mov_b32_dpp v163, v162 row_bcast:15 row_mask:0xa bank_mask:0xf
	v_add_f32_e32 v162, v162, v163
	v_mov_b32_e32 v163, v172
	s_nop 1
	v_mov_b32_dpp v163, v162 row_bcast:31 row_mask:0xc bank_mask:0xf
	v_add_f32_e32 v162, v162, v163
	s_nop 0
	v_readlane_b32 s1, v162, 63
	s_nop 1
	v_fma_f32 v162, s1, v182, v181
	v_mul_f32_e32 v163, 0x4f800000, v162
	v_cmp_gt_f32_e32 vcc, s31, v162
	s_ashr_i32 s1, s0, 31
	s_lshl_b64 s[34:35], s[0:1], 12
	v_cndmask_b32_e32 v162, v162, v163, vcc
	v_sqrt_f32_e32 v163, v162
	s_nop 0
	v_add_u32_e32 v164, -1, v163
	v_fma_f32 v165, -v164, v163, v162
	v_cmp_ge_f32_e64 s[8:9], 0, v165
	v_add_u32_e32 v165, 1, v163
	s_nop 0
	v_cndmask_b32_e64 v164, v163, v164, s[8:9]
	v_fma_f32 v163, -v165, v163, v162
	v_cmp_lt_f32_e64 s[8:9], 0, v163
	s_nop 1
	v_cndmask_b32_e64 v163, v164, v165, s[8:9]
	v_mul_f32_e32 v164, 0x37800000, v163
	v_cndmask_b32_e32 v163, v163, v164, vcc
	v_cmp_class_f32_e32 vcc, v162, v183
	s_nop 1
	v_cndmask_b32_e32 v162, v163, v162, vcc
	v_div_scale_f32 v163, s[8:9], v162, v162, 1.0
	v_rcp_f32_e32 v164, v163
	s_lshl_b64 s[8:9], s[0:1], 11
	s_cmp_lg_u32 s50, 1
	s_cselect_b32 s1, s28, 0
	v_fma_f32 v165, -v163, v164, 1.0
	v_fmac_f32_e32 v164, v165, v164
	v_div_scale_f32 v165, vcc, 1.0, v162, 1.0
	v_mul_f32_e32 v166, v165, v164
	v_fma_f32 v167, -v163, v166, v165
	v_fmac_f32_e32 v166, v167, v164
	v_fma_f32 v163, -v163, v166, v165
	v_div_fmas_f32 v163, v163, v164, v166
	ds_read_b128 v[164:167], v184
	ds_read_b128 v[204:207], v185
	ds_read_b128 v[208:211], v184 offset:16
	ds_read_b128 v[212:215], v185 offset:16
	v_div_fixup_f32 v162, v163, v162, 1.0
	v_pk_mul_f32 v[154:155], v[162:163], v[154:155] op_sel_hi:[0,1]
	v_pk_mul_f32 v[158:159], v[162:163], v[158:159] op_sel_hi:[0,1]
	s_waitcnt lgkmcnt(2)
	v_pk_fma_f32 v[168:169], v[154:155], v[166:167], v[206:207]
	v_pk_mul_f32 v[156:157], v[162:163], v[156:157] op_sel_hi:[0,1]
	v_pk_fma_f32 v[204:205], v[158:159], v[164:165], v[204:205]
	v_pk_mul_f32 v[154:155], v[162:163], v[160:161] op_sel_hi:[0,1]
	s_waitcnt lgkmcnt(0)
	v_pk_fma_f32 v[160:161], v[156:157], v[210:211], v[214:215]
	v_cvt_pk_bf16_f32 v157, v168, v169
	v_lshlrev_b32_e32 v166, 16, v157
	v_and_b32_e32 v167, 0xffff0000, v157
	v_mul_f32_e32 v163, 0x41000000, v204
	v_mul_f32_e32 v173, 0x41000000, v205
	v_pk_add_f32 v[166:167], v[168:169], v[166:167] neg_lo:[0,1] neg_hi:[0,1]
	v_mul_f32_e32 v203, 0x41000000, v168
	v_med3_f32 v163, v163, s37, v186
	v_med3_f32 v173, v173, s37, v186
	v_mov_b32_e32 v168, v172
	v_cvt_pk_fp8_f32 v168, v163, v173
	v_mul_f32_e32 v163, 0x41000000, v169
	v_pk_fma_f32 v[206:207], v[154:155], v[208:209], v[212:213]
	v_med3_f32 v169, v203, s37, v186
	v_med3_f32 v163, v163, s37, v186
	v_cvt_pk_fp8_f32 v168, v169, v163 op_sel:[0,0,1]
	v_mul_f32_e32 v163, 0x41000000, v206
	v_mul_f32_e32 v169, 0x41000000, v207
	v_med3_f32 v163, v163, s37, v186
	v_med3_f32 v173, v169, s37, v186
	v_mov_b32_e32 v169, v172
	v_cvt_pk_bf16_f32 v159, v160, v161
	v_cvt_pk_fp8_f32 v169, v163, v173
	v_lshlrev_b32_e32 v208, 16, v159
	v_and_b32_e32 v209, 0xffff0000, v159
	v_cvt_pk_bf16_f32 v156, v204, v205
	v_pk_add_f32 v[208:209], v[160:161], v[208:209] neg_lo:[0,1] neg_hi:[0,1]
	v_mul_f32_e32 v160, 0x41000000, v160
	v_mul_f32_e32 v161, 0x41000000, v161
	v_lshlrev_b32_e32 v164, 16, v156
	v_and_b32_e32 v165, 0xffff0000, v156
	v_med3_f32 v160, v160, s37, v186
	v_med3_f32 v161, v161, s37, v186
	v_cvt_pk_bf16_f32 v158, v206, v207
	v_pk_add_f32 v[164:165], v[204:205], v[164:165] neg_lo:[0,1] neg_hi:[0,1]
	v_cvt_pk_fp8_f32 v169, v160, v161 op_sel:[0,0,1]
	v_cvt_pk_bf16_f32 v164, v164, v165
	v_cvt_pk_bf16_f32 v165, v166, v167
	v_lshlrev_b32_e32 v166, 16, v158
	v_and_b32_e32 v167, 0xffff0000, v158
	v_lshl_add_u64 v[154:155], v[178:179], 0, s[34:35]
	v_pk_add_f32 v[166:167], v[206:207], v[166:167] neg_lo:[0,1] neg_hi:[0,1]
	global_store_dwordx4 v[154:155], v[156:159], off nt
	v_cvt_pk_bf16_f32 v166, v166, v167
	v_cvt_pk_bf16_f32 v167, v208, v209
	ds_write_b128 v187, v[156:159]
	ds_write_b128 v187, v[164:167] offset:33280
	v_lshl_add_u64 v[156:157], v[170:171], 0, s[8:9]
	global_store_dwordx2 v[156:157], v[168:169], off
	ds_read_b128 v[158:161], v188
	ds_read_b128 v[164:167], v189
	ds_read_b128 v[204:207], v188 offset:16
	ds_read_b128 v[208:211], v189 offset:16
	v_pk_mul_f32 v[150:151], v[162:163], v[150:151] op_sel_hi:[0,1]
	v_pk_mul_f32 v[146:147], v[162:163], v[146:147] op_sel_hi:[0,1]
	v_pk_mul_f32 v[148:149], v[162:163], v[148:149] op_sel_hi:[0,1]
	s_waitcnt lgkmcnt(2)
	v_pk_fma_f32 v[160:161], v[146:147], v[160:161], v[166:167]
	v_pk_fma_f32 v[158:159], v[150:151], v[158:159], v[164:165]
	v_pk_mul_f32 v[146:147], v[162:163], v[152:153] op_sel_hi:[0,1]
	s_waitcnt lgkmcnt(0)
	v_pk_fma_f32 v[166:167], v[146:147], v[204:205], v[208:209]
	v_cvt_pk_bf16_f32 v146, v158, v159
	v_cvt_pk_bf16_f32 v147, v160, v161
	v_lshlrev_b32_e32 v150, 16, v146
	v_and_b32_e32 v151, 0xffff0000, v146
	v_lshlrev_b32_e32 v152, 16, v147
	v_and_b32_e32 v153, 0xffff0000, v147
	v_pk_fma_f32 v[164:165], v[148:149], v[206:207], v[210:211]
	v_cvt_pk_bf16_f32 v148, v166, v167
	v_pk_add_f32 v[150:151], v[158:159], v[150:151] neg_lo:[0,1] neg_hi:[0,1]
	v_pk_add_f32 v[152:153], v[160:161], v[152:153] neg_lo:[0,1] neg_hi:[0,1]
	v_cvt_pk_bf16_f32 v150, v150, v151
	v_cvt_pk_bf16_f32 v151, v152, v153
	v_lshlrev_b32_e32 v152, 16, v148
	v_and_b32_e32 v153, 0xffff0000, v148
	v_pk_add_f32 v[152:153], v[166:167], v[152:153] neg_lo:[0,1] neg_hi:[0,1]
	v_cvt_pk_bf16_f32 v149, v164, v165
	v_cvt_pk_bf16_f32 v152, v152, v153
	v_mul_f32_e32 v153, 0x41000000, v158
	v_mul_f32_e32 v158, 0x41000000, v159
	v_mul_f32_e32 v159, 0x41000000, v160
	v_med3_f32 v153, v153, s37, v186
	v_med3_f32 v160, v158, s37, v186
	v_mov_b32_e32 v158, v172
	v_cvt_pk_fp8_f32 v158, v153, v160
	v_mul_f32_e32 v153, 0x41000000, v161
	v_med3_f32 v159, v159, s37, v186
	v_med3_f32 v153, v153, s37, v186
	v_cvt_pk_fp8_f32 v158, v159, v153 op_sel:[0,0,1]
	v_mul_f32_e32 v153, 0x41000000, v166
	v_mul_f32_e32 v159, 0x41000000, v167
	v_med3_f32 v153, v153, s37, v186
	v_med3_f32 v161, v159, s37, v186
	v_mov_b32_e32 v159, v172
	v_cvt_pk_fp8_f32 v159, v153, v161
	v_mul_f32_e32 v160, 0x41000000, v164
	v_mul_f32_e32 v153, 0x41000000, v165
	v_med3_f32 v160, v160, s37, v186
	v_med3_f32 v153, v153, s37, v186
	v_cvt_pk_fp8_f32 v159, v160, v153 op_sel:[0,0,1]
	v_lshlrev_b32_e32 v168, 16, v149
	v_and_b32_e32 v169, 0xffff0000, v149
	v_pk_add_f32 v[168:169], v[164:165], v[168:169] neg_lo:[0,1] neg_hi:[0,1]
	global_store_dwordx4 v[154:155], v[146:149], off offset:1024 nt
	v_cvt_pk_bf16_f32 v153, v168, v169
	ds_write_b128 v187, v[146:149] offset:1024
	ds_write_b128 v187, v[150:153] offset:34304
	global_store_dwordx2 v[156:157], v[158:159], off offset:512
	ds_read_b128 v[146:149], v190
	ds_read_b128 v[150:153], v191
	ds_read_b128 v[158:161], v190 offset:16
	ds_read_b128 v[164:167], v191 offset:16
	v_pk_mul_f32 v[142:143], v[162:163], v[142:143] op_sel_hi:[0,1]
	v_pk_mul_f32 v[138:139], v[162:163], v[138:139] op_sel_hi:[0,1]
	v_pk_mul_f32 v[140:141], v[162:163], v[140:141] op_sel_hi:[0,1]
	s_waitcnt lgkmcnt(2)
	v_pk_fma_f32 v[148:149], v[138:139], v[148:149], v[152:153]
	v_pk_fma_f32 v[146:147], v[142:143], v[146:147], v[150:151]
	v_pk_mul_f32 v[138:139], v[162:163], v[144:145] op_sel_hi:[0,1]
	s_waitcnt lgkmcnt(0)
	v_pk_fma_f32 v[152:153], v[138:139], v[158:159], v[164:165]
	v_cvt_pk_bf16_f32 v138, v146, v147
	v_cvt_pk_bf16_f32 v139, v148, v149
	v_lshlrev_b32_e32 v142, 16, v138
	v_and_b32_e32 v143, 0xffff0000, v138
	v_lshlrev_b32_e32 v144, 16, v139
	v_and_b32_e32 v145, 0xffff0000, v139
	v_pk_fma_f32 v[150:151], v[140:141], v[160:161], v[166:167]
	v_cvt_pk_bf16_f32 v140, v152, v153
	v_pk_add_f32 v[142:143], v[146:147], v[142:143] neg_lo:[0,1] neg_hi:[0,1]
	v_pk_add_f32 v[144:145], v[148:149], v[144:145] neg_lo:[0,1] neg_hi:[0,1]
	v_cvt_pk_bf16_f32 v142, v142, v143
	v_cvt_pk_bf16_f32 v143, v144, v145
	v_lshlrev_b32_e32 v144, 16, v140
	v_and_b32_e32 v145, 0xffff0000, v140
	v_pk_add_f32 v[144:145], v[152:153], v[144:145] neg_lo:[0,1] neg_hi:[0,1]
	v_cvt_pk_bf16_f32 v141, v150, v151
	v_cvt_pk_bf16_f32 v144, v144, v145
	v_mul_f32_e32 v145, 0x41000000, v146
	v_mul_f32_e32 v146, 0x41000000, v147
	v_mul_f32_e32 v147, 0x41000000, v148
	v_med3_f32 v145, v145, s37, v186
	v_med3_f32 v148, v146, s37, v186
	v_mov_b32_e32 v146, v172
	v_cvt_pk_fp8_f32 v146, v145, v148
	v_mul_f32_e32 v145, 0x41000000, v149
	v_med3_f32 v147, v147, s37, v186
	v_med3_f32 v145, v145, s37, v186
	v_cvt_pk_fp8_f32 v146, v147, v145 op_sel:[0,0,1]
	v_mul_f32_e32 v145, 0x41000000, v152
	v_mul_f32_e32 v147, 0x41000000, v153
	v_med3_f32 v145, v145, s37, v186
	v_med3_f32 v149, v147, s37, v186
	v_mov_b32_e32 v147, v172
	v_cvt_pk_fp8_f32 v147, v145, v149
	v_mul_f32_e32 v148, 0x41000000, v150
	v_mul_f32_e32 v145, 0x41000000, v151
	v_med3_f32 v148, v148, s37, v186
	v_med3_f32 v145, v145, s37, v186
	v_cvt_pk_fp8_f32 v147, v148, v145 op_sel:[0,0,1]
	v_lshlrev_b32_e32 v158, 16, v141
	v_and_b32_e32 v159, 0xffff0000, v141
	v_pk_add_f32 v[158:159], v[150:151], v[158:159] neg_lo:[0,1] neg_hi:[0,1]
	global_store_dwordx4 v[154:155], v[138:141], off offset:2048 nt
	v_cvt_pk_bf16_f32 v145, v158, v159
	ds_write_b128 v187, v[138:141] offset:2048
	ds_write_b128 v187, v[142:145] offset:35328
	global_store_dwordx2 v[156:157], v[146:147], off offset:1024
	ds_read_b128 v[138:141], v193
	ds_read_b128 v[142:145], v196
	ds_read_b128 v[146:149], v193 offset:16
	ds_read_b128 v[150:153], v196 offset:16
	v_pk_mul_f32 v[134:135], v[162:163], v[134:135] op_sel_hi:[0,1]
	v_pk_mul_f32 v[130:131], v[162:163], v[130:131] op_sel_hi:[0,1]
	v_pk_mul_f32 v[132:133], v[162:163], v[132:133] op_sel_hi:[0,1]
	s_waitcnt lgkmcnt(2)
	v_pk_fma_f32 v[168:169], v[130:131], v[140:141], v[144:145]
	v_pk_fma_f32 v[166:167], v[134:135], v[138:139], v[142:143]
	v_pk_mul_f32 v[130:131], v[162:163], v[136:137] op_sel_hi:[0,1]
	s_waitcnt lgkmcnt(0)
	v_pk_fma_f32 v[206:207], v[130:131], v[146:147], v[150:151]
	v_mul_f32_e32 v130, 0x41000000, v166
	v_mul_f32_e32 v131, 0x41000000, v167
	v_pk_fma_f32 v[204:205], v[132:133], v[148:149], v[152:153]
	v_med3_f32 v133, v130, s37, v186
	v_med3_f32 v131, v131, s37, v186
	v_mov_b32_e32 v130, v172
	v_cvt_pk_fp8_f32 v130, v133, v131
	v_mul_f32_e32 v132, 0x41000000, v168
	v_mul_f32_e32 v131, 0x41000000, v169
	v_med3_f32 v132, v132, s37, v186
	v_med3_f32 v131, v131, s37, v186
	v_cvt_pk_fp8_f32 v130, v132, v131 op_sel:[0,0,1]
	v_mul_f32_e32 v131, 0x41000000, v206
	v_mul_f32_e32 v132, 0x41000000, v207
	v_med3_f32 v134, v131, s37, v186
	v_med3_f32 v132, v132, s37, v186
	v_mov_b32_e32 v131, v172
	v_cvt_pk_fp8_f32 v131, v134, v132
	v_mul_f32_e32 v133, 0x41000000, v204
	v_mul_f32_e32 v132, 0x41000000, v205
	v_med3_f32 v133, v133, s37, v186
	v_med3_f32 v132, v132, s37, v186
	v_cvt_pk_fp8_f32 v131, v133, v132 op_sel:[0,0,1]
	s_add_i32 s8, s1, s0
	s_ashr_i32 s9, s8, 31
	v_cvt_pk_bf16_f32 v162, v166, v167
	v_cvt_pk_bf16_f32 v163, v168, v169
	v_cvt_pk_bf16_f32 v164, v206, v207
	v_cvt_pk_bf16_f32 v165, v204, v205
	s_lshl_b64 s[8:9], s[8:9], 12
	global_store_dwordx4 v[154:155], v[162:165], off offset:3072 nt
	global_store_dwordx2 v[156:157], v[130:131], off offset:1536
	v_lshl_add_u64 v[130:131], v[174:175], 0, s[8:9]
	v_lshl_add_u64 v[134:135], v[176:177], 0, s[8:9]
	global_load_dwordx4 v[154:157], v[130:131], off
	global_load_dwordx4 v[146:149], v[130:131], off offset:1024
	global_load_dwordx4 v[158:161], v[134:135], off
	global_load_dwordx4 v[150:153], v[134:135], off offset:1024
	global_load_dwordx4 v[138:141], v[130:131], off offset:2048
	s_nop 0
	global_load_dwordx4 v[130:133], v[130:131], off offset:3072
	s_nop 0
	global_load_dwordx4 v[142:145], v[134:135], off offset:2048
	s_nop 0
	global_load_dwordx4 v[134:137], v[134:135], off offset:3072
	v_lshlrev_b32_e32 v208, 16, v162
	v_and_b32_e32 v209, 0xffff0000, v162
	v_pk_add_f32 v[166:167], v[166:167], v[208:209] neg_lo:[0,1] neg_hi:[0,1]
	v_lshlrev_b32_e32 v208, 16, v163
	v_and_b32_e32 v209, 0xffff0000, v163
	v_pk_add_f32 v[168:169], v[168:169], v[208:209] neg_lo:[0,1] neg_hi:[0,1]
	v_cvt_pk_bf16_f32 v166, v166, v167
	v_cvt_pk_bf16_f32 v167, v168, v169
	v_lshlrev_b32_e32 v168, 16, v164
	v_and_b32_e32 v169, 0xffff0000, v164
	v_pk_add_f32 v[168:169], v[206:207], v[168:169] neg_lo:[0,1] neg_hi:[0,1]
	v_lshlrev_b32_e32 v206, 16, v165
	v_and_b32_e32 v207, 0xffff0000, v165
	v_pk_add_f32 v[204:205], v[204:205], v[206:207] neg_lo:[0,1] neg_hi:[0,1]
	v_cvt_pk_bf16_f32 v168, v168, v169
	v_cvt_pk_bf16_f32 v169, v204, v205
	ds_write_b128 v187, v[162:165] offset:3072
	ds_write_b128 v187, v[166:169] offset:36352
	v_mov_b32_e32 v165, 0xff61b1e6
	s_and_saveexec_b64 s[8:9], s[6:7]
	s_cbranch_execz .LBB0_812
	ds_read2st64_b32 v[162:163], v198 offset1:4
	ds_read2st64_b32 v[164:165], v198 offset0:16 offset1:20
	ds_read2st64_b32 v[166:167], v198 offset0:8 offset1:12
	ds_read2st64_b32 v[168:169], v198 offset0:24 offset1:28
	s_waitcnt lgkmcnt(3)
	v_mov_b32_e32 v204, v162
	s_waitcnt lgkmcnt(2)
	v_mov_b32_e32 v205, v164
	v_mov_b32_e32 v164, v163
	v_pk_add_f32 v[162:163], v[204:205], v[164:165]
	s_waitcnt lgkmcnt(1)
	v_mov_b32_e32 v164, v166
	s_waitcnt lgkmcnt(0)
	v_mov_b32_e32 v165, v168
	v_mov_b32_e32 v168, v167
	v_pk_add_f32 v[164:165], v[164:165], v[168:169]
	s_nop 0
	v_pk_add_f32 v[162:163], v[162:163], v[164:165]
	s_nop 0
	v_add_f32_e32 v162, v162, v163
	v_add_f32_e32 v162, v1, v162
	v_max_f32_e32 v163, 0xf149f2ca, v162
	v_min_f32_e32 v163, 0x7149f2ca, v163
	v_cmp_o_f32_e32 vcc, v162, v162
	s_nop 1
	v_cndmask_b32_e32 v165, v201, v163, vcc

; #define GAS __attribute__((address_space(1)))
; __global__ void __launch_bounds__(NTHR, 2) mk_fwd(Args args) {
;     ...
;         for (int m = gw; m < M; m += NGW) {
;             int sl[4]; float gt[4];
; #pragma unroll
;             for (int k = 0; k < 4; ++k) { sl[k] = nsl[k]; gt[k] = ngt[k]; }
;             { const int mn = m + NGW < M ? m + NGW : m;
; #pragma unroll
;               for (int k = 0; k < 4; ++k) { nsl[k] = SLOT_OF[mn * 4 + k]; ngt[k] = GATE[mn * 4 + k]; } }
;             f32x4 v[8]; float s = 0.f;
; #pragma unroll
;             for (int q = 0; q < 8; ++q) { const int c = 4 * lane + 256 * q; f32x4 f = (f32x4){0.f, 0.f, 0.f, 0.f};
; #pragma unroll
;                 for (int k = 0; k < 4; ++k) { const unsigned yv = *(const GAS unsigned*)(YS + (size_t)sl[k] * D + c); const f32x2n lo2 = __builtin_amdgcn_cvt_pk_f32_fp8(yv, false), hi2 = __builtin_amdgcn_cvt_pk_f32_fp8(yv, true); f += (gt[k] * (1.0f / pg8::YS_SCALE)) * (f32x4){lo2.x, lo2.y, hi2.x, hi2.y}; }
;                 { const v2u hw = *(const GAS v2u*)(H + (size_t)m * D + c); v[q] = ALPHA * (f32x4){bflo(hw.x), bfhi(hw.x), bflo(hw.y), bfhi(hw.y)} + f; } s += (v[q].x + v[q].y) + (v[q].z + v[q].w); }
.LBB0_1219:
	s_waitcnt vmcnt(0)
	v_ashrrev_i32_e32 v97, 31, v64
	v_mov_b32_e32 v96, v64
	v_ashrrev_i32_e32 v99, 31, v65
	v_mov_b32_e32 v98, v65
	v_ashrrev_i32_e32 v101, 31, v66
	v_mov_b32_e32 v100, v66
	v_ashrrev_i32_e32 v103, 31, v67
	v_mov_b32_e32 v102, v67
	v_lshlrev_b64 v[96:97], 11, v[96:97]
	v_lshlrev_b64 v[98:99], 11, v[98:99]
	v_lshlrev_b64 v[100:101], 11, v[100:101]
	v_lshlrev_b64 v[102:103], 11, v[102:103]
	v_lshl_add_u64 v[124:125], v[74:75], 0, v[96:97]
	v_lshl_add_u64 v[96:97], s[8:9], 0, v[96:97]
	v_mul_f32_e32 v94, 0x3d800000, v68
	v_mul_f32_e32 v92, 0x3d800000, v69
	v_mul_f32_e32 v64, 0x3d800000, v70
	v_mul_f32_e32 v68, 0x3d800000, v71
	global_load_dwordx2 v[66:67], v[90:91], off
	global_load_dwordx2 v[70:71], v[90:91], off offset:512
	global_load_dwordx2 v[104:105], v[90:91], off offset:1024
	global_load_dwordx2 v[108:109], v[90:91], off offset:1536
	global_load_dwordx2 v[110:111], v[90:91], off offset:2048
	global_load_dwordx2 v[112:113], v[90:91], off offset:2560
	global_load_dwordx2 v[114:115], v[90:91], off offset:3072
	global_load_dwordx2 v[116:117], v[90:91], off offset:3584
	v_lshl_add_u64 v[126:127], v[74:75], 0, v[98:99]
	v_lshl_add_u64 v[128:129], v[74:75], 0, v[100:101]
	v_lshl_add_u64 v[130:131], v[74:75], 0, v[102:103]
	global_load_dword v65, v[124:125], off
	global_load_dword v69, v[126:127], off
	global_load_dword v172, v[128:129], off
	global_load_dword v173, v[130:131], off
	v_lshl_add_u64 v[124:125], v[96:97], 0, v[72:73]
	s_add_i32 s0, s30, s28
	global_load_dword v174, v[124:125], off
	s_cmpk_lt_i32 s0, 0x4000
	s_cselect_b64 s[2:3], -1, 0
	s_and_b64 s[16:17], s[2:3], exec
	s_cselect_b32 s1, s0, s30
	v_lshl_add_u64 v[98:99], s[8:9], 0, v[98:99]
	s_mov_b32 s30, s0
	s_lshl_b32 s0, s1, 2
	v_lshl_add_u64 v[100:101], s[8:9], 0, v[100:101]
	v_lshl_add_u64 v[102:103], s[8:9], 0, v[102:103]
	v_lshl_add_u64 v[126:127], v[98:99], 0, v[72:73]
	s_ashr_i32 s1, s0, 31
	v_lshl_add_u64 v[128:129], v[100:101], 0, v[72:73]
	v_lshl_add_u64 v[130:131], v[102:103], 0, v[72:73]
	v_lshl_add_u64 v[132:133], v[96:97], 0, v[76:77]
	v_lshl_add_u64 v[134:135], v[98:99], 0, v[76:77]
	v_lshl_add_u64 v[136:137], v[100:101], 0, v[76:77]
	v_lshl_add_u64 v[138:139], v[102:103], 0, v[76:77]
	v_lshl_add_u64 v[140:141], v[96:97], 0, v[78:79]
	v_lshl_add_u64 v[142:143], v[98:99], 0, v[78:79]
	v_lshl_add_u64 v[144:145], v[100:101], 0, v[78:79]
	v_lshl_add_u64 v[146:147], v[102:103], 0, v[78:79]
	v_lshl_add_u64 v[148:149], v[96:97], 0, v[80:81]
	v_lshl_add_u64 v[150:151], v[98:99], 0, v[80:81]
	v_lshl_add_u64 v[152:153], v[100:101], 0, v[80:81]
	v_lshl_add_u64 v[154:155], v[102:103], 0, v[80:81]
	v_lshl_add_u64 v[156:157], v[96:97], 0, v[82:83]
	v_lshl_add_u64 v[158:159], v[98:99], 0, v[82:83]
	v_lshl_add_u64 v[160:161], v[100:101], 0, v[82:83]
	v_lshl_add_u64 v[162:163], v[102:103], 0, v[82:83]
	v_lshl_add_u64 v[164:165], v[96:97], 0, v[84:85]
	v_lshl_add_u64 v[166:167], v[98:99], 0, v[84:85]
	v_lshl_add_u64 v[168:169], v[100:101], 0, v[84:85]
	v_lshl_add_u64 v[170:171], v[102:103], 0, v[84:85]
	v_lshl_add_u64 v[96:97], v[96:97], 0, v[86:87]
	v_lshl_add_u64 v[98:99], v[98:99], 0, v[86:87]
	v_lshl_add_u64 v[100:101], v[100:101], 0, v[86:87]
	v_lshl_add_u64 v[102:103], v[102:103], 0, v[86:87]
	global_load_dword v175, v[126:127], off
	global_load_dword v176, v[128:129], off
	global_load_dword v177, v[130:131], off
	global_load_dword v178, v[132:133], off
	global_load_dword v179, v[134:135], off
	global_load_dword v182, v[136:137], off
	global_load_dword v186, v[138:139], off
	global_load_dword v190, v[140:141], off
	global_load_dword v194, v[142:143], off
	global_load_dword v198, v[144:145], off
	global_load_dword v202, v[146:147], off
	global_load_dword v206, v[148:149], off
	global_load_dword v210, v[150:151], off
	global_load_dword v214, v[152:153], off
	global_load_dword v218, v[154:155], off
	global_load_dword v222, v[156:157], off
	global_load_dword v226, v[158:159], off
	global_load_dword v230, v[160:161], off
	global_load_dword v234, v[162:163], off
	global_load_dword v238, v[164:165], off
	global_load_dword v242, v[166:167], off
	global_load_dword v246, v[168:169], off
	global_load_dword v248, v[170:171], off
	global_load_dword v244, v[96:97], off
	global_load_dword v249, v[98:99], off
	global_load_dword v250, v[100:101], off
	global_load_dword v251, v[102:103], off
	s_lshl_b64 s[0:1], s[0:1], 2
	s_add_u32 s16, s4, s0
	s_addc_u32 s17, s5, s1
	global_load_dwordx4 v[96:99], v73, s[16:17]
	s_add_u32 s18, s66, s0
	s_addc_u32 s19, s67, s1
	global_load_dwordx4 v[100:103], v73, s[18:19]
	v_mov_b32_e32 v120, 0
	v_mov_b32_e32 v121, 0
	s_and_b64 s[0:1], s[2:3], exec
	v_mov_b32_e32 v122, 0
	v_mov_b32_e32 v123, 0
	v_add_co_u32_e32 v106, vcc, s14, v88
	v_lshl_add_u64 v[90:91], v[90:91], 0, s[10:11]
	s_nop 0
	v_addc_co_u32_e32 v107, vcc, -1, v89, vcc
	s_waitcnt vmcnt(41)
	v_lshlrev_b32_e32 v124, 16, v66
	v_and_b32_e32 v125, 0xffff0000, v66
	v_lshlrev_b32_e32 v126, 16, v67
	v_and_b32_e32 v127, 0xffff0000, v67
	s_waitcnt vmcnt(40)
	v_lshlrev_b32_e32 v128, 16, v70
	v_and_b32_e32 v129, 0xffff0000, v70
	v_lshlrev_b32_e32 v70, 16, v71
	v_and_b32_e32 v71, 0xffff0000, v71
	s_waitcnt vmcnt(33)
	v_cvt_pk_f32_fp8_e32 v[66:67], v65
	v_cvt_pk_f32_fp8_sdwa v[142:143], v65 src0_sel:WORD_1
	s_waitcnt vmcnt(32)
	v_cvt_pk_f32_fp8_e32 v[144:145], v69
	v_cvt_pk_f32_fp8_sdwa v[146:147], v69 src0_sel:WORD_1
	s_waitcnt vmcnt(31)
	v_cvt_pk_f32_fp8_e32 v[148:149], v172
	v_cvt_pk_f32_fp8_sdwa v[150:151], v172 src0_sel:WORD_1
	s_waitcnt vmcnt(29)
; #define GAS __attribute__((address_space(1)))
; __global__ void __launch_bounds__(NTHR, 2) mk_fwd(Args args) {
;     ...
;             for (int q = 0; q < 8; ++q) { const int c = 4 * lane + 256 * q; f32x4 f = (f32x4){0.f, 0.f, 0.f, 0.f};
; #pragma unroll
;                 for (int k = 0; k < 4; ++k) { const unsigned yv = *(const GAS unsigned*)(YS + (size_t)sl[k] * D + c); const f32x2n lo2 = __builtin_amdgcn_cvt_pk_f32_fp8(yv, false), hi2 = __builtin_amdgcn_cvt_pk_f32_fp8(yv, true); f += (gt[k] * (1.0f / pg8::YS_SCALE)) * (f32x4){lo2.x, lo2.y, hi2.x, hi2.y}; }
;                 { const v2u hw = *(const GAS v2u*)(H + (size_t)m * D + c); v[q] = ALPHA * (f32x4){bflo(hw.x), bfhi(hw.x), bflo(hw.y), bfhi(hw.y)} + f; } s += (v[q].x + v[q].y) + (v[q].z + v[q].w); }
	v_cvt_pk_f32_fp8_e32 v[156:157], v174
	v_cvt_pk_f32_fp8_e32 v[152:153], v173
	v_cvt_pk_f32_fp8_sdwa v[154:155], v173 src0_sel:WORD_1
	v_cvt_pk_f32_fp8_sdwa v[158:159], v174 src0_sel:WORD_1
	v_pk_fma_f32 v[66:67], v[66:67], v[94:95], 0 op_sel_hi:[1,0,0]
	v_pk_fma_f32 v[142:143], v[142:143], v[94:95], 0 op_sel_hi:[1,0,0]
	v_pk_fma_f32 v[66:67], v[144:145], v[92:93], v[66:67] op_sel_hi:[1,0,1]
	v_pk_fma_f32 v[142:143], v[146:147], v[92:93], v[142:143] op_sel_hi:[1,0,1]
	v_pk_fma_f32 v[156:157], v[156:157], v[94:95], 0 op_sel_hi:[1,0,0]
	v_pk_fma_f32 v[158:159], v[158:159], v[94:95], 0 op_sel_hi:[1,0,0]
	v_pk_fma_f32 v[142:143], v[150:151], v[64:65], v[142:143] op_sel_hi:[1,0,1]
	v_pk_fma_f32 v[66:67], v[148:149], v[64:65], v[66:67] op_sel_hi:[1,0,1]
	s_waitcnt vmcnt(28)
	v_cvt_pk_f32_fp8_e32 v[160:161], v175
	v_cvt_pk_f32_fp8_sdwa v[162:163], v175 src0_sel:WORD_1
	s_waitcnt vmcnt(27)
	v_cvt_pk_f32_fp8_e32 v[164:165], v176
	s_waitcnt vmcnt(25)
	v_cvt_pk_f32_fp8_e32 v[172:173], v178
	v_cvt_pk_f32_fp8_sdwa v[166:167], v176 src0_sel:WORD_1
	v_cvt_pk_f32_fp8_e32 v[168:169], v177
	v_cvt_pk_f32_fp8_sdwa v[170:171], v177 src0_sel:WORD_1
	s_waitcnt vmcnt(24)
	v_cvt_pk_f32_fp8_e32 v[176:177], v179
	v_cvt_pk_f32_fp8_sdwa v[174:175], v178 src0_sel:WORD_1
	v_cvt_pk_f32_fp8_sdwa v[178:179], v179 src0_sel:WORD_1
	s_waitcnt vmcnt(21)
	v_cvt_pk_f32_fp8_e32 v[188:189], v190
	v_cvt_pk_f32_fp8_sdwa v[190:191], v190 src0_sel:WORD_1
	s_waitcnt vmcnt(17)
	v_cvt_pk_f32_fp8_e32 v[204:205], v206
	v_cvt_pk_f32_fp8_sdwa v[206:207], v206 src0_sel:WORD_1
	v_cvt_pk_f32_fp8_e32 v[192:193], v194
	s_waitcnt vmcnt(13)
	v_cvt_pk_f32_fp8_e32 v[220:221], v222
	v_cvt_pk_f32_fp8_sdwa v[222:223], v222 src0_sel:WORD_1
	v_cvt_pk_f32_fp8_sdwa v[194:195], v194 src0_sel:WORD_1
	v_cvt_pk_f32_fp8_e32 v[208:209], v210
	s_waitcnt vmcnt(9)
	v_cvt_pk_f32_fp8_e32 v[236:237], v238
	v_cvt_pk_f32_fp8_sdwa v[238:239], v238 src0_sel:WORD_1
	v_cvt_pk_f32_fp8_sdwa v[210:211], v210 src0_sel:WORD_1
	v_cvt_pk_f32_fp8_e32 v[224:225], v226
	s_waitcnt vmcnt(5)
	v_cvt_pk_f32_fp8_e32 v[144:145], v244
	v_cvt_pk_f32_fp8_sdwa v[146:147], v244 src0_sel:WORD_1
	v_cvt_pk_f32_fp8_sdwa v[226:227], v226 src0_sel:WORD_1
	v_cvt_pk_f32_fp8_e32 v[240:241], v242
	v_cvt_pk_f32_fp8_sdwa v[242:243], v242 src0_sel:WORD_1
	v_pk_fma_f32 v[172:173], v[172:173], v[94:95], 0 op_sel_hi:[1,0,0]
	v_cvt_pk_f32_fp8_e32 v[150:151], v248
	v_cvt_pk_f32_fp8_sdwa v[148:149], v248 src0_sel:WORD_1
	v_pk_fma_f32 v[156:157], v[160:161], v[92:93], v[156:157] op_sel_hi:[1,0,1]
	s_waitcnt vmcnt(4)
	v_cvt_pk_f32_fp8_e32 v[160:161], v249
	v_cvt_pk_f32_fp8_sdwa v[248:249], v249 src0_sel:WORD_1
	v_cvt_pk_f32_fp8_e32 v[180:181], v182
	v_cvt_pk_f32_fp8_sdwa v[182:183], v182 src0_sel:WORD_1
	v_cvt_pk_f32_fp8_e32 v[196:197], v198
	v_cvt_pk_f32_fp8_sdwa v[198:199], v198 src0_sel:WORD_1
	v_cvt_pk_f32_fp8_e32 v[212:213], v214
	v_cvt_pk_f32_fp8_sdwa v[214:215], v214 src0_sel:WORD_1
	v_cvt_pk_f32_fp8_e32 v[228:229], v230
	v_cvt_pk_f32_fp8_sdwa v[230:231], v230 src0_sel:WORD_1
	v_cvt_pk_f32_fp8_e32 v[244:245], v246
	v_cvt_pk_f32_fp8_sdwa v[246:247], v246 src0_sel:WORD_1
	v_pk_fma_f32 v[158:159], v[162:163], v[92:93], v[158:159] op_sel_hi:[1,0,1]
	s_waitcnt vmcnt(3)
	v_cvt_pk_f32_fp8_e32 v[162:163], v250
	v_pk_fma_f32 v[172:173], v[176:177], v[92:93], v[172:173] op_sel_hi:[1,0,1]
	v_cvt_pk_f32_fp8_sdwa v[176:177], v250 src0_sel:WORD_1
	v_cvt_pk_f32_fp8_e32 v[184:185], v186
	v_cvt_pk_f32_fp8_sdwa v[186:187], v186 src0_sel:WORD_1
	v_pk_fma_f32 v[174:175], v[174:175], v[94:95], 0 op_sel_hi:[1,0,0]
	v_cvt_pk_f32_fp8_e32 v[200:201], v202
	v_cvt_pk_f32_fp8_sdwa v[202:203], v202 src0_sel:WORD_1
	v_cvt_pk_f32_fp8_e32 v[216:217], v218
	v_cvt_pk_f32_fp8_sdwa v[218:219], v218 src0_sel:WORD_1
	v_cvt_pk_f32_fp8_e32 v[232:233], v234
	v_cvt_pk_f32_fp8_sdwa v[234:235], v234 src0_sel:WORD_1
	v_pk_fma_f32 v[190:191], v[190:191], v[94:95], 0 op_sel_hi:[1,0,0]
	v_pk_fma_f32 v[188:189], v[188:189], v[94:95], 0 op_sel_hi:[1,0,0]
	v_pk_fma_f32 v[206:207], v[206:207], v[94:95], 0 op_sel_hi:[1,0,0]
	v_pk_fma_f32 v[204:205], v[204:205], v[94:95], 0 op_sel_hi:[1,0,0]
	v_pk_fma_f32 v[222:223], v[222:223], v[94:95], 0 op_sel_hi:[1,0,0]
	v_pk_fma_f32 v[220:221], v[220:221], v[94:95], 0 op_sel_hi:[1,0,0]
	v_pk_fma_f32 v[238:239], v[238:239], v[94:95], 0 op_sel_hi:[1,0,0]
	v_pk_fma_f32 v[236:237], v[236:237], v[94:95], 0 op_sel_hi:[1,0,0]
	v_pk_fma_f32 v[146:147], v[146:147], v[94:95], 0 op_sel_hi:[1,0,0]
	v_pk_fma_f32 v[144:145], v[144:145], v[94:95], 0 op_sel_hi:[1,0,0]
	v_pk_fma_f32 v[174:175], v[178:179], v[92:93], v[174:175] op_sel_hi:[1,0,1]
	s_waitcnt vmcnt(2)
; #define GAS __attribute__((address_space(1)))
; __global__ void __launch_bounds__(NTHR, 2) mk_fwd(Args args) {
;     ...
;             for (int q = 0; q < 8; ++q) { const int c = 4 * lane + 256 * q; f32x4 f = (f32x4){0.f, 0.f, 0.f, 0.f};
; #pragma unroll
;                 for (int k = 0; k < 4; ++k) { const unsigned yv = *(const GAS unsigned*)(YS + (size_t)sl[k] * D + c); const f32x2n lo2 = __builtin_amdgcn_cvt_pk_f32_fp8(yv, false), hi2 = __builtin_amdgcn_cvt_pk_f32_fp8(yv, true); f += (gt[k] * (1.0f / pg8::YS_SCALE)) * (f32x4){lo2.x, lo2.y, hi2.x, hi2.y}; }
;                 { const v2u hw = *(const GAS v2u*)(H + (size_t)m * D + c); v[q] = ALPHA * (f32x4){bflo(hw.x), bfhi(hw.x), bflo(hw.y), bfhi(hw.y)} + f; } s += (v[q].x + v[q].y) + (v[q].z + v[q].w); }
	v_cvt_pk_f32_fp8_e32 v[178:179], v251
	v_cvt_pk_f32_fp8_sdwa v[250:251], v251 src0_sel:WORD_1
	v_pk_fma_f32 v[188:189], v[192:193], v[92:93], v[188:189] op_sel_hi:[1,0,1]
	v_pk_fma_f32 v[190:191], v[194:195], v[92:93], v[190:191] op_sel_hi:[1,0,1]
	v_pk_fma_f32 v[192:193], v[208:209], v[92:93], v[204:205] op_sel_hi:[1,0,1]
	v_pk_fma_f32 v[194:195], v[210:211], v[92:93], v[206:207] op_sel_hi:[1,0,1]
	v_pk_fma_f32 v[204:205], v[224:225], v[92:93], v[220:221] op_sel_hi:[1,0,1]
	v_pk_fma_f32 v[206:207], v[226:227], v[92:93], v[222:223] op_sel_hi:[1,0,1]
	v_pk_fma_f32 v[208:209], v[240:241], v[92:93], v[236:237] op_sel_hi:[1,0,1]
	v_pk_fma_f32 v[210:211], v[242:243], v[92:93], v[238:239] op_sel_hi:[1,0,1]
	v_pk_fma_f32 v[144:145], v[160:161], v[92:93], v[144:145] op_sel_hi:[1,0,1]
	v_pk_fma_f32 v[146:147], v[248:249], v[92:93], v[146:147] op_sel_hi:[1,0,1]
	v_pk_fma_f32 v[152:153], v[152:153], v[68:69], v[66:67] op_sel_hi:[1,0,1]
	v_pk_fma_f32 v[142:143], v[154:155], v[68:69], v[142:143] op_sel_hi:[1,0,1]
	v_pk_fma_f32 v[154:155], v[166:167], v[64:65], v[158:159] op_sel_hi:[1,0,1]
	v_pk_fma_f32 v[156:157], v[164:165], v[64:65], v[156:157] op_sel_hi:[1,0,1]
	v_pk_fma_f32 v[158:159], v[182:183], v[64:65], v[174:175] op_sel_hi:[1,0,1]
	v_pk_fma_f32 v[160:161], v[180:181], v[64:65], v[172:173] op_sel_hi:[1,0,1]
	v_pk_fma_f32 v[164:165], v[198:199], v[64:65], v[190:191] op_sel_hi:[1,0,1]
	v_pk_fma_f32 v[166:167], v[196:197], v[64:65], v[188:189] op_sel_hi:[1,0,1]
	v_pk_fma_f32 v[172:173], v[214:215], v[64:65], v[194:195] op_sel_hi:[1,0,1]
	v_pk_fma_f32 v[174:175], v[212:213], v[64:65], v[192:193] op_sel_hi:[1,0,1]
	v_pk_fma_f32 v[180:181], v[230:231], v[64:65], v[206:207] op_sel_hi:[1,0,1]
	v_pk_fma_f32 v[182:183], v[228:229], v[64:65], v[204:205] op_sel_hi:[1,0,1]
	v_pk_fma_f32 v[188:189], v[246:247], v[64:65], v[210:211] op_sel_hi:[1,0,1]
	v_pk_fma_f32 v[190:191], v[244:245], v[64:65], v[208:209] op_sel_hi:[1,0,1]
	v_pk_fma_f32 v[146:147], v[176:177], v[64:65], v[146:147] op_sel_hi:[1,0,1]
	v_pk_fma_f32 v[144:145], v[162:163], v[64:65], v[144:145] op_sel_hi:[1,0,1]
	s_waitcnt vmcnt(1)
	v_mov_b64_e32 v[66:67], v[98:99]
	v_mov_b64_e32 v[64:65], v[96:97]
	v_pk_fma_f32 v[96:97], v[126:127], s[12:13], v[142:143] op_sel_hi:[1,0,1]
	v_pk_fma_f32 v[98:99], v[124:125], s[12:13], v[152:153] op_sel_hi:[1,0,1]
	v_pk_fma_f32 v[124:125], v[168:169], v[68:69], v[156:157] op_sel_hi:[1,0,1]
	v_pk_fma_f32 v[126:127], v[170:171], v[68:69], v[154:155] op_sel_hi:[1,0,1]
	v_lshlrev_b32_e32 v130, 16, v104
	v_and_b32_e32 v131, 0xffff0000, v104
	v_lshlrev_b32_e32 v104, 16, v105
	v_and_b32_e32 v105, 0xffff0000, v105
	v_pk_fma_f32 v[142:143], v[184:185], v[68:69], v[160:161] op_sel_hi:[1,0,1]
	v_pk_fma_f32 v[152:153], v[186:187], v[68:69], v[158:159] op_sel_hi:[1,0,1]
	v_pk_fma_f32 v[126:127], v[70:71], s[12:13], v[126:127] op_sel_hi:[1,0,1]
	v_pk_fma_f32 v[124:125], v[128:129], s[12:13], v[124:125] op_sel_hi:[1,0,1]
	v_lshlrev_b32_e32 v140, 16, v116
	v_and_b32_e32 v141, 0xffff0000, v116
	v_lshlrev_b32_e32 v116, 16, v117
	v_and_b32_e32 v117, 0xffff0000, v117
	v_pk_fma_f32 v[154:155], v[200:201], v[68:69], v[166:167] op_sel_hi:[1,0,1]
	v_pk_fma_f32 v[156:157], v[202:203], v[68:69], v[164:165] op_sel_hi:[1,0,1]
	v_pk_fma_f32 v[158:159], v[216:217], v[68:69], v[174:175] op_sel_hi:[1,0,1]
	v_pk_fma_f32 v[160:161], v[218:219], v[68:69], v[172:173] op_sel_hi:[1,0,1]
	v_pk_fma_f32 v[162:163], v[232:233], v[68:69], v[182:183] op_sel_hi:[1,0,1]
	v_pk_fma_f32 v[164:165], v[234:235], v[68:69], v[180:181] op_sel_hi:[1,0,1]
	v_pk_fma_f32 v[150:151], v[150:151], v[68:69], v[190:191] op_sel_hi:[1,0,1]
	v_pk_fma_f32 v[148:149], v[148:149], v[68:69], v[188:189] op_sel_hi:[1,0,1]
	v_pk_fma_f32 v[144:145], v[178:179], v[68:69], v[144:145] op_sel_hi:[1,0,1]
	v_pk_fma_f32 v[68:69], v[250:251], v[68:69], v[146:147] op_sel_hi:[1,0,1]
	v_mov_b32_e32 v128, v98
	v_mov_b32_e32 v146, v99
	v_mov_b32_e32 v166, v96
	v_mov_b32_e32 v168, v97
	v_pk_fma_f32 v[104:105], v[104:105], s[12:13], v[152:153] op_sel_hi:[1,0,1]
	v_pk_fma_f32 v[130:131], v[130:131], s[12:13], v[142:143] op_sel_hi:[1,0,1]
	v_mov_b32_e32 v129, v124
	v_mov_b32_e32 v147, v125
	v_mov_b32_e32 v167, v126
	v_mov_b32_e32 v169, v127
	v_pk_fma_f32 v[116:117], v[116:117], s[12:13], v[68:69] op_sel_hi:[1,0,1]
	s_waitcnt vmcnt(0)
; #define GAS __attribute__((address_space(1)))
; __global__ void __launch_bounds__(NTHR, 2) mk_fwd(Args args) {
;     ...
;             f32x4 v[8]; float s = 0.f;
; #pragma unroll
;             for (int q = 0; q < 8; ++q) { const int c = 4 * lane + 256 * q; f32x4 f = (f32x4){0.f, 0.f, 0.f, 0.f};
; #pragma unroll
;                 for (int k = 0; k < 4; ++k) { const unsigned yv = *(const GAS unsigned*)(YS + (size_t)sl[k] * D + c); const f32x2n lo2 = __builtin_amdgcn_cvt_pk_f32_fp8(yv, false), hi2 = __builtin_amdgcn_cvt_pk_f32_fp8(yv, true); f += (gt[k] * (1.0f / pg8::YS_SCALE)) * (f32x4){lo2.x, lo2.y, hi2.x, hi2.y}; }
;                 { const v2u hw = *(const GAS v2u*)(H + (size_t)m * D + c); v[q] = ALPHA * (f32x4){bflo(hw.x), bfhi(hw.x), bflo(hw.y), bfhi(hw.y)} + f; } s += (v[q].x + v[q].y) + (v[q].z + v[q].w); }
;             const float mean = wave_sum_dpp(s) * (1.0f / D); float s2 = 0.f;
; #pragma unroll
;             for (int q = 0; q < 8; ++q) { v[q] = v[q] - mean; s2 += (v[q].x * v[q].x + v[q].y * v[q].y) + (v[q].z * v[q].z + v[q].w * v[q].w); }
	v_mov_b64_e32 v[70:71], v[102:103]
	v_mov_b64_e32 v[68:69], v[100:101]
	v_pk_mov_b32 v[100:101], v[130:131], v[104:105] op_sel:[1,0]
	v_mov_b32_e32 v102, v130
	v_mov_b32_e32 v103, v105
	v_pk_add_f32 v[128:129], v[128:129], v[146:147]
	v_pk_add_f32 v[146:147], v[166:167], v[168:169]
	v_lshlrev_b32_e32 v132, 16, v108
	v_and_b32_e32 v133, 0xffff0000, v108
	v_lshlrev_b32_e32 v108, 16, v109
	v_and_b32_e32 v109, 0xffff0000, v109
	v_lshlrev_b32_e32 v134, 16, v110
	v_and_b32_e32 v135, 0xffff0000, v110
	v_lshlrev_b32_e32 v110, 16, v111
	v_and_b32_e32 v111, 0xffff0000, v111
	v_pk_add_f32 v[100:101], v[100:101], v[102:103]
	v_pk_add_f32 v[128:129], v[128:129], v[146:147]
	v_lshlrev_b32_e32 v136, 16, v112
	v_and_b32_e32 v137, 0xffff0000, v112
	v_lshlrev_b32_e32 v112, 16, v113
	v_and_b32_e32 v113, 0xffff0000, v113
	v_lshlrev_b32_e32 v138, 16, v114
	v_and_b32_e32 v139, 0xffff0000, v114
	v_lshlrev_b32_e32 v114, 16, v115
	v_and_b32_e32 v115, 0xffff0000, v115
	v_pk_fma_f32 v[108:109], v[108:109], s[12:13], v[156:157] op_sel_hi:[1,0,1]
	v_pk_fma_f32 v[132:133], v[132:133], s[12:13], v[154:155] op_sel_hi:[1,0,1]
	v_pk_fma_f32 v[110:111], v[110:111], s[12:13], v[160:161] op_sel_hi:[1,0,1]
	v_pk_fma_f32 v[134:135], v[134:135], s[12:13], v[158:159] op_sel_hi:[1,0,1]
	v_pk_add_f32 v[100:101], v[100:101], v[100:101] op_sel:[0,1] op_sel_hi:[1,0]
	v_add_f32_e32 v92, 0, v128
	v_pk_fma_f32 v[112:113], v[112:113], s[12:13], v[164:165] op_sel_hi:[1,0,1]
	v_pk_fma_f32 v[136:137], v[136:137], s[12:13], v[162:163] op_sel_hi:[1,0,1]
	v_pk_fma_f32 v[114:115], v[114:115], s[12:13], v[148:149] op_sel_hi:[1,0,1]
	v_pk_fma_f32 v[140:141], v[140:141], s[12:13], v[144:145] op_sel_hi:[1,0,1]
	v_add_f32_e32 v142, v132, v133
	v_add_f32_e32 v144, v108, v109
	v_mov_b32_e32 v149, v134
	v_mov_b32_e32 v143, v110
	v_mov_b32_e32 v145, v111
	v_mov_b32_e32 v101, v135
	v_add_f32_e32 v148, v92, v129
	v_pk_fma_f32 v[138:139], v[138:139], s[12:13], v[150:151] op_sel_hi:[1,0,1]
	v_pk_mov_b32 v[150:151], v[136:137], v[112:113] op_sel:[1,0]
	v_mov_b32_e32 v152, v136
	v_mov_b32_e32 v153, v113
	v_pk_add_f32 v[102:103], v[142:143], v[144:145]
	v_pk_add_f32 v[100:101], v[148:149], v[100:101]
	v_pk_add_f32 v[142:143], v[150:151], v[152:153]
	v_pk_add_f32 v[100:101], v[100:101], v[102:103]
	v_pk_add_f32 v[142:143], v[142:143], v[142:143] op_sel:[0,1] op_sel_hi:[1,0]
	v_pk_add_f32 v[100:101], v[100:101], v[100:101] op_sel:[0,1] op_sel_hi:[1,0]
	v_add_f32_e32 v154, v138, v139
	v_add_f32_e32 v156, v114, v115
	v_mov_b32_e32 v155, v116
	v_mov_b32_e32 v157, v117
	v_mov_b32_e32 v143, v141
	v_mov_b32_e32 v101, v140
	v_pk_add_f32 v[144:145], v[154:155], v[156:157]
	v_pk_add_f32 v[100:101], v[100:101], v[142:143]
	s_nop 0
	v_pk_add_f32 v[100:101], v[100:101], v[144:145]
	s_nop 0
	v_add_f32_e32 v92, v100, v101
	s_nop 1
	v_add_f32_dpp v92, v92, v92 quad_perm:[1,0,3,2] row_mask:0xf bank_mask:0xf bound_ctrl:1
	s_nop 1
	v_add_f32_dpp v92, v92, v92 quad_perm:[2,3,0,1] row_mask:0xf bank_mask:0xf bound_ctrl:1
	s_nop 1
	v_add_f32_dpp v92, v92, v92 row_half_mirror row_mask:0xf bank_mask:0xf bound_ctrl:1
	s_nop 1
	v_add_f32_dpp v92, v92, v92 row_mirror row_mask:0xf bank_mask:0xf bound_ctrl:1
	s_nop 1
	v_mov_b32_dpp v120, v92 row_bcast:15 row_mask:0xa bank_mask:0xf
	v_add_f32_e32 v92, v92, v120
	s_nop 1
	v_mov_b32_dpp v121, v92 row_bcast:31 row_mask:0xc bank_mask:0xf
	v_add_f32_e32 v92, v92, v121
	s_nop 0
	v_readlane_b32 s2, v92, 63
	s_nop 1
	v_fmac_f32_e32 v97, s2, v118
	v_fmac_f32_e32 v99, s2, v118
	v_fmac_f32_e32 v127, s2, v118
	v_fmac_f32_e32 v125, s2, v118
	v_fma_f32 v96, s2, v118, v96
	v_fma_f32 v98, s2, v118, v98
	v_fma_f32 v126, s2, v118, v126
	v_fma_f32 v124, s2, v118, v124
	v_fmac_f32_e32 v105, s2, v118
	v_fmac_f32_e32 v131, s2, v118
	v_mul_f32_e32 v92, v99, v99
	v_mul_f32_e32 v94, v97, v97
	v_mul_f32_e32 v100, v125, v125
	v_mul_f32_e32 v101, v127, v127
	v_fma_f32 v104, s2, v118, v104
	v_fma_f32 v130, s2, v118, v130
	v_fmac_f32_e32 v109, s2, v118
	v_fmac_f32_e32 v133, s2, v118
	v_mul_f32_e32 v102, v131, v131
	v_mul_f32_e32 v103, v105, v105
	v_fmac_f32_e32 v92, v98, v98
	v_fmac_f32_e32 v94, v96, v96
	v_fmac_f32_e32 v100, v124, v124
	v_fmac_f32_e32 v101, v126, v126
	v_fma_f32 v108, s2, v118, v108
	v_fma_f32 v132, s2, v118, v132
	v_fmac_f32_e32 v111, s2, v118
	v_fmac_f32_e32 v135, s2, v118
	v_mul_f32_e32 v120, v133, v133
	v_mul_f32_e32 v121, v109, v109
	v_fmac_f32_e32 v102, v130, v130
	v_fmac_f32_e32 v103, v104, v104
	v_add_f32_e32 v92, v92, v94
	v_add_f32_e32 v94, v100, v101
	v_fma_f32 v110, s2, v118, v110
	v_fma_f32 v134, s2, v118, v134
	v_fmac_f32_e32 v113, s2, v118
	v_fmac_f32_e32 v137, s2, v118
	v_mul_f32_e32 v128, v135, v135
	v_mul_f32_e32 v129, v111, v111
	v_fmac_f32_e32 v120, v132, v132
	v_fmac_f32_e32 v121, v108, v108
	v_add_f32_e32 v100, v102, v103
	v_add_f32_e32 v92, v92, v94
	v_fma_f32 v112, s2, v118, v112
	v_fma_f32 v136, s2, v118, v136
	v_fmac_f32_e32 v115, s2, v118
	v_fmac_f32_e32 v139, s2, v118
	v_mul_f32_e32 v142, v137, v137
	v_mul_f32_e32 v143, v113, v113
	v_fmac_f32_e32 v128, v134, v134
	v_fmac_f32_e32 v129, v110, v110
	v_add_f32_e32 v101, v120, v121
	v_add_f32_e32 v92, v92, v100
; #define GAS __attribute__((address_space(1)))
; #define LAS __attribute__((address_space(3)))
; __global__ void __launch_bounds__(NTHR, 2) mk_fwd(Args args) {
;     ...
;             const float mean = wave_sum_dpp(s) * (1.0f / D); float s2 = 0.f;
; #pragma unroll
;             for (int q = 0; q < 8; ++q) { v[q] = v[q] - mean; s2 += (v[q].x * v[q].x + v[q].y * v[q].y) + (v[q].z * v[q].z + v[q].w * v[q].w); }
;             const float rstd = 1.0f / sqrtf(wave_sum_dpp(s2) * (1.0f / D) + LN_EPS);
; #pragma unroll
;             for (int q = 0; q < 8; ++q) { const int c = 4 * lane + 256 * q; *(GAS f32x4*)(out + (size_t)m * D + c) = v[q] * rstd * *(const LAS f32x4*)(s_lnw + c) + *(const LAS f32x4*)(s_lnb + c); }
	v_fma_f32 v114, s2, v118, v114
	v_fma_f32 v138, s2, v118, v138
	v_fmac_f32_e32 v117, s2, v118
	v_fmac_f32_e32 v141, s2, v118
	v_mul_f32_e32 v144, v139, v139
	v_mul_f32_e32 v145, v115, v115
	v_fmac_f32_e32 v142, v136, v136
	v_fmac_f32_e32 v143, v112, v112
	v_add_f32_e32 v102, v128, v129
	v_add_f32_e32 v92, v92, v101
	v_fma_f32 v116, s2, v118, v116
	v_fma_f32 v140, s2, v118, v140
	v_mul_f32_e32 v146, v141, v141
	v_mul_f32_e32 v147, v117, v117
	v_fmac_f32_e32 v144, v138, v138
	v_fmac_f32_e32 v145, v114, v114
	v_add_f32_e32 v103, v142, v143
	v_add_f32_e32 v92, v92, v102
	v_fmac_f32_e32 v146, v140, v140
	v_fmac_f32_e32 v147, v116, v116
	v_add_f32_e32 v120, v144, v145
	v_add_f32_e32 v92, v92, v103
	v_add_f32_e32 v121, v146, v147
	v_add_f32_e32 v92, v92, v120
	v_add_f32_e32 v92, v92, v121
	s_nop 1
	v_add_f32_dpp v92, v92, v92 quad_perm:[1,0,3,2] row_mask:0xf bank_mask:0xf bound_ctrl:1
	s_nop 1
	v_add_f32_dpp v92, v92, v92 quad_perm:[2,3,0,1] row_mask:0xf bank_mask:0xf bound_ctrl:1
	s_nop 1
	v_add_f32_dpp v92, v92, v92 row_half_mirror row_mask:0xf bank_mask:0xf bound_ctrl:1
	s_nop 1
	v_add_f32_dpp v92, v92, v92 row_mirror row_mask:0xf bank_mask:0xf bound_ctrl:1
	s_nop 1
	v_mov_b32_dpp v122, v92 row_bcast:15 row_mask:0xa bank_mask:0xf
	v_add_f32_e32 v92, v92, v122
	s_nop 1
	v_mov_b32_dpp v123, v92 row_bcast:31 row_mask:0xc bank_mask:0xf
	v_add_f32_e32 v92, v92, v123
	s_nop 0
	v_readlane_b32 s2, v92, 63
	s_nop 1
	v_fma_f32 v92, s2, v119, v93
	v_mul_f32_e32 v94, 0x4f800000, v92
	v_cmp_gt_f32_e32 vcc, s13, v92
	s_nop 1
	v_cndmask_b32_e32 v92, v92, v94, vcc
	v_sqrt_f32_e32 v94, v92
	s_nop 0
	v_add_u32_e32 v100, -1, v94
	v_add_u32_e32 v101, 1, v94
	v_fma_f32 v102, -v100, v94, v92
	v_fma_f32 v103, -v101, v94, v92
	v_cmp_ge_f32_e64 s[2:3], 0, v102
	s_nop 1
	v_cndmask_b32_e64 v94, v94, v100, s[2:3]
	v_cmp_lt_f32_e64 s[2:3], 0, v103
	s_nop 1
	v_cndmask_b32_e64 v94, v94, v101, s[2:3]
	v_mul_f32_e32 v100, 0x37800000, v94
	v_cndmask_b32_e32 v94, v94, v100, vcc
	v_cmp_class_f32_e32 vcc, v92, v95
	s_nop 1
	v_cndmask_b32_e32 v92, v94, v92, vcc
	v_div_scale_f32 v94, s[2:3], v92, v92, 1.0
	v_rcp_f32_e32 v101, v94
	v_div_scale_f32 v100, vcc, 1.0, v92, 1.0
	v_fma_f32 v102, -v94, v101, 1.0
	v_fmac_f32_e32 v101, v102, v101
	v_mul_f32_e32 v102, v100, v101
	v_fma_f32 v103, -v94, v102, v100
	v_fmac_f32_e32 v102, v103, v101
	v_fma_f32 v94, -v94, v102, v100
	v_div_fmas_f32 v94, v94, v101, v102
	v_div_fixup_f32 v92, v94, v92, 1.0
	v_pk_mul_f32 v[100:101], v[92:93], v[98:99] op_sel_hi:[0,1]
	v_pk_mul_f32 v[96:97], v[92:93], v[96:97] op_sel_hi:[0,1]
	v_pk_mul_f32 v[120:121], v[92:93], v[124:125] op_sel_hi:[0,1]
	v_pk_mul_f32 v[102:103], v[92:93], v[126:127] op_sel_hi:[0,1]
	v_pk_mul_f32 v[122:123], v[92:93], v[130:131] op_sel_hi:[0,1]
	v_pk_mul_f32 v[104:105], v[92:93], v[104:105] op_sel_hi:[0,1]
	v_pk_mul_f32 v[124:125], v[92:93], v[132:133] op_sel_hi:[0,1]
	v_pk_mul_f32 v[126:127], v[92:93], v[108:109] op_sel_hi:[0,1]
	v_pk_mul_f32 v[128:129], v[92:93], v[134:135] op_sel_hi:[0,1]
	v_pk_mul_f32 v[130:131], v[92:93], v[110:111] op_sel_hi:[0,1]
	v_pk_mul_f32 v[132:133], v[92:93], v[136:137] op_sel_hi:[0,1]
	v_pk_mul_f32 v[134:135], v[92:93], v[112:113] op_sel_hi:[0,1]
	v_pk_mul_f32 v[136:137], v[92:93], v[138:139] op_sel_hi:[0,1]
	v_pk_mul_f32 v[138:139], v[92:93], v[114:115] op_sel_hi:[0,1]
	v_pk_mul_f32 v[140:141], v[92:93], v[140:141] op_sel_hi:[0,1]
	v_pk_mul_f32 v[116:117], v[92:93], v[116:117] op_sel_hi:[0,1]
	s_waitcnt lgkmcnt(13)
	v_pk_fma_f32 v[98:99], v[96:97], v[2:3], v[10:11]
	v_pk_fma_f32 v[96:97], v[100:101], v[0:1], v[8:9]
	s_waitcnt lgkmcnt(12)
	v_pk_fma_f32 v[102:103], v[102:103], v[6:7], v[14:15]
	v_pk_fma_f32 v[100:101], v[120:121], v[4:5], v[12:13]
	s_waitcnt lgkmcnt(9)
	v_pk_fma_f32 v[110:111], v[104:105], v[18:19], v[26:27]
	v_pk_fma_f32 v[108:109], v[122:123], v[16:17], v[24:25]
	s_waitcnt lgkmcnt(8)
	v_pk_fma_f32 v[114:115], v[126:127], v[22:23], v[30:31]
	v_pk_fma_f32 v[112:113], v[124:125], v[20:21], v[28:29]
	s_waitcnt lgkmcnt(5)
	v_pk_fma_f32 v[122:123], v[130:131], v[34:35], v[42:43]
	v_pk_fma_f32 v[120:121], v[128:129], v[32:33], v[40:41]
	s_waitcnt lgkmcnt(4)
	v_pk_fma_f32 v[126:127], v[134:135], v[38:39], v[46:47]
	v_pk_fma_f32 v[124:125], v[132:133], v[36:37], v[44:45]
	s_waitcnt lgkmcnt(1)
	v_pk_fma_f32 v[130:131], v[138:139], v[50:51], v[58:59]
	v_pk_fma_f32 v[128:129], v[136:137], v[48:49], v[56:57]
	s_waitcnt lgkmcnt(0)
	v_pk_fma_f32 v[134:135], v[116:117], v[54:55], v[62:63]
	v_pk_fma_f32 v[132:133], v[140:141], v[52:53], v[60:61]
	global_store_dwordx4 v[106:107], v[96:99], off offset:-3072 nt
	global_store_dwordx4 v[106:107], v[100:103], off offset:-2048 nt
	global_store_dwordx4 v[106:107], v[108:111], off offset:-1024 nt
	global_store_dwordx4 v[88:89], v[112:115], off offset:-4096 nt
	global_store_dwordx4 v[88:89], v[120:123], off offset:-3072 nt
	global_store_dwordx4 v[88:89], v[124:127], off offset:-2048 nt
	global_store_dwordx4 v[88:89], v[128:131], off offset:-1024 nt
	global_store_dwordx4 v[88:89], v[132:135], off nt
	v_lshl_add_u64 v[88:89], v[88:89], 0, s[6:7]
	s_mov_b64 vcc, s[0:1]
	s_cbranch_vccnz .LBB0_1219
